# table bytes enter the f32 FMAs as raw integers (an integer below 2^24 read as f32 is that integer times 2^-149 exactly; f32 denormals are on in the baseline mode) with the scale carried by h / the coe
# speedup vs baseline: 1.0055x; 1.0055x over previous
.Lgba_1444:
	s_or_b64 exec, exec, s[2:3]
	s_waitcnt lgkmcnt(0)
	s_barrier
	s_mov_b64 exec, -1
	v_and_b32_e32 v1, 63, v0
	v_readfirstlane_b32 s16, v0
	s_load_dwordx2 s[12:13], s[0:1], 0xc0
	s_lshr_b32 s16, s16, 6
	s_and_b32 s18, s33, 7
	s_lshr_b32 s19, s33, 3
	s_lshl_b32 s19, s19, 8
	s_lshl_b32 s16, s16, 5
	s_add_i32 s16, s16, s19
	s_add_i32 s17, s16, 32
	s_add_i32 s24, s17, -1
	s_lshl_b32 s19, s18, 9
	v_lshl_add_u32 v162, v1, 3, s19
	v_mov_b32_e32 v163, 0
	s_mov_b32 s31, 0
	v_and_b32_e32 v4, 8, v1
	v_cmp_eq_u32_e64 s[8:9], 0, v4
	v_and_b32_e32 v4, 4, v1
	v_cmp_eq_u32_e64 s[10:11], 0, v4
	v_and_b32_e32 v4, 2, v1
	v_cmp_eq_u32_e64 s[14:15], 0, v4
	s_mov_b32 s2, 0x55555555
	s_mov_b32 s3, 0x55555555
	s_mov_b32 s6, 0xff
	s_mov_b32 s7, 0xff00
	s_mov_b32 s42, 0xff0000
	s_load_dwordx2 s[4:5], s[0:1], 0x88
	s_waitcnt lgkmcnt(0)
	v_lshl_add_u64 v[160:161], v[162:163], 2, s[4:5]
	global_load_dwordx4 v[100:103], v[160:161], off
	global_load_dwordx4 v[104:107], v[160:161], off offset:16
	s_lshl_b32 s19, s18, 20
	s_add_u32 s22, s12, 0x25c00000
	s_addc_u32 s23, s13, 0
	s_add_u32 s22, s22, s19
	s_addc_u32 s23, s23, 0
	s_add_u32 s26, s12, 0xfc00000
	s_addc_u32 s27, s13, 0
	s_add_u32 s20, s12, 0x100000
	s_addc_u32 s21, s13, 0
	v_lshl_add_u64 v[172:173], v[162:163], 1, s[20:21]
	s_add_u32 s20, s12, 0x4da00000
	s_addc_u32 s21, s13, 0
	v_mov_b32_e32 v4, v1
	v_mov_b32_e32 v5, 0
	v_lshl_add_u64 v[174:175], v[4:5], 2, s[20:21]
	s_lshl_b32 s19, s18, 22
	s_add_u32 s20, s12, 0x23c00000
	s_addc_u32 s21, s13, 0
	s_add_u32 s20, s20, s19
	s_addc_u32 s21, s21, 0
	v_lshl_add_u64 v[176:177], v[4:5], 1, s[20:21]
	s_lshl_b32 s30, s16, 13
	v_lshl_add_u64 v[160:161], v[172:173], 0, s[30:31]
	global_load_dwordx4 v[116:119], v[160:161], off
	s_lshl_b32 s30, s16, 9
	v_lshl_add_u64 v[160:161], v[174:175], 0, s[30:31]
	global_load_dword v122, v[160:161], off
	global_load_dword v123, v[160:161], off offset:256
	s_waitcnt vmcnt(0)
	s_add_u32 s40, s12, 0x4da00000
	s_addc_u32 s41, s13, 0
	s_lshl_b32 s30, s16, 9
	s_add_u32 s36, s40, s30
	s_addc_u32 s37, s41, 0
	s_load_dwordx16 s[68:83], s[36:37], 0x0 glc
	s_load_dwordx16 s[84:99], s[36:37], 0x40 glc
	s_waitcnt lgkmcnt(0)
	s_lshl_b32 s30, s68, 12
	s_add_u32 s28, s26, s30
	s_addc_u32 s29, s27, 0
	global_load_dwordx2 v[24:25], v162, s[28:29]
	s_lshl_b32 s30, s69, 12
	s_add_u32 s28, s26, s30
	s_addc_u32 s29, s27, 0
	global_load_dwordx2 v[26:27], v162, s[28:29]
	s_lshl_b32 s30, s70, 12
	s_add_u32 s28, s26, s30
	s_addc_u32 s29, s27, 0
	global_load_dwordx2 v[28:29], v162, s[28:29]
	s_lshl_b32 s30, s71, 12
	s_add_u32 s28, s26, s30
	s_addc_u32 s29, s27, 0
	global_load_dwordx2 v[30:31], v162, s[28:29]
	s_lshl_b32 s30, s72, 12
	s_add_u32 s28, s26, s30
	s_addc_u32 s29, s27, 0
	global_load_dwordx2 v[32:33], v162, s[28:29]
	s_lshl_b32 s30, s73, 12
	s_add_u32 s28, s26, s30
	s_addc_u32 s29, s27, 0
	global_load_dwordx2 v[34:35], v162, s[28:29]
	s_lshl_b32 s30, s74, 12
	s_add_u32 s28, s26, s30
	s_addc_u32 s29, s27, 0
	global_load_dwordx2 v[36:37], v162, s[28:29]
	s_lshl_b32 s30, s75, 12
	s_add_u32 s28, s26, s30
	s_addc_u32 s29, s27, 0
	global_load_dwordx2 v[38:39], v162, s[28:29]
	s_lshl_b32 s30, s76, 12
	s_add_u32 s28, s26, s30
	s_addc_u32 s29, s27, 0
	global_load_dwordx2 v[40:41], v162, s[28:29]
	s_lshl_b32 s30, s77, 12
	s_add_u32 s28, s26, s30
	s_addc_u32 s29, s27, 0
	global_load_dwordx2 v[42:43], v162, s[28:29]
	s_lshl_b32 s30, s78, 12
	s_add_u32 s28, s26, s30
	s_addc_u32 s29, s27, 0
	global_load_dwordx2 v[44:45], v162, s[28:29]
	s_lshl_b32 s30, s79, 12
	s_add_u32 s28, s26, s30
	s_addc_u32 s29, s27, 0
	global_load_dwordx2 v[46:47], v162, s[28:29]
	s_lshl_b32 s30, s80, 12
	s_add_u32 s28, s26, s30
	s_addc_u32 s29, s27, 0
	global_load_dwordx2 v[48:49], v162, s[28:29]
	s_lshl_b32 s30, s81, 12
	s_add_u32 s28, s26, s30
	s_addc_u32 s29, s27, 0
	global_load_dwordx2 v[50:51], v162, s[28:29]
	s_lshl_b32 s30, s82, 12
	s_add_u32 s28, s26, s30
	s_addc_u32 s29, s27, 0
	global_load_dwordx2 v[52:53], v162, s[28:29]
	s_lshl_b32 s30, s83, 12
	s_add_u32 s28, s26, s30
	s_addc_u32 s29, s27, 0
	global_load_dwordx2 v[54:55], v162, s[28:29]
	s_lshl_b32 s30, s84, 12
	s_add_u32 s28, s26, s30
	s_addc_u32 s29, s27, 0
	global_load_dwordx2 v[56:57], v162, s[28:29]
	s_lshl_b32 s30, s85, 12
	s_add_u32 s28, s26, s30
	s_addc_u32 s29, s27, 0
	global_load_dwordx2 v[58:59], v162, s[28:29]
	s_lshl_b32 s30, s86, 12
	s_add_u32 s28, s26, s30
	s_addc_u32 s29, s27, 0
	global_load_dwordx2 v[60:61], v162, s[28:29]
	s_lshl_b32 s30, s87, 12
	s_add_u32 s28, s26, s30
	s_addc_u32 s29, s27, 0
	global_load_dwordx2 v[62:63], v162, s[28:29]
	s_lshl_b32 s30, s88, 12
	s_add_u32 s28, s26, s30
	s_addc_u32 s29, s27, 0
	global_load_dwordx2 v[64:65], v162, s[28:29]
	s_lshl_b32 s30, s89, 12
	s_add_u32 s28, s26, s30
	s_addc_u32 s29, s27, 0
	global_load_dwordx2 v[66:67], v162, s[28:29]
	s_lshl_b32 s30, s90, 12
	s_add_u32 s28, s26, s30
	s_addc_u32 s29, s27, 0
	global_load_dwordx2 v[68:69], v162, s[28:29]
	s_lshl_b32 s30, s91, 12
	s_add_u32 s28, s26, s30
	s_addc_u32 s29, s27, 0
	global_load_dwordx2 v[70:71], v162, s[28:29]
	s_lshl_b32 s30, s92, 12
	s_add_u32 s28, s26, s30
	s_addc_u32 s29, s27, 0
	global_load_dwordx2 v[72:73], v162, s[28:29]
	s_lshl_b32 s30, s93, 12
	s_add_u32 s28, s26, s30
	s_addc_u32 s29, s27, 0
	global_load_dwordx2 v[74:75], v162, s[28:29]
	s_lshl_b32 s30, s94, 12
	s_add_u32 s28, s26, s30
	s_addc_u32 s29, s27, 0
	global_load_dwordx2 v[76:77], v162, s[28:29]
	s_lshl_b32 s30, s95, 12
	s_add_u32 s28, s26, s30
	s_addc_u32 s29, s27, 0
	global_load_dwordx2 v[78:79], v162, s[28:29]
	s_lshl_b32 s30, s96, 12
	s_add_u32 s28, s26, s30
	s_addc_u32 s29, s27, 0
	global_load_dwordx2 v[80:81], v162, s[28:29]
	s_lshl_b32 s30, s97, 12
	s_add_u32 s28, s26, s30
	s_addc_u32 s29, s27, 0
	global_load_dwordx2 v[82:83], v162, s[28:29]
	s_lshl_b32 s30, s98, 12
	s_add_u32 s28, s26, s30
	s_addc_u32 s29, s27, 0
	global_load_dwordx2 v[84:85], v162, s[28:29]
	s_lshl_b32 s30, s99, 12
	s_add_u32 s28, s26, s30
	s_addc_u32 s29, s27, 0
	global_load_dwordx2 v[86:87], v162, s[28:29]
	s_load_dwordx16 s[68:83], s[36:37], 0x80 glc
.Lpa_tok:
	v_lshlrev_b32_e32 v124, 16, v116
	v_and_b32_e32 v125, 0xffff0000, v116
	v_pk_mul_f32 v[108:109], v[124:125], v[100:101]
	v_lshlrev_b32_e32 v124, 16, v117
	v_and_b32_e32 v125, 0xffff0000, v117
	v_pk_mul_f32 v[110:111], v[124:125], v[102:103]
	v_lshlrev_b32_e32 v124, 16, v118
	v_and_b32_e32 v125, 0xffff0000, v118
	v_pk_mul_f32 v[112:113], v[124:125], v[104:105]
	v_lshlrev_b32_e32 v124, 16, v119
	v_and_b32_e32 v125, 0xffff0000, v119
	v_pk_mul_f32 v[114:115], v[124:125], v[106:107]
	v_add_f32_e32 v16, v108, v109
	v_add_f32_e32 v17, v110, v111
	v_add_f32_e32 v18, v112, v113
	v_add_f32_e32 v19, v114, v115
	v_add_f32_e32 v16, v16, v17
	v_add_f32_e32 v18, v18, v19
	v_add_f32_e32 v16, v16, v18
	s_nop 1
	v_add_f32_dpp v17, v16, v16 quad_perm:[1,0,3,2] row_mask:0xf bank_mask:0xf
	s_nop 1
	v_add_f32_dpp v16, v17, v17 quad_perm:[2,3,0,1] row_mask:0xf bank_mask:0xf
	s_nop 1
	v_add_f32_dpp v17, v16, v16 row_half_mirror row_mask:0xf bank_mask:0xf
	s_nop 1
	v_add_f32_dpp v16, v17, v17 row_ror:8 row_mask:0xf bank_mask:0xf
	v_mov_b32_e32 v17, v16
	s_nop 1
	v_permlane16_swap_b32_e32 v16, v17
	v_add_f32_e32 v16, v16, v17
	v_mov_b32_e32 v17, v16
	s_nop 1
	v_permlane32_swap_b32_e32 v16, v17
	v_add_f32_e32 v16, v16, v17
	s_lshl_b32 s30, s16, 7
	s_add_u32 s28, s22, s30
	s_addc_u32 s29, s23, 0
	v_lshlrev_b32_e32 v19, 1, v1
	s_mov_b64 exec, s[2:3]
	global_store_dword v19, v16, s[28:29]
	s_mov_b64 exec, -1
	v_mul_f32_e32 v108, 0x71800000, v108
	v_mul_f32_e32 v109, 0x6d800000, v109
	v_mul_f32_e32 v110, 0x69800000, v110
	v_mul_f32_e32 v111, 0x71800000, v111
	v_mul_f32_e32 v112, 0x71800000, v112
	v_mul_f32_e32 v113, 0x6d800000, v113
	v_mul_f32_e32 v114, 0x69800000, v114
	v_mul_f32_e32 v115, 0x71800000, v115
	v_mov_b32_e32 v120, v122
	v_mov_b32_e32 v121, v123
	s_lshl_b32 s30, s16, 9
	v_lshl_add_u64 v[22:23], v[176:177], 0, s[30:31]
	s_add_i32 s18, s16, 1
	s_min_i32 s18, s18, s24
	s_lshl_b32 s30, s16, 9
	s_add_u32 s36, s40, s30
	s_addc_u32 s37, s41, 0
	s_lshl_b32 s30, s18, 9
	s_add_u32 s38, s40, s30
	s_addc_u32 s39, s41, 0
	s_lshl_b32 s30, s18, 13
	v_lshl_add_u64 v[160:161], v[172:173], 0, s[30:31]
	global_load_dwordx4 v[116:119], v[160:161], off
	s_lshl_b32 s30, s18, 9
	v_lshl_add_u64 v[160:161], v[174:175], 0, s[30:31]
	global_load_dword v122, v[160:161], off
	global_load_dword v123, v[160:161], off offset:256
	s_waitcnt vmcnt(31)
	v_and_b32_e32 v124, s6, v24
	v_and_b32_e32 v126, s7, v24
	v_and_b32_e32 v128, s42, v24
	v_lshrrev_b32_e32 v130, 24, v24
	v_and_b32_e32 v132, s6, v25
	v_and_b32_e32 v134, s7, v25
	v_and_b32_e32 v136, s42, v25
	v_lshrrev_b32_e32 v138, 24, v25
	s_waitcnt lgkmcnt(0)
	s_load_dwordx16 s[84:99], s[36:37], 0xc0 glc
	s_lshl_b32 s30, s68, 12
	s_add_u32 s28, s26, s30
	s_addc_u32 s29, s27, 0
	global_load_dwordx2 v[24:25], v162, s[28:29]
	v_and_b32_e32 v125, s6, v26
	v_and_b32_e32 v127, s7, v26
	v_and_b32_e32 v129, s42, v26
	v_lshrrev_b32_e32 v131, 24, v26
	v_and_b32_e32 v133, s6, v27
	v_and_b32_e32 v135, s7, v27
	v_and_b32_e32 v137, s42, v27
	v_lshrrev_b32_e32 v139, 24, v27
	s_lshl_b32 s30, s69, 12
	s_add_u32 s28, s26, s30
	s_addc_u32 s29, s27, 0
	global_load_dwordx2 v[26:27], v162, s[28:29]
	v_and_b32_e32 v140, s6, v28
	v_and_b32_e32 v142, s7, v28
	v_and_b32_e32 v144, s42, v28
	v_lshrrev_b32_e32 v146, 24, v28
	v_and_b32_e32 v148, s6, v29
	v_and_b32_e32 v150, s7, v29
	v_and_b32_e32 v152, s42, v29
	v_lshrrev_b32_e32 v154, 24, v29
	s_lshl_b32 s30, s70, 12
	s_add_u32 s28, s26, s30
	s_addc_u32 s29, s27, 0
	global_load_dwordx2 v[28:29], v162, s[28:29]
	v_and_b32_e32 v141, s6, v30
	v_and_b32_e32 v143, s7, v30
	v_and_b32_e32 v145, s42, v30
	v_lshrrev_b32_e32 v147, 24, v30
	v_and_b32_e32 v149, s6, v31
	v_and_b32_e32 v151, s7, v31
	v_and_b32_e32 v153, s42, v31
	v_lshrrev_b32_e32 v155, 24, v31
	s_lshl_b32 s30, s71, 12
	s_add_u32 s28, s26, s30
	s_addc_u32 s29, s27, 0
	global_load_dwordx2 v[30:31], v162, s[28:29]
	v_mul_f32_e32 v178, v124, v108
	v_mul_f32_e32 v179, v125, v108
	v_mul_f32_e32 v180, v140, v108
	v_mul_f32_e32 v181, v141, v108
	v_fmac_f32_e32 v178, v126, v109
	v_fmac_f32_e32 v179, v127, v109
	v_fmac_f32_e32 v180, v142, v109
	v_fmac_f32_e32 v181, v143, v109
	v_fmac_f32_e32 v178, v128, v110
	v_fmac_f32_e32 v179, v129, v110
	v_fmac_f32_e32 v180, v144, v110
	v_fmac_f32_e32 v181, v145, v110
	v_fmac_f32_e32 v178, v130, v111
	v_fmac_f32_e32 v179, v131, v111
	v_fmac_f32_e32 v180, v146, v111
	v_fmac_f32_e32 v181, v147, v111
	v_fmac_f32_e32 v178, v132, v112
	v_fmac_f32_e32 v179, v133, v112
	v_fmac_f32_e32 v180, v148, v112
	v_fmac_f32_e32 v181, v149, v112
	v_fmac_f32_e32 v178, v134, v113
	v_fmac_f32_e32 v179, v135, v113
	v_fmac_f32_e32 v180, v150, v113
	v_fmac_f32_e32 v181, v151, v113
	v_fmac_f32_e32 v178, v136, v114
	v_fmac_f32_e32 v179, v137, v114
	v_fmac_f32_e32 v180, v152, v114
	v_fmac_f32_e32 v181, v153, v114
	v_fmac_f32_e32 v178, v138, v115
	v_fmac_f32_e32 v179, v139, v115
	v_fmac_f32_e32 v180, v154, v115
	v_fmac_f32_e32 v181, v155, v115
	s_waitcnt vmcnt(31)
	v_and_b32_e32 v124, s6, v32
	v_and_b32_e32 v126, s7, v32
	v_and_b32_e32 v128, s42, v32
	v_lshrrev_b32_e32 v130, 24, v32
	v_and_b32_e32 v132, s6, v33
	v_and_b32_e32 v134, s7, v33
	v_and_b32_e32 v136, s42, v33
	v_lshrrev_b32_e32 v138, 24, v33
	s_lshl_b32 s30, s72, 12
	s_add_u32 s28, s26, s30
	s_addc_u32 s29, s27, 0
	global_load_dwordx2 v[32:33], v162, s[28:29]
	v_and_b32_e32 v125, s6, v34
	v_and_b32_e32 v127, s7, v34
	v_and_b32_e32 v129, s42, v34
	v_lshrrev_b32_e32 v131, 24, v34
	v_and_b32_e32 v133, s6, v35
	v_and_b32_e32 v135, s7, v35
	v_and_b32_e32 v137, s42, v35
	v_lshrrev_b32_e32 v139, 24, v35
	s_lshl_b32 s30, s73, 12
	s_add_u32 s28, s26, s30
	s_addc_u32 s29, s27, 0
	global_load_dwordx2 v[34:35], v162, s[28:29]
	v_and_b32_e32 v140, s6, v36
	v_and_b32_e32 v142, s7, v36
	v_and_b32_e32 v144, s42, v36
	v_lshrrev_b32_e32 v146, 24, v36
	v_and_b32_e32 v148, s6, v37
	v_and_b32_e32 v150, s7, v37
	v_and_b32_e32 v152, s42, v37
	v_lshrrev_b32_e32 v154, 24, v37
	s_lshl_b32 s30, s74, 12
	s_add_u32 s28, s26, s30
	s_addc_u32 s29, s27, 0
	global_load_dwordx2 v[36:37], v162, s[28:29]
	v_and_b32_e32 v141, s6, v38
	v_and_b32_e32 v143, s7, v38
	v_and_b32_e32 v145, s42, v38
	v_lshrrev_b32_e32 v147, 24, v38
	v_and_b32_e32 v149, s6, v39
	v_and_b32_e32 v151, s7, v39
	v_and_b32_e32 v153, s42, v39
	v_lshrrev_b32_e32 v155, 24, v39
	s_lshl_b32 s30, s75, 12
	s_add_u32 s28, s26, s30
	s_addc_u32 s29, s27, 0
	global_load_dwordx2 v[38:39], v162, s[28:29]
	v_mul_f32_e32 v182, v124, v108
	v_mul_f32_e32 v183, v125, v108
	v_mul_f32_e32 v184, v140, v108
	v_mul_f32_e32 v185, v141, v108
	v_fmac_f32_e32 v182, v126, v109
	v_fmac_f32_e32 v183, v127, v109
	v_fmac_f32_e32 v184, v142, v109
	v_fmac_f32_e32 v185, v143, v109
	v_fmac_f32_e32 v182, v128, v110
	v_fmac_f32_e32 v183, v129, v110
	v_fmac_f32_e32 v184, v144, v110
	v_fmac_f32_e32 v185, v145, v110
	v_fmac_f32_e32 v182, v130, v111
	v_fmac_f32_e32 v183, v131, v111
	v_fmac_f32_e32 v184, v146, v111
	v_fmac_f32_e32 v185, v147, v111
	v_fmac_f32_e32 v182, v132, v112
	v_fmac_f32_e32 v183, v133, v112
	v_fmac_f32_e32 v184, v148, v112
	v_fmac_f32_e32 v185, v149, v112
	v_fmac_f32_e32 v182, v134, v113
	v_fmac_f32_e32 v183, v135, v113
	v_fmac_f32_e32 v184, v150, v113
	v_fmac_f32_e32 v185, v151, v113
	v_fmac_f32_e32 v182, v136, v114
	v_fmac_f32_e32 v183, v137, v114
	v_fmac_f32_e32 v184, v152, v114
	v_fmac_f32_e32 v185, v153, v114
	v_fmac_f32_e32 v182, v138, v115
	v_fmac_f32_e32 v183, v139, v115
	v_fmac_f32_e32 v184, v154, v115
	v_fmac_f32_e32 v185, v155, v115
	s_waitcnt vmcnt(31)
	v_and_b32_e32 v124, s6, v40
	v_and_b32_e32 v126, s7, v40
	v_and_b32_e32 v128, s42, v40
	v_lshrrev_b32_e32 v130, 24, v40
	v_and_b32_e32 v132, s6, v41
	v_and_b32_e32 v134, s7, v41
	v_and_b32_e32 v136, s42, v41
	v_lshrrev_b32_e32 v138, 24, v41
	s_lshl_b32 s30, s76, 12
	s_add_u32 s28, s26, s30
	s_addc_u32 s29, s27, 0
	global_load_dwordx2 v[40:41], v162, s[28:29]
	v_and_b32_e32 v125, s6, v42
	v_and_b32_e32 v127, s7, v42
	v_and_b32_e32 v129, s42, v42
	v_lshrrev_b32_e32 v131, 24, v42
	v_and_b32_e32 v133, s6, v43
	v_and_b32_e32 v135, s7, v43
	v_and_b32_e32 v137, s42, v43
	v_lshrrev_b32_e32 v139, 24, v43
	s_lshl_b32 s30, s77, 12
	s_add_u32 s28, s26, s30
	s_addc_u32 s29, s27, 0
	global_load_dwordx2 v[42:43], v162, s[28:29]
	v_and_b32_e32 v140, s6, v44
	v_and_b32_e32 v142, s7, v44
	v_and_b32_e32 v144, s42, v44
	v_lshrrev_b32_e32 v146, 24, v44
	v_and_b32_e32 v148, s6, v45
	v_and_b32_e32 v150, s7, v45
	v_and_b32_e32 v152, s42, v45
	v_lshrrev_b32_e32 v154, 24, v45
	s_lshl_b32 s30, s78, 12
	s_add_u32 s28, s26, s30
	s_addc_u32 s29, s27, 0
	global_load_dwordx2 v[44:45], v162, s[28:29]
	v_and_b32_e32 v141, s6, v46
	v_and_b32_e32 v143, s7, v46
	v_and_b32_e32 v145, s42, v46
	v_lshrrev_b32_e32 v147, 24, v46
	v_and_b32_e32 v149, s6, v47
	v_and_b32_e32 v151, s7, v47
	v_and_b32_e32 v153, s42, v47
	v_lshrrev_b32_e32 v155, 24, v47
	s_lshl_b32 s30, s79, 12
	s_add_u32 s28, s26, s30
	s_addc_u32 s29, s27, 0
	global_load_dwordx2 v[46:47], v162, s[28:29]
	v_mul_f32_e32 v186, v124, v108
	v_mul_f32_e32 v187, v125, v108
	v_mul_f32_e32 v188, v140, v108
	v_mul_f32_e32 v189, v141, v108
	v_fmac_f32_e32 v186, v126, v109
	v_fmac_f32_e32 v187, v127, v109
	v_fmac_f32_e32 v188, v142, v109
	v_fmac_f32_e32 v189, v143, v109
	v_fmac_f32_e32 v186, v128, v110
	v_fmac_f32_e32 v187, v129, v110
	v_fmac_f32_e32 v188, v144, v110
	v_fmac_f32_e32 v189, v145, v110
	v_fmac_f32_e32 v186, v130, v111
	v_fmac_f32_e32 v187, v131, v111
	v_fmac_f32_e32 v188, v146, v111
	v_fmac_f32_e32 v189, v147, v111
	v_fmac_f32_e32 v186, v132, v112
	v_fmac_f32_e32 v187, v133, v112
	v_fmac_f32_e32 v188, v148, v112
	v_fmac_f32_e32 v189, v149, v112
	v_fmac_f32_e32 v186, v134, v113
	v_fmac_f32_e32 v187, v135, v113
	v_fmac_f32_e32 v188, v150, v113
	v_fmac_f32_e32 v189, v151, v113
	v_fmac_f32_e32 v186, v136, v114
	v_fmac_f32_e32 v187, v137, v114
	v_fmac_f32_e32 v188, v152, v114
	v_fmac_f32_e32 v189, v153, v114
	v_fmac_f32_e32 v186, v138, v115
	v_fmac_f32_e32 v187, v139, v115
	v_fmac_f32_e32 v188, v154, v115
	v_fmac_f32_e32 v189, v155, v115
	s_waitcnt vmcnt(31)
	v_and_b32_e32 v124, s6, v48
	v_and_b32_e32 v126, s7, v48
	v_and_b32_e32 v128, s42, v48
	v_lshrrev_b32_e32 v130, 24, v48
	v_and_b32_e32 v132, s6, v49
	v_and_b32_e32 v134, s7, v49
	v_and_b32_e32 v136, s42, v49
	v_lshrrev_b32_e32 v138, 24, v49
	s_lshl_b32 s30, s80, 12
	s_add_u32 s28, s26, s30
	s_addc_u32 s29, s27, 0
	global_load_dwordx2 v[48:49], v162, s[28:29]
	v_and_b32_e32 v125, s6, v50
	v_and_b32_e32 v127, s7, v50
	v_and_b32_e32 v129, s42, v50
	v_lshrrev_b32_e32 v131, 24, v50
	v_and_b32_e32 v133, s6, v51
	v_and_b32_e32 v135, s7, v51
	v_and_b32_e32 v137, s42, v51
	v_lshrrev_b32_e32 v139, 24, v51
	s_lshl_b32 s30, s81, 12
	s_add_u32 s28, s26, s30
	s_addc_u32 s29, s27, 0
	global_load_dwordx2 v[50:51], v162, s[28:29]
	v_and_b32_e32 v140, s6, v52
	v_and_b32_e32 v142, s7, v52
	v_and_b32_e32 v144, s42, v52
	v_lshrrev_b32_e32 v146, 24, v52
	v_and_b32_e32 v148, s6, v53
	v_and_b32_e32 v150, s7, v53
	v_and_b32_e32 v152, s42, v53
	v_lshrrev_b32_e32 v154, 24, v53
	s_lshl_b32 s30, s82, 12
	s_add_u32 s28, s26, s30
	s_addc_u32 s29, s27, 0
	global_load_dwordx2 v[52:53], v162, s[28:29]
	v_and_b32_e32 v141, s6, v54
	v_and_b32_e32 v143, s7, v54
	v_and_b32_e32 v145, s42, v54
	v_lshrrev_b32_e32 v147, 24, v54
	v_and_b32_e32 v149, s6, v55
	v_and_b32_e32 v151, s7, v55
	v_and_b32_e32 v153, s42, v55
	v_lshrrev_b32_e32 v155, 24, v55
	s_lshl_b32 s30, s83, 12
	s_add_u32 s28, s26, s30
	s_addc_u32 s29, s27, 0
	global_load_dwordx2 v[54:55], v162, s[28:29]
	v_mul_f32_e32 v190, v124, v108
	v_mul_f32_e32 v191, v125, v108
	v_mul_f32_e32 v192, v140, v108
	v_mul_f32_e32 v193, v141, v108
	v_fmac_f32_e32 v190, v126, v109
	v_fmac_f32_e32 v191, v127, v109
	v_fmac_f32_e32 v192, v142, v109
	v_fmac_f32_e32 v193, v143, v109
	v_fmac_f32_e32 v190, v128, v110
	v_fmac_f32_e32 v191, v129, v110
	v_fmac_f32_e32 v192, v144, v110
	v_fmac_f32_e32 v193, v145, v110
	v_fmac_f32_e32 v190, v130, v111
	v_fmac_f32_e32 v191, v131, v111
	v_fmac_f32_e32 v192, v146, v111
	v_fmac_f32_e32 v193, v147, v111
	v_fmac_f32_e32 v190, v132, v112
	v_fmac_f32_e32 v191, v133, v112
	v_fmac_f32_e32 v192, v148, v112
	v_fmac_f32_e32 v193, v149, v112
	v_fmac_f32_e32 v190, v134, v113
	v_fmac_f32_e32 v191, v135, v113
	v_fmac_f32_e32 v192, v150, v113
	v_fmac_f32_e32 v193, v151, v113
	v_fmac_f32_e32 v190, v136, v114
	v_fmac_f32_e32 v191, v137, v114
	v_fmac_f32_e32 v192, v152, v114
	v_fmac_f32_e32 v193, v153, v114
	v_fmac_f32_e32 v190, v138, v115
	v_fmac_f32_e32 v191, v139, v115
	v_fmac_f32_e32 v192, v154, v115
	v_fmac_f32_e32 v193, v155, v115
	s_waitcnt vmcnt(31)
	v_and_b32_e32 v124, s6, v56
	v_and_b32_e32 v126, s7, v56
	v_and_b32_e32 v128, s42, v56
	v_lshrrev_b32_e32 v130, 24, v56
	v_and_b32_e32 v132, s6, v57
	v_and_b32_e32 v134, s7, v57
	v_and_b32_e32 v136, s42, v57
	v_lshrrev_b32_e32 v138, 24, v57
	s_waitcnt lgkmcnt(0)
	s_load_dwordx16 s[68:83], s[36:37], 0x100 glc
	s_lshl_b32 s30, s84, 12
	s_add_u32 s28, s26, s30
	s_addc_u32 s29, s27, 0
	global_load_dwordx2 v[56:57], v162, s[28:29]
	v_and_b32_e32 v125, s6, v58
	v_and_b32_e32 v127, s7, v58
	v_and_b32_e32 v129, s42, v58
	v_lshrrev_b32_e32 v131, 24, v58
	v_and_b32_e32 v133, s6, v59
	v_and_b32_e32 v135, s7, v59
	v_and_b32_e32 v137, s42, v59
	v_lshrrev_b32_e32 v139, 24, v59
	s_lshl_b32 s30, s85, 12
	s_add_u32 s28, s26, s30
	s_addc_u32 s29, s27, 0
	global_load_dwordx2 v[58:59], v162, s[28:29]
	v_and_b32_e32 v140, s6, v60
	v_and_b32_e32 v142, s7, v60
	v_and_b32_e32 v144, s42, v60
	v_lshrrev_b32_e32 v146, 24, v60
	v_and_b32_e32 v148, s6, v61
	v_and_b32_e32 v150, s7, v61
	v_and_b32_e32 v152, s42, v61
	v_lshrrev_b32_e32 v154, 24, v61
	s_lshl_b32 s30, s86, 12
	s_add_u32 s28, s26, s30
	s_addc_u32 s29, s27, 0
	global_load_dwordx2 v[60:61], v162, s[28:29]
	v_and_b32_e32 v141, s6, v62
	v_and_b32_e32 v143, s7, v62
	v_and_b32_e32 v145, s42, v62
	v_lshrrev_b32_e32 v147, 24, v62
	v_and_b32_e32 v149, s6, v63
	v_and_b32_e32 v151, s7, v63
	v_and_b32_e32 v153, s42, v63
	v_lshrrev_b32_e32 v155, 24, v63
	s_lshl_b32 s30, s87, 12
	s_add_u32 s28, s26, s30
	s_addc_u32 s29, s27, 0
	global_load_dwordx2 v[62:63], v162, s[28:29]
	v_mul_f32_e32 v194, v124, v108
	v_mul_f32_e32 v195, v125, v108
	v_mul_f32_e32 v196, v140, v108
	v_mul_f32_e32 v197, v141, v108
	v_fmac_f32_e32 v194, v126, v109
	v_fmac_f32_e32 v195, v127, v109
	v_fmac_f32_e32 v196, v142, v109
	v_fmac_f32_e32 v197, v143, v109
	v_fmac_f32_e32 v194, v128, v110
	v_fmac_f32_e32 v195, v129, v110
	v_fmac_f32_e32 v196, v144, v110
	v_fmac_f32_e32 v197, v145, v110
	v_fmac_f32_e32 v194, v130, v111
	v_fmac_f32_e32 v195, v131, v111
	v_fmac_f32_e32 v196, v146, v111
	v_fmac_f32_e32 v197, v147, v111
	v_fmac_f32_e32 v194, v132, v112
	v_fmac_f32_e32 v195, v133, v112
	v_fmac_f32_e32 v196, v148, v112
	v_fmac_f32_e32 v197, v149, v112
	v_fmac_f32_e32 v194, v134, v113
	v_fmac_f32_e32 v195, v135, v113
	v_fmac_f32_e32 v196, v150, v113
	v_fmac_f32_e32 v197, v151, v113
	v_fmac_f32_e32 v194, v136, v114
	v_fmac_f32_e32 v195, v137, v114
	v_fmac_f32_e32 v196, v152, v114
	v_fmac_f32_e32 v197, v153, v114
	v_fmac_f32_e32 v194, v138, v115
	v_fmac_f32_e32 v195, v139, v115
	v_fmac_f32_e32 v196, v154, v115
	v_fmac_f32_e32 v197, v155, v115
	s_waitcnt vmcnt(31)
	v_and_b32_e32 v124, s6, v64
	v_and_b32_e32 v126, s7, v64
	v_and_b32_e32 v128, s42, v64
	v_lshrrev_b32_e32 v130, 24, v64
	v_and_b32_e32 v132, s6, v65
	v_and_b32_e32 v134, s7, v65
	v_and_b32_e32 v136, s42, v65
	v_lshrrev_b32_e32 v138, 24, v65
	s_lshl_b32 s30, s88, 12
	s_add_u32 s28, s26, s30
	s_addc_u32 s29, s27, 0
	global_load_dwordx2 v[64:65], v162, s[28:29]
	v_and_b32_e32 v125, s6, v66
	v_and_b32_e32 v127, s7, v66
	v_and_b32_e32 v129, s42, v66
	v_lshrrev_b32_e32 v131, 24, v66
	v_and_b32_e32 v133, s6, v67
	v_and_b32_e32 v135, s7, v67
	v_and_b32_e32 v137, s42, v67
	v_lshrrev_b32_e32 v139, 24, v67
	s_lshl_b32 s30, s89, 12
	s_add_u32 s28, s26, s30
	s_addc_u32 s29, s27, 0
	global_load_dwordx2 v[66:67], v162, s[28:29]
	v_and_b32_e32 v140, s6, v68
	v_and_b32_e32 v142, s7, v68
	v_and_b32_e32 v144, s42, v68
	v_lshrrev_b32_e32 v146, 24, v68
	v_and_b32_e32 v148, s6, v69
	v_and_b32_e32 v150, s7, v69
	v_and_b32_e32 v152, s42, v69
	v_lshrrev_b32_e32 v154, 24, v69
	s_lshl_b32 s30, s90, 12
	s_add_u32 s28, s26, s30
	s_addc_u32 s29, s27, 0
	global_load_dwordx2 v[68:69], v162, s[28:29]
	v_and_b32_e32 v141, s6, v70
	v_and_b32_e32 v143, s7, v70
	v_and_b32_e32 v145, s42, v70
	v_lshrrev_b32_e32 v147, 24, v70
	v_and_b32_e32 v149, s6, v71
	v_and_b32_e32 v151, s7, v71
	v_and_b32_e32 v153, s42, v71
	v_lshrrev_b32_e32 v155, 24, v71
	s_lshl_b32 s30, s91, 12
	s_add_u32 s28, s26, s30
	s_addc_u32 s29, s27, 0
	global_load_dwordx2 v[70:71], v162, s[28:29]
	v_mul_f32_e32 v198, v124, v108
	v_mul_f32_e32 v199, v125, v108
	v_mul_f32_e32 v200, v140, v108
	v_mul_f32_e32 v201, v141, v108
	v_fmac_f32_e32 v198, v126, v109
	v_fmac_f32_e32 v199, v127, v109
	v_fmac_f32_e32 v200, v142, v109
	v_fmac_f32_e32 v201, v143, v109
	v_fmac_f32_e32 v198, v128, v110
	v_fmac_f32_e32 v199, v129, v110
	v_fmac_f32_e32 v200, v144, v110
	v_fmac_f32_e32 v201, v145, v110
	v_fmac_f32_e32 v198, v130, v111
	v_fmac_f32_e32 v199, v131, v111
	v_fmac_f32_e32 v200, v146, v111
	v_fmac_f32_e32 v201, v147, v111
	v_fmac_f32_e32 v198, v132, v112
	v_fmac_f32_e32 v199, v133, v112
	v_fmac_f32_e32 v200, v148, v112
	v_fmac_f32_e32 v201, v149, v112
	v_fmac_f32_e32 v198, v134, v113
	v_fmac_f32_e32 v199, v135, v113
	v_fmac_f32_e32 v200, v150, v113
	v_fmac_f32_e32 v201, v151, v113
	v_fmac_f32_e32 v198, v136, v114
	v_fmac_f32_e32 v199, v137, v114
	v_fmac_f32_e32 v200, v152, v114
	v_fmac_f32_e32 v201, v153, v114
	v_fmac_f32_e32 v198, v138, v115
	v_fmac_f32_e32 v199, v139, v115
	v_fmac_f32_e32 v200, v154, v115
	v_fmac_f32_e32 v201, v155, v115
	s_waitcnt vmcnt(31)
	v_and_b32_e32 v124, s6, v72
	v_and_b32_e32 v126, s7, v72
	v_and_b32_e32 v128, s42, v72
	v_lshrrev_b32_e32 v130, 24, v72
	v_and_b32_e32 v132, s6, v73
	v_and_b32_e32 v134, s7, v73
	v_and_b32_e32 v136, s42, v73
	v_lshrrev_b32_e32 v138, 24, v73
	s_lshl_b32 s30, s92, 12
	s_add_u32 s28, s26, s30
	s_addc_u32 s29, s27, 0
	global_load_dwordx2 v[72:73], v162, s[28:29]
	v_and_b32_e32 v125, s6, v74
	v_and_b32_e32 v127, s7, v74
	v_and_b32_e32 v129, s42, v74
	v_lshrrev_b32_e32 v131, 24, v74
	v_and_b32_e32 v133, s6, v75
	v_and_b32_e32 v135, s7, v75
	v_and_b32_e32 v137, s42, v75
	v_lshrrev_b32_e32 v139, 24, v75
	s_lshl_b32 s30, s93, 12
	s_add_u32 s28, s26, s30
	s_addc_u32 s29, s27, 0
	global_load_dwordx2 v[74:75], v162, s[28:29]
	v_and_b32_e32 v140, s6, v76
	v_and_b32_e32 v142, s7, v76
	v_and_b32_e32 v144, s42, v76
	v_lshrrev_b32_e32 v146, 24, v76
	v_and_b32_e32 v148, s6, v77
	v_and_b32_e32 v150, s7, v77
	v_and_b32_e32 v152, s42, v77
	v_lshrrev_b32_e32 v154, 24, v77
	s_lshl_b32 s30, s94, 12
	s_add_u32 s28, s26, s30
	s_addc_u32 s29, s27, 0
	global_load_dwordx2 v[76:77], v162, s[28:29]
	v_and_b32_e32 v141, s6, v78
	v_and_b32_e32 v143, s7, v78
	v_and_b32_e32 v145, s42, v78
	v_lshrrev_b32_e32 v147, 24, v78
	v_and_b32_e32 v149, s6, v79
	v_and_b32_e32 v151, s7, v79
	v_and_b32_e32 v153, s42, v79
	v_lshrrev_b32_e32 v155, 24, v79
	s_lshl_b32 s30, s95, 12
	s_add_u32 s28, s26, s30
	s_addc_u32 s29, s27, 0
	global_load_dwordx2 v[78:79], v162, s[28:29]
	v_mul_f32_e32 v202, v124, v108
	v_mul_f32_e32 v203, v125, v108
	v_mul_f32_e32 v204, v140, v108
	v_mul_f32_e32 v205, v141, v108
	v_fmac_f32_e32 v202, v126, v109
	v_fmac_f32_e32 v203, v127, v109
	v_fmac_f32_e32 v204, v142, v109
	v_fmac_f32_e32 v205, v143, v109
	v_fmac_f32_e32 v202, v128, v110
	v_fmac_f32_e32 v203, v129, v110
	v_fmac_f32_e32 v204, v144, v110
	v_fmac_f32_e32 v205, v145, v110
	v_fmac_f32_e32 v202, v130, v111
	v_fmac_f32_e32 v203, v131, v111
	v_fmac_f32_e32 v204, v146, v111
	v_fmac_f32_e32 v205, v147, v111
	v_fmac_f32_e32 v202, v132, v112
	v_fmac_f32_e32 v203, v133, v112
	v_fmac_f32_e32 v204, v148, v112
	v_fmac_f32_e32 v205, v149, v112
	v_fmac_f32_e32 v202, v134, v113
	v_fmac_f32_e32 v203, v135, v113
	v_fmac_f32_e32 v204, v150, v113
	v_fmac_f32_e32 v205, v151, v113
	v_fmac_f32_e32 v202, v136, v114
	v_fmac_f32_e32 v203, v137, v114
	v_fmac_f32_e32 v204, v152, v114
	v_fmac_f32_e32 v205, v153, v114
	v_fmac_f32_e32 v202, v138, v115
	v_fmac_f32_e32 v203, v139, v115
	v_fmac_f32_e32 v204, v154, v115
	v_fmac_f32_e32 v205, v155, v115
	s_waitcnt vmcnt(31)
	v_and_b32_e32 v124, s6, v80
	v_and_b32_e32 v126, s7, v80
	v_and_b32_e32 v128, s42, v80
	v_lshrrev_b32_e32 v130, 24, v80
	v_and_b32_e32 v132, s6, v81
	v_and_b32_e32 v134, s7, v81
	v_and_b32_e32 v136, s42, v81
	v_lshrrev_b32_e32 v138, 24, v81
	s_lshl_b32 s30, s96, 12
	s_add_u32 s28, s26, s30
	s_addc_u32 s29, s27, 0
	global_load_dwordx2 v[80:81], v162, s[28:29]
	v_and_b32_e32 v125, s6, v82
	v_and_b32_e32 v127, s7, v82
	v_and_b32_e32 v129, s42, v82
	v_lshrrev_b32_e32 v131, 24, v82
	v_and_b32_e32 v133, s6, v83
	v_and_b32_e32 v135, s7, v83
	v_and_b32_e32 v137, s42, v83
	v_lshrrev_b32_e32 v139, 24, v83
	s_lshl_b32 s30, s97, 12
	s_add_u32 s28, s26, s30
	s_addc_u32 s29, s27, 0
	global_load_dwordx2 v[82:83], v162, s[28:29]
	v_and_b32_e32 v140, s6, v84
	v_and_b32_e32 v142, s7, v84
	v_and_b32_e32 v144, s42, v84
	v_lshrrev_b32_e32 v146, 24, v84
	v_and_b32_e32 v148, s6, v85
	v_and_b32_e32 v150, s7, v85
	v_and_b32_e32 v152, s42, v85
	v_lshrrev_b32_e32 v154, 24, v85
	s_lshl_b32 s30, s98, 12
	s_add_u32 s28, s26, s30
	s_addc_u32 s29, s27, 0
	global_load_dwordx2 v[84:85], v162, s[28:29]
	v_and_b32_e32 v141, s6, v86
	v_and_b32_e32 v143, s7, v86
	v_and_b32_e32 v145, s42, v86
	v_lshrrev_b32_e32 v147, 24, v86
	v_and_b32_e32 v149, s6, v87
	v_and_b32_e32 v151, s7, v87
	v_and_b32_e32 v153, s42, v87
	v_lshrrev_b32_e32 v155, 24, v87
	s_lshl_b32 s30, s99, 12
	s_add_u32 s28, s26, s30
	s_addc_u32 s29, s27, 0
	global_load_dwordx2 v[86:87], v162, s[28:29]
	v_mul_f32_e32 v206, v124, v108
	v_mul_f32_e32 v207, v125, v108
	v_mul_f32_e32 v208, v140, v108
	v_mul_f32_e32 v209, v141, v108
	v_fmac_f32_e32 v206, v126, v109
	v_fmac_f32_e32 v207, v127, v109
	v_fmac_f32_e32 v208, v142, v109
	v_fmac_f32_e32 v209, v143, v109
	v_fmac_f32_e32 v206, v128, v110
	v_fmac_f32_e32 v207, v129, v110
	v_fmac_f32_e32 v208, v144, v110
	v_fmac_f32_e32 v209, v145, v110
	v_fmac_f32_e32 v206, v130, v111
	v_fmac_f32_e32 v207, v131, v111
	v_fmac_f32_e32 v208, v146, v111
	v_fmac_f32_e32 v209, v147, v111
	v_fmac_f32_e32 v206, v132, v112
	v_fmac_f32_e32 v207, v133, v112
	v_fmac_f32_e32 v208, v148, v112
	v_fmac_f32_e32 v209, v149, v112
	v_fmac_f32_e32 v206, v134, v113
	v_fmac_f32_e32 v207, v135, v113
	v_fmac_f32_e32 v208, v150, v113
	v_fmac_f32_e32 v209, v151, v113
	v_fmac_f32_e32 v206, v136, v114
	v_fmac_f32_e32 v207, v137, v114
	v_fmac_f32_e32 v208, v152, v114
	v_fmac_f32_e32 v209, v153, v114
	v_fmac_f32_e32 v206, v138, v115
	v_fmac_f32_e32 v207, v139, v115
	v_fmac_f32_e32 v208, v154, v115
	v_fmac_f32_e32 v209, v155, v115
	v_permlane32_swap_b32_e32 v178, v194
	v_permlane32_swap_b32_e32 v179, v195
	v_permlane32_swap_b32_e32 v180, v196
	v_permlane32_swap_b32_e32 v181, v197
	v_permlane32_swap_b32_e32 v182, v198
	v_permlane32_swap_b32_e32 v183, v199
	v_permlane32_swap_b32_e32 v184, v200
	v_permlane32_swap_b32_e32 v185, v201
	v_permlane32_swap_b32_e32 v186, v202
	v_permlane32_swap_b32_e32 v187, v203
	v_permlane32_swap_b32_e32 v188, v204
	v_permlane32_swap_b32_e32 v189, v205
	v_permlane32_swap_b32_e32 v190, v206
	v_permlane32_swap_b32_e32 v191, v207
	v_permlane32_swap_b32_e32 v192, v208
	v_permlane32_swap_b32_e32 v193, v209
	v_add_f32_e32 v178, v178, v194
	v_add_f32_e32 v179, v179, v195
	v_add_f32_e32 v180, v180, v196
	v_add_f32_e32 v181, v181, v197
	v_add_f32_e32 v182, v182, v198
	v_add_f32_e32 v183, v183, v199
	v_add_f32_e32 v184, v184, v200
	v_add_f32_e32 v185, v185, v201
	v_add_f32_e32 v186, v186, v202
	v_add_f32_e32 v187, v187, v203
	v_add_f32_e32 v188, v188, v204
	v_add_f32_e32 v189, v189, v205
	v_add_f32_e32 v190, v190, v206
	v_add_f32_e32 v191, v191, v207
	v_add_f32_e32 v192, v192, v208
	v_add_f32_e32 v193, v193, v209
	v_permlane16_swap_b32_e32 v178, v186
	v_permlane16_swap_b32_e32 v179, v187
	v_permlane16_swap_b32_e32 v180, v188
	v_permlane16_swap_b32_e32 v181, v189
	v_permlane16_swap_b32_e32 v182, v190
	v_permlane16_swap_b32_e32 v183, v191
	v_permlane16_swap_b32_e32 v184, v192
	v_permlane16_swap_b32_e32 v185, v193
	v_add_f32_e32 v178, v178, v186
	v_add_f32_e32 v179, v179, v187
	v_add_f32_e32 v180, v180, v188
	v_add_f32_e32 v181, v181, v189
	v_add_f32_e32 v182, v182, v190
	v_add_f32_e32 v183, v183, v191
	v_add_f32_e32 v184, v184, v192
	v_add_f32_e32 v185, v185, v193
	v_cndmask_b32_e64 v2, v178, v182, s[8:9]
	v_cndmask_b32_e64 v3, v179, v183, s[8:9]
	v_cndmask_b32_e64 v4, v180, v184, s[8:9]
	v_cndmask_b32_e64 v5, v181, v185, s[8:9]
	v_cndmask_b32_e64 v6, v182, v178, s[8:9]
	v_cndmask_b32_e64 v7, v183, v179, s[8:9]
	v_cndmask_b32_e64 v8, v184, v180, s[8:9]
	v_cndmask_b32_e64 v9, v185, v181, s[8:9]
	v_add_f32_dpp v6, v2, v6 row_ror:8 row_mask:0xf bank_mask:0xf
	v_add_f32_dpp v7, v3, v7 row_ror:8 row_mask:0xf bank_mask:0xf
	v_add_f32_dpp v8, v4, v8 row_ror:8 row_mask:0xf bank_mask:0xf
	v_add_f32_dpp v9, v5, v9 row_ror:8 row_mask:0xf bank_mask:0xf
	v_cndmask_b32_e64 v2, v6, v8, s[10:11]
	v_cndmask_b32_e64 v3, v7, v9, s[10:11]
	v_cndmask_b32_e64 v4, v8, v6, s[10:11]
	v_cndmask_b32_e64 v5, v9, v7, s[10:11]
	v_add_f32_dpp v4, v2, v4 row_half_mirror row_mask:0xf bank_mask:0xf
	v_add_f32_dpp v5, v3, v5 row_half_mirror row_mask:0xf bank_mask:0xf
	v_cndmask_b32_e64 v2, v4, v5, s[14:15]
	v_cndmask_b32_e64 v3, v5, v4, s[14:15]
	s_nop 0
	v_add_f32_dpp v3, v2, v3 quad_perm:[2,3,0,1] row_mask:0xf bank_mask:0xf
	s_nop 1
	v_add_f32_dpp v11, v3, v3 quad_perm:[1,0,3,2] row_mask:0xf bank_mask:0xf
	v_mul_f32_e32 v11, 0x58000000, v11
	s_mov_b64 exec, s[2:3]
	global_store_dword v[22:23], v11, off
	s_mov_b64 exec, -1
	s_waitcnt vmcnt(29)
	v_and_b32_e32 v124, s6, v24
	v_and_b32_e32 v126, s7, v24
	v_and_b32_e32 v128, s42, v24
	v_lshrrev_b32_e32 v130, 24, v24
	v_and_b32_e32 v132, s6, v25
	v_and_b32_e32 v134, s7, v25
	v_and_b32_e32 v136, s42, v25
	v_lshrrev_b32_e32 v138, 24, v25
	s_waitcnt lgkmcnt(0)
	s_load_dwordx16 s[84:99], s[36:37], 0x140 glc
	s_lshl_b32 s30, s68, 12
	s_add_u32 s28, s26, s30
	s_addc_u32 s29, s27, 0
	global_load_dwordx2 v[24:25], v162, s[28:29]
	v_and_b32_e32 v125, s6, v26
	v_and_b32_e32 v127, s7, v26
	v_and_b32_e32 v129, s42, v26
	v_lshrrev_b32_e32 v131, 24, v26
	v_and_b32_e32 v133, s6, v27
	v_and_b32_e32 v135, s7, v27
	v_and_b32_e32 v137, s42, v27
	v_lshrrev_b32_e32 v139, 24, v27
	s_lshl_b32 s30, s69, 12
	s_add_u32 s28, s26, s30
	s_addc_u32 s29, s27, 0
	global_load_dwordx2 v[26:27], v162, s[28:29]
	v_and_b32_e32 v140, s6, v28
	v_and_b32_e32 v142, s7, v28
	v_and_b32_e32 v144, s42, v28
	v_lshrrev_b32_e32 v146, 24, v28
	v_and_b32_e32 v148, s6, v29
	v_and_b32_e32 v150, s7, v29
	v_and_b32_e32 v152, s42, v29
	v_lshrrev_b32_e32 v154, 24, v29
	s_lshl_b32 s30, s70, 12
	s_add_u32 s28, s26, s30
	s_addc_u32 s29, s27, 0
	global_load_dwordx2 v[28:29], v162, s[28:29]
	v_and_b32_e32 v141, s6, v30
	v_and_b32_e32 v143, s7, v30
	v_and_b32_e32 v145, s42, v30
	v_lshrrev_b32_e32 v147, 24, v30
	v_and_b32_e32 v149, s6, v31
	v_and_b32_e32 v151, s7, v31
	v_and_b32_e32 v153, s42, v31
	v_lshrrev_b32_e32 v155, 24, v31
	s_lshl_b32 s30, s71, 12
	s_add_u32 s28, s26, s30
	s_addc_u32 s29, s27, 0
	global_load_dwordx2 v[30:31], v162, s[28:29]
	v_mul_f32_e32 v178, v124, v108
	v_mul_f32_e32 v179, v125, v108
	v_mul_f32_e32 v180, v140, v108
	v_mul_f32_e32 v181, v141, v108
	v_fmac_f32_e32 v178, v126, v109
	v_fmac_f32_e32 v179, v127, v109
	v_fmac_f32_e32 v180, v142, v109
	v_fmac_f32_e32 v181, v143, v109
	v_fmac_f32_e32 v178, v128, v110
	v_fmac_f32_e32 v179, v129, v110
	v_fmac_f32_e32 v180, v144, v110
	v_fmac_f32_e32 v181, v145, v110
	v_fmac_f32_e32 v178, v130, v111
	v_fmac_f32_e32 v179, v131, v111
	v_fmac_f32_e32 v180, v146, v111
	v_fmac_f32_e32 v181, v147, v111
	v_fmac_f32_e32 v178, v132, v112
	v_fmac_f32_e32 v179, v133, v112
	v_fmac_f32_e32 v180, v148, v112
	v_fmac_f32_e32 v181, v149, v112
	v_fmac_f32_e32 v178, v134, v113
	v_fmac_f32_e32 v179, v135, v113
	v_fmac_f32_e32 v180, v150, v113
	v_fmac_f32_e32 v181, v151, v113
	v_fmac_f32_e32 v178, v136, v114
	v_fmac_f32_e32 v179, v137, v114
	v_fmac_f32_e32 v180, v152, v114
	v_fmac_f32_e32 v181, v153, v114
	v_fmac_f32_e32 v178, v138, v115
	v_fmac_f32_e32 v179, v139, v115
	v_fmac_f32_e32 v180, v154, v115
	v_fmac_f32_e32 v181, v155, v115
	s_waitcnt vmcnt(29)
	v_and_b32_e32 v124, s6, v32
	v_and_b32_e32 v126, s7, v32
	v_and_b32_e32 v128, s42, v32
	v_lshrrev_b32_e32 v130, 24, v32
	v_and_b32_e32 v132, s6, v33
	v_and_b32_e32 v134, s7, v33
	v_and_b32_e32 v136, s42, v33
	v_lshrrev_b32_e32 v138, 24, v33
	s_lshl_b32 s30, s72, 12
	s_add_u32 s28, s26, s30
	s_addc_u32 s29, s27, 0
	global_load_dwordx2 v[32:33], v162, s[28:29]
	v_and_b32_e32 v125, s6, v34
	v_and_b32_e32 v127, s7, v34
	v_and_b32_e32 v129, s42, v34
	v_lshrrev_b32_e32 v131, 24, v34
	v_and_b32_e32 v133, s6, v35
	v_and_b32_e32 v135, s7, v35
	v_and_b32_e32 v137, s42, v35
	v_lshrrev_b32_e32 v139, 24, v35
	s_lshl_b32 s30, s73, 12
	s_add_u32 s28, s26, s30
	s_addc_u32 s29, s27, 0
	global_load_dwordx2 v[34:35], v162, s[28:29]
	v_and_b32_e32 v140, s6, v36
	v_and_b32_e32 v142, s7, v36
	v_and_b32_e32 v144, s42, v36
	v_lshrrev_b32_e32 v146, 24, v36
	v_and_b32_e32 v148, s6, v37
	v_and_b32_e32 v150, s7, v37
	v_and_b32_e32 v152, s42, v37
	v_lshrrev_b32_e32 v154, 24, v37
	s_lshl_b32 s30, s74, 12
	s_add_u32 s28, s26, s30
	s_addc_u32 s29, s27, 0
	global_load_dwordx2 v[36:37], v162, s[28:29]
	v_and_b32_e32 v141, s6, v38
	v_and_b32_e32 v143, s7, v38
	v_and_b32_e32 v145, s42, v38
	v_lshrrev_b32_e32 v147, 24, v38
	v_and_b32_e32 v149, s6, v39
	v_and_b32_e32 v151, s7, v39
	v_and_b32_e32 v153, s42, v39
	v_lshrrev_b32_e32 v155, 24, v39
	s_lshl_b32 s30, s75, 12
	s_add_u32 s28, s26, s30
	s_addc_u32 s29, s27, 0
	global_load_dwordx2 v[38:39], v162, s[28:29]
	v_mul_f32_e32 v182, v124, v108
	v_mul_f32_e32 v183, v125, v108
	v_mul_f32_e32 v184, v140, v108
	v_mul_f32_e32 v185, v141, v108
	v_fmac_f32_e32 v182, v126, v109
	v_fmac_f32_e32 v183, v127, v109
	v_fmac_f32_e32 v184, v142, v109
	v_fmac_f32_e32 v185, v143, v109
	v_fmac_f32_e32 v182, v128, v110
	v_fmac_f32_e32 v183, v129, v110
	v_fmac_f32_e32 v184, v144, v110
	v_fmac_f32_e32 v185, v145, v110
	v_fmac_f32_e32 v182, v130, v111
	v_fmac_f32_e32 v183, v131, v111
	v_fmac_f32_e32 v184, v146, v111
	v_fmac_f32_e32 v185, v147, v111
	v_fmac_f32_e32 v182, v132, v112
	v_fmac_f32_e32 v183, v133, v112
	v_fmac_f32_e32 v184, v148, v112
	v_fmac_f32_e32 v185, v149, v112
	v_fmac_f32_e32 v182, v134, v113
	v_fmac_f32_e32 v183, v135, v113
	v_fmac_f32_e32 v184, v150, v113
	v_fmac_f32_e32 v185, v151, v113
	v_fmac_f32_e32 v182, v136, v114
	v_fmac_f32_e32 v183, v137, v114
	v_fmac_f32_e32 v184, v152, v114
	v_fmac_f32_e32 v185, v153, v114
	v_fmac_f32_e32 v182, v138, v115
	v_fmac_f32_e32 v183, v139, v115
	v_fmac_f32_e32 v184, v154, v115
	v_fmac_f32_e32 v185, v155, v115
	s_waitcnt vmcnt(29)
	v_and_b32_e32 v124, s6, v40
	v_and_b32_e32 v126, s7, v40
	v_and_b32_e32 v128, s42, v40
	v_lshrrev_b32_e32 v130, 24, v40
	v_and_b32_e32 v132, s6, v41
	v_and_b32_e32 v134, s7, v41
	v_and_b32_e32 v136, s42, v41
	v_lshrrev_b32_e32 v138, 24, v41
	s_lshl_b32 s30, s76, 12
	s_add_u32 s28, s26, s30
	s_addc_u32 s29, s27, 0
	global_load_dwordx2 v[40:41], v162, s[28:29]
	v_and_b32_e32 v125, s6, v42
	v_and_b32_e32 v127, s7, v42
	v_and_b32_e32 v129, s42, v42
	v_lshrrev_b32_e32 v131, 24, v42
	v_and_b32_e32 v133, s6, v43
	v_and_b32_e32 v135, s7, v43
	v_and_b32_e32 v137, s42, v43
	v_lshrrev_b32_e32 v139, 24, v43
	s_lshl_b32 s30, s77, 12
	s_add_u32 s28, s26, s30
	s_addc_u32 s29, s27, 0
	global_load_dwordx2 v[42:43], v162, s[28:29]
	v_and_b32_e32 v140, s6, v44
	v_and_b32_e32 v142, s7, v44
	v_and_b32_e32 v144, s42, v44
	v_lshrrev_b32_e32 v146, 24, v44
	v_and_b32_e32 v148, s6, v45
	v_and_b32_e32 v150, s7, v45
	v_and_b32_e32 v152, s42, v45
	v_lshrrev_b32_e32 v154, 24, v45
	s_lshl_b32 s30, s78, 12
	s_add_u32 s28, s26, s30
	s_addc_u32 s29, s27, 0
	global_load_dwordx2 v[44:45], v162, s[28:29]
	v_and_b32_e32 v141, s6, v46
	v_and_b32_e32 v143, s7, v46
	v_and_b32_e32 v145, s42, v46
	v_lshrrev_b32_e32 v147, 24, v46
	v_and_b32_e32 v149, s6, v47
	v_and_b32_e32 v151, s7, v47
	v_and_b32_e32 v153, s42, v47
	v_lshrrev_b32_e32 v155, 24, v47
	s_lshl_b32 s30, s79, 12
	s_add_u32 s28, s26, s30
	s_addc_u32 s29, s27, 0
	global_load_dwordx2 v[46:47], v162, s[28:29]
	v_mul_f32_e32 v186, v124, v108
	v_mul_f32_e32 v187, v125, v108
	v_mul_f32_e32 v188, v140, v108
	v_mul_f32_e32 v189, v141, v108
	v_fmac_f32_e32 v186, v126, v109
	v_fmac_f32_e32 v187, v127, v109
	v_fmac_f32_e32 v188, v142, v109
	v_fmac_f32_e32 v189, v143, v109
	v_fmac_f32_e32 v186, v128, v110
	v_fmac_f32_e32 v187, v129, v110
	v_fmac_f32_e32 v188, v144, v110
	v_fmac_f32_e32 v189, v145, v110
	v_fmac_f32_e32 v186, v130, v111
	v_fmac_f32_e32 v187, v131, v111
	v_fmac_f32_e32 v188, v146, v111
	v_fmac_f32_e32 v189, v147, v111
	v_fmac_f32_e32 v186, v132, v112
	v_fmac_f32_e32 v187, v133, v112
	v_fmac_f32_e32 v188, v148, v112
	v_fmac_f32_e32 v189, v149, v112
	v_fmac_f32_e32 v186, v134, v113
	v_fmac_f32_e32 v187, v135, v113
	v_fmac_f32_e32 v188, v150, v113
	v_fmac_f32_e32 v189, v151, v113
	v_fmac_f32_e32 v186, v136, v114
	v_fmac_f32_e32 v187, v137, v114
	v_fmac_f32_e32 v188, v152, v114
	v_fmac_f32_e32 v189, v153, v114
	v_fmac_f32_e32 v186, v138, v115
	v_fmac_f32_e32 v187, v139, v115
	v_fmac_f32_e32 v188, v154, v115
	v_fmac_f32_e32 v189, v155, v115
	s_waitcnt vmcnt(29)
	v_and_b32_e32 v124, s6, v48
	v_and_b32_e32 v126, s7, v48
	v_and_b32_e32 v128, s42, v48
	v_lshrrev_b32_e32 v130, 24, v48
	v_and_b32_e32 v132, s6, v49
	v_and_b32_e32 v134, s7, v49
	v_and_b32_e32 v136, s42, v49
	v_lshrrev_b32_e32 v138, 24, v49
	s_lshl_b32 s30, s80, 12
	s_add_u32 s28, s26, s30
	s_addc_u32 s29, s27, 0
	global_load_dwordx2 v[48:49], v162, s[28:29]
	v_and_b32_e32 v125, s6, v50
	v_and_b32_e32 v127, s7, v50
	v_and_b32_e32 v129, s42, v50
	v_lshrrev_b32_e32 v131, 24, v50
	v_and_b32_e32 v133, s6, v51
	v_and_b32_e32 v135, s7, v51
	v_and_b32_e32 v137, s42, v51
	v_lshrrev_b32_e32 v139, 24, v51
	s_lshl_b32 s30, s81, 12
	s_add_u32 s28, s26, s30
	s_addc_u32 s29, s27, 0
	global_load_dwordx2 v[50:51], v162, s[28:29]
	v_and_b32_e32 v140, s6, v52
	v_and_b32_e32 v142, s7, v52
	v_and_b32_e32 v144, s42, v52
	v_lshrrev_b32_e32 v146, 24, v52
	v_and_b32_e32 v148, s6, v53
	v_and_b32_e32 v150, s7, v53
	v_and_b32_e32 v152, s42, v53
	v_lshrrev_b32_e32 v154, 24, v53
	s_lshl_b32 s30, s82, 12
	s_add_u32 s28, s26, s30
	s_addc_u32 s29, s27, 0
	global_load_dwordx2 v[52:53], v162, s[28:29]
	v_and_b32_e32 v141, s6, v54
	v_and_b32_e32 v143, s7, v54
	v_and_b32_e32 v145, s42, v54
	v_lshrrev_b32_e32 v147, 24, v54
	v_and_b32_e32 v149, s6, v55
	v_and_b32_e32 v151, s7, v55
	v_and_b32_e32 v153, s42, v55
	v_lshrrev_b32_e32 v155, 24, v55
	s_lshl_b32 s30, s83, 12
	s_add_u32 s28, s26, s30
	s_addc_u32 s29, s27, 0
	global_load_dwordx2 v[54:55], v162, s[28:29]
	v_mul_f32_e32 v190, v124, v108
	v_mul_f32_e32 v191, v125, v108
	v_mul_f32_e32 v192, v140, v108
	v_mul_f32_e32 v193, v141, v108
	v_fmac_f32_e32 v190, v126, v109
	v_fmac_f32_e32 v191, v127, v109
	v_fmac_f32_e32 v192, v142, v109
	v_fmac_f32_e32 v193, v143, v109
	v_fmac_f32_e32 v190, v128, v110
	v_fmac_f32_e32 v191, v129, v110
	v_fmac_f32_e32 v192, v144, v110
	v_fmac_f32_e32 v193, v145, v110
	v_fmac_f32_e32 v190, v130, v111
	v_fmac_f32_e32 v191, v131, v111
	v_fmac_f32_e32 v192, v146, v111
	v_fmac_f32_e32 v193, v147, v111
	v_fmac_f32_e32 v190, v132, v112
	v_fmac_f32_e32 v191, v133, v112
	v_fmac_f32_e32 v192, v148, v112
	v_fmac_f32_e32 v193, v149, v112
	v_fmac_f32_e32 v190, v134, v113
	v_fmac_f32_e32 v191, v135, v113
	v_fmac_f32_e32 v192, v150, v113
	v_fmac_f32_e32 v193, v151, v113
	v_fmac_f32_e32 v190, v136, v114
	v_fmac_f32_e32 v191, v137, v114
	v_fmac_f32_e32 v192, v152, v114
	v_fmac_f32_e32 v193, v153, v114
	v_fmac_f32_e32 v190, v138, v115
	v_fmac_f32_e32 v191, v139, v115
	v_fmac_f32_e32 v192, v154, v115
	v_fmac_f32_e32 v193, v155, v115
	s_waitcnt vmcnt(29)
	v_and_b32_e32 v124, s6, v56
	v_and_b32_e32 v126, s7, v56
	v_and_b32_e32 v128, s42, v56
	v_lshrrev_b32_e32 v130, 24, v56
	v_and_b32_e32 v132, s6, v57
	v_and_b32_e32 v134, s7, v57
	v_and_b32_e32 v136, s42, v57
	v_lshrrev_b32_e32 v138, 24, v57
	s_waitcnt lgkmcnt(0)
	s_load_dwordx16 s[68:83], s[36:37], 0x180 glc
	s_lshl_b32 s30, s84, 12
	s_add_u32 s28, s26, s30
	s_addc_u32 s29, s27, 0
	global_load_dwordx2 v[56:57], v162, s[28:29]
	v_and_b32_e32 v125, s6, v58
	v_and_b32_e32 v127, s7, v58
	v_and_b32_e32 v129, s42, v58
	v_lshrrev_b32_e32 v131, 24, v58
	v_and_b32_e32 v133, s6, v59
	v_and_b32_e32 v135, s7, v59
	v_and_b32_e32 v137, s42, v59
	v_lshrrev_b32_e32 v139, 24, v59
	s_lshl_b32 s30, s85, 12
	s_add_u32 s28, s26, s30
	s_addc_u32 s29, s27, 0
	global_load_dwordx2 v[58:59], v162, s[28:29]
	v_and_b32_e32 v140, s6, v60
	v_and_b32_e32 v142, s7, v60
	v_and_b32_e32 v144, s42, v60
	v_lshrrev_b32_e32 v146, 24, v60
	v_and_b32_e32 v148, s6, v61
	v_and_b32_e32 v150, s7, v61
	v_and_b32_e32 v152, s42, v61
	v_lshrrev_b32_e32 v154, 24, v61
	s_lshl_b32 s30, s86, 12
	s_add_u32 s28, s26, s30
	s_addc_u32 s29, s27, 0
	global_load_dwordx2 v[60:61], v162, s[28:29]
	v_and_b32_e32 v141, s6, v62
	v_and_b32_e32 v143, s7, v62
	v_and_b32_e32 v145, s42, v62
	v_lshrrev_b32_e32 v147, 24, v62
	v_and_b32_e32 v149, s6, v63
	v_and_b32_e32 v151, s7, v63
	v_and_b32_e32 v153, s42, v63
	v_lshrrev_b32_e32 v155, 24, v63
	s_lshl_b32 s30, s87, 12
	s_add_u32 s28, s26, s30
	s_addc_u32 s29, s27, 0
	global_load_dwordx2 v[62:63], v162, s[28:29]
	v_mul_f32_e32 v194, v124, v108
	v_mul_f32_e32 v195, v125, v108
	v_mul_f32_e32 v196, v140, v108
	v_mul_f32_e32 v197, v141, v108
	v_fmac_f32_e32 v194, v126, v109
	v_fmac_f32_e32 v195, v127, v109
	v_fmac_f32_e32 v196, v142, v109
	v_fmac_f32_e32 v197, v143, v109
	v_fmac_f32_e32 v194, v128, v110
	v_fmac_f32_e32 v195, v129, v110
	v_fmac_f32_e32 v196, v144, v110
	v_fmac_f32_e32 v197, v145, v110
	v_fmac_f32_e32 v194, v130, v111
	v_fmac_f32_e32 v195, v131, v111
	v_fmac_f32_e32 v196, v146, v111
	v_fmac_f32_e32 v197, v147, v111
	v_fmac_f32_e32 v194, v132, v112
	v_fmac_f32_e32 v195, v133, v112
	v_fmac_f32_e32 v196, v148, v112
	v_fmac_f32_e32 v197, v149, v112
	v_fmac_f32_e32 v194, v134, v113
	v_fmac_f32_e32 v195, v135, v113
	v_fmac_f32_e32 v196, v150, v113
	v_fmac_f32_e32 v197, v151, v113
	v_fmac_f32_e32 v194, v136, v114
	v_fmac_f32_e32 v195, v137, v114
	v_fmac_f32_e32 v196, v152, v114
	v_fmac_f32_e32 v197, v153, v114
	v_fmac_f32_e32 v194, v138, v115
	v_fmac_f32_e32 v195, v139, v115
	v_fmac_f32_e32 v196, v154, v115
	v_fmac_f32_e32 v197, v155, v115
	s_waitcnt vmcnt(29)
	v_and_b32_e32 v124, s6, v64
	v_and_b32_e32 v126, s7, v64
	v_and_b32_e32 v128, s42, v64
	v_lshrrev_b32_e32 v130, 24, v64
	v_and_b32_e32 v132, s6, v65
	v_and_b32_e32 v134, s7, v65
	v_and_b32_e32 v136, s42, v65
	v_lshrrev_b32_e32 v138, 24, v65
	s_lshl_b32 s30, s88, 12
	s_add_u32 s28, s26, s30
	s_addc_u32 s29, s27, 0
	global_load_dwordx2 v[64:65], v162, s[28:29]
	v_and_b32_e32 v125, s6, v66
	v_and_b32_e32 v127, s7, v66
	v_and_b32_e32 v129, s42, v66
	v_lshrrev_b32_e32 v131, 24, v66
	v_and_b32_e32 v133, s6, v67
	v_and_b32_e32 v135, s7, v67
	v_and_b32_e32 v137, s42, v67
	v_lshrrev_b32_e32 v139, 24, v67
	s_lshl_b32 s30, s89, 12
	s_add_u32 s28, s26, s30
	s_addc_u32 s29, s27, 0
	global_load_dwordx2 v[66:67], v162, s[28:29]
	v_and_b32_e32 v140, s6, v68
	v_and_b32_e32 v142, s7, v68
	v_and_b32_e32 v144, s42, v68
	v_lshrrev_b32_e32 v146, 24, v68
	v_and_b32_e32 v148, s6, v69
	v_and_b32_e32 v150, s7, v69
	v_and_b32_e32 v152, s42, v69
	v_lshrrev_b32_e32 v154, 24, v69
	s_lshl_b32 s30, s90, 12
	s_add_u32 s28, s26, s30
	s_addc_u32 s29, s27, 0
	global_load_dwordx2 v[68:69], v162, s[28:29]
	v_and_b32_e32 v141, s6, v70
	v_and_b32_e32 v143, s7, v70
	v_and_b32_e32 v145, s42, v70
	v_lshrrev_b32_e32 v147, 24, v70
	v_and_b32_e32 v149, s6, v71
	v_and_b32_e32 v151, s7, v71
	v_and_b32_e32 v153, s42, v71
	v_lshrrev_b32_e32 v155, 24, v71
	s_lshl_b32 s30, s91, 12
	s_add_u32 s28, s26, s30
	s_addc_u32 s29, s27, 0
	global_load_dwordx2 v[70:71], v162, s[28:29]
	v_mul_f32_e32 v198, v124, v108
	v_mul_f32_e32 v199, v125, v108
	v_mul_f32_e32 v200, v140, v108
	v_mul_f32_e32 v201, v141, v108
	v_fmac_f32_e32 v198, v126, v109
	v_fmac_f32_e32 v199, v127, v109
	v_fmac_f32_e32 v200, v142, v109
	v_fmac_f32_e32 v201, v143, v109
	v_fmac_f32_e32 v198, v128, v110
	v_fmac_f32_e32 v199, v129, v110
	v_fmac_f32_e32 v200, v144, v110
	v_fmac_f32_e32 v201, v145, v110
	v_fmac_f32_e32 v198, v130, v111
	v_fmac_f32_e32 v199, v131, v111
	v_fmac_f32_e32 v200, v146, v111
	v_fmac_f32_e32 v201, v147, v111
	v_fmac_f32_e32 v198, v132, v112
	v_fmac_f32_e32 v199, v133, v112
	v_fmac_f32_e32 v200, v148, v112
	v_fmac_f32_e32 v201, v149, v112
	v_fmac_f32_e32 v198, v134, v113
	v_fmac_f32_e32 v199, v135, v113
	v_fmac_f32_e32 v200, v150, v113
	v_fmac_f32_e32 v201, v151, v113
	v_fmac_f32_e32 v198, v136, v114
	v_fmac_f32_e32 v199, v137, v114
	v_fmac_f32_e32 v200, v152, v114
	v_fmac_f32_e32 v201, v153, v114
	v_fmac_f32_e32 v198, v138, v115
	v_fmac_f32_e32 v199, v139, v115
	v_fmac_f32_e32 v200, v154, v115
	v_fmac_f32_e32 v201, v155, v115
	s_waitcnt vmcnt(29)
	v_and_b32_e32 v124, s6, v72
	v_and_b32_e32 v126, s7, v72
	v_and_b32_e32 v128, s42, v72
	v_lshrrev_b32_e32 v130, 24, v72
	v_and_b32_e32 v132, s6, v73
	v_and_b32_e32 v134, s7, v73
	v_and_b32_e32 v136, s42, v73
	v_lshrrev_b32_e32 v138, 24, v73
	s_lshl_b32 s30, s92, 12
	s_add_u32 s28, s26, s30
	s_addc_u32 s29, s27, 0
	global_load_dwordx2 v[72:73], v162, s[28:29]
	v_and_b32_e32 v125, s6, v74
	v_and_b32_e32 v127, s7, v74
	v_and_b32_e32 v129, s42, v74
	v_lshrrev_b32_e32 v131, 24, v74
	v_and_b32_e32 v133, s6, v75
	v_and_b32_e32 v135, s7, v75
	v_and_b32_e32 v137, s42, v75
	v_lshrrev_b32_e32 v139, 24, v75
	s_lshl_b32 s30, s93, 12
	s_add_u32 s28, s26, s30
	s_addc_u32 s29, s27, 0
	global_load_dwordx2 v[74:75], v162, s[28:29]
	v_and_b32_e32 v140, s6, v76
	v_and_b32_e32 v142, s7, v76
	v_and_b32_e32 v144, s42, v76
	v_lshrrev_b32_e32 v146, 24, v76
	v_and_b32_e32 v148, s6, v77
	v_and_b32_e32 v150, s7, v77
	v_and_b32_e32 v152, s42, v77
	v_lshrrev_b32_e32 v154, 24, v77
	s_lshl_b32 s30, s94, 12
	s_add_u32 s28, s26, s30
	s_addc_u32 s29, s27, 0
	global_load_dwordx2 v[76:77], v162, s[28:29]
	v_and_b32_e32 v141, s6, v78
	v_and_b32_e32 v143, s7, v78
	v_and_b32_e32 v145, s42, v78
	v_lshrrev_b32_e32 v147, 24, v78
	v_and_b32_e32 v149, s6, v79
	v_and_b32_e32 v151, s7, v79
	v_and_b32_e32 v153, s42, v79
	v_lshrrev_b32_e32 v155, 24, v79
	s_lshl_b32 s30, s95, 12
	s_add_u32 s28, s26, s30
	s_addc_u32 s29, s27, 0
	global_load_dwordx2 v[78:79], v162, s[28:29]
	v_mul_f32_e32 v202, v124, v108
	v_mul_f32_e32 v203, v125, v108
	v_mul_f32_e32 v204, v140, v108
	v_mul_f32_e32 v205, v141, v108
	v_fmac_f32_e32 v202, v126, v109
	v_fmac_f32_e32 v203, v127, v109
	v_fmac_f32_e32 v204, v142, v109
	v_fmac_f32_e32 v205, v143, v109
	v_fmac_f32_e32 v202, v128, v110
	v_fmac_f32_e32 v203, v129, v110
	v_fmac_f32_e32 v204, v144, v110
	v_fmac_f32_e32 v205, v145, v110
	v_fmac_f32_e32 v202, v130, v111
	v_fmac_f32_e32 v203, v131, v111
	v_fmac_f32_e32 v204, v146, v111
	v_fmac_f32_e32 v205, v147, v111
	v_fmac_f32_e32 v202, v132, v112
	v_fmac_f32_e32 v203, v133, v112
	v_fmac_f32_e32 v204, v148, v112
	v_fmac_f32_e32 v205, v149, v112
	v_fmac_f32_e32 v202, v134, v113
	v_fmac_f32_e32 v203, v135, v113
	v_fmac_f32_e32 v204, v150, v113
	v_fmac_f32_e32 v205, v151, v113
	v_fmac_f32_e32 v202, v136, v114
	v_fmac_f32_e32 v203, v137, v114
	v_fmac_f32_e32 v204, v152, v114
	v_fmac_f32_e32 v205, v153, v114
	v_fmac_f32_e32 v202, v138, v115
	v_fmac_f32_e32 v203, v139, v115
	v_fmac_f32_e32 v204, v154, v115
	v_fmac_f32_e32 v205, v155, v115
	s_waitcnt vmcnt(29)
	v_and_b32_e32 v124, s6, v80
	v_and_b32_e32 v126, s7, v80
	v_and_b32_e32 v128, s42, v80
	v_lshrrev_b32_e32 v130, 24, v80
	v_and_b32_e32 v132, s6, v81
	v_and_b32_e32 v134, s7, v81
	v_and_b32_e32 v136, s42, v81
	v_lshrrev_b32_e32 v138, 24, v81
	s_lshl_b32 s30, s96, 12
	s_add_u32 s28, s26, s30
	s_addc_u32 s29, s27, 0
	global_load_dwordx2 v[80:81], v162, s[28:29]
	v_and_b32_e32 v125, s6, v82
	v_and_b32_e32 v127, s7, v82
	v_and_b32_e32 v129, s42, v82
	v_lshrrev_b32_e32 v131, 24, v82
	v_and_b32_e32 v133, s6, v83
	v_and_b32_e32 v135, s7, v83
	v_and_b32_e32 v137, s42, v83
	v_lshrrev_b32_e32 v139, 24, v83
	s_lshl_b32 s30, s97, 12
	s_add_u32 s28, s26, s30
	s_addc_u32 s29, s27, 0
	global_load_dwordx2 v[82:83], v162, s[28:29]
	v_and_b32_e32 v140, s6, v84
	v_and_b32_e32 v142, s7, v84
	v_and_b32_e32 v144, s42, v84
	v_lshrrev_b32_e32 v146, 24, v84
	v_and_b32_e32 v148, s6, v85
	v_and_b32_e32 v150, s7, v85
	v_and_b32_e32 v152, s42, v85
	v_lshrrev_b32_e32 v154, 24, v85
	s_lshl_b32 s30, s98, 12
	s_add_u32 s28, s26, s30
	s_addc_u32 s29, s27, 0
	global_load_dwordx2 v[84:85], v162, s[28:29]
	v_and_b32_e32 v141, s6, v86
	v_and_b32_e32 v143, s7, v86
	v_and_b32_e32 v145, s42, v86
	v_lshrrev_b32_e32 v147, 24, v86
	v_and_b32_e32 v149, s6, v87
	v_and_b32_e32 v151, s7, v87
	v_and_b32_e32 v153, s42, v87
	v_lshrrev_b32_e32 v155, 24, v87
	s_lshl_b32 s30, s99, 12
	s_add_u32 s28, s26, s30
	s_addc_u32 s29, s27, 0
	global_load_dwordx2 v[86:87], v162, s[28:29]
	v_mul_f32_e32 v206, v124, v108
	v_mul_f32_e32 v207, v125, v108
	v_mul_f32_e32 v208, v140, v108
	v_mul_f32_e32 v209, v141, v108
	v_fmac_f32_e32 v206, v126, v109
	v_fmac_f32_e32 v207, v127, v109
	v_fmac_f32_e32 v208, v142, v109
	v_fmac_f32_e32 v209, v143, v109
	v_fmac_f32_e32 v206, v128, v110
	v_fmac_f32_e32 v207, v129, v110
	v_fmac_f32_e32 v208, v144, v110
	v_fmac_f32_e32 v209, v145, v110
	v_fmac_f32_e32 v206, v130, v111
	v_fmac_f32_e32 v207, v131, v111
	v_fmac_f32_e32 v208, v146, v111
	v_fmac_f32_e32 v209, v147, v111
	v_fmac_f32_e32 v206, v132, v112
	v_fmac_f32_e32 v207, v133, v112
	v_fmac_f32_e32 v208, v148, v112
	v_fmac_f32_e32 v209, v149, v112
	v_fmac_f32_e32 v206, v134, v113
	v_fmac_f32_e32 v207, v135, v113
	v_fmac_f32_e32 v208, v150, v113
	v_fmac_f32_e32 v209, v151, v113
	v_fmac_f32_e32 v206, v136, v114
	v_fmac_f32_e32 v207, v137, v114
	v_fmac_f32_e32 v208, v152, v114
	v_fmac_f32_e32 v209, v153, v114
	v_fmac_f32_e32 v206, v138, v115
	v_fmac_f32_e32 v207, v139, v115
	v_fmac_f32_e32 v208, v154, v115
	v_fmac_f32_e32 v209, v155, v115
	v_permlane32_swap_b32_e32 v178, v194
	v_permlane32_swap_b32_e32 v179, v195
	v_permlane32_swap_b32_e32 v180, v196
	v_permlane32_swap_b32_e32 v181, v197
	v_permlane32_swap_b32_e32 v182, v198
	v_permlane32_swap_b32_e32 v183, v199
	v_permlane32_swap_b32_e32 v184, v200
	v_permlane32_swap_b32_e32 v185, v201
	v_permlane32_swap_b32_e32 v186, v202
	v_permlane32_swap_b32_e32 v187, v203
	v_permlane32_swap_b32_e32 v188, v204
	v_permlane32_swap_b32_e32 v189, v205
	v_permlane32_swap_b32_e32 v190, v206
	v_permlane32_swap_b32_e32 v191, v207
	v_permlane32_swap_b32_e32 v192, v208
	v_permlane32_swap_b32_e32 v193, v209
	v_add_f32_e32 v178, v178, v194
	v_add_f32_e32 v179, v179, v195
	v_add_f32_e32 v180, v180, v196
	v_add_f32_e32 v181, v181, v197
	v_add_f32_e32 v182, v182, v198
	v_add_f32_e32 v183, v183, v199
	v_add_f32_e32 v184, v184, v200
	v_add_f32_e32 v185, v185, v201
	v_add_f32_e32 v186, v186, v202
	v_add_f32_e32 v187, v187, v203
	v_add_f32_e32 v188, v188, v204
	v_add_f32_e32 v189, v189, v205
	v_add_f32_e32 v190, v190, v206
	v_add_f32_e32 v191, v191, v207
	v_add_f32_e32 v192, v192, v208
	v_add_f32_e32 v193, v193, v209
	v_permlane16_swap_b32_e32 v178, v186
	v_permlane16_swap_b32_e32 v179, v187
	v_permlane16_swap_b32_e32 v180, v188
	v_permlane16_swap_b32_e32 v181, v189
	v_permlane16_swap_b32_e32 v182, v190
	v_permlane16_swap_b32_e32 v183, v191
	v_permlane16_swap_b32_e32 v184, v192
	v_permlane16_swap_b32_e32 v185, v193
	v_add_f32_e32 v178, v178, v186
	v_add_f32_e32 v179, v179, v187
	v_add_f32_e32 v180, v180, v188
	v_add_f32_e32 v181, v181, v189
	v_add_f32_e32 v182, v182, v190
	v_add_f32_e32 v183, v183, v191
	v_add_f32_e32 v184, v184, v192
	v_add_f32_e32 v185, v185, v193
	v_cndmask_b32_e64 v2, v178, v182, s[8:9]
	v_cndmask_b32_e64 v3, v179, v183, s[8:9]
	v_cndmask_b32_e64 v4, v180, v184, s[8:9]
	v_cndmask_b32_e64 v5, v181, v185, s[8:9]
	v_cndmask_b32_e64 v6, v182, v178, s[8:9]
	v_cndmask_b32_e64 v7, v183, v179, s[8:9]
	v_cndmask_b32_e64 v8, v184, v180, s[8:9]
	v_cndmask_b32_e64 v9, v185, v181, s[8:9]
	v_add_f32_dpp v6, v2, v6 row_ror:8 row_mask:0xf bank_mask:0xf
	v_add_f32_dpp v7, v3, v7 row_ror:8 row_mask:0xf bank_mask:0xf
	v_add_f32_dpp v8, v4, v8 row_ror:8 row_mask:0xf bank_mask:0xf
	v_add_f32_dpp v9, v5, v9 row_ror:8 row_mask:0xf bank_mask:0xf
	v_cndmask_b32_e64 v2, v6, v8, s[10:11]
	v_cndmask_b32_e64 v3, v7, v9, s[10:11]
	v_cndmask_b32_e64 v4, v8, v6, s[10:11]
	v_cndmask_b32_e64 v5, v9, v7, s[10:11]
	v_add_f32_dpp v4, v2, v4 row_half_mirror row_mask:0xf bank_mask:0xf
	v_add_f32_dpp v5, v3, v5 row_half_mirror row_mask:0xf bank_mask:0xf
	v_cndmask_b32_e64 v2, v4, v5, s[14:15]
	v_cndmask_b32_e64 v3, v5, v4, s[14:15]
	s_nop 0
	v_add_f32_dpp v3, v2, v3 quad_perm:[2,3,0,1] row_mask:0xf bank_mask:0xf
	s_nop 1
	v_add_f32_dpp v11, v3, v3 quad_perm:[1,0,3,2] row_mask:0xf bank_mask:0xf
	v_mul_f32_e32 v11, 0x58000000, v11
	s_mov_b64 exec, s[2:3]
	global_store_dword v[22:23], v11, off offset:128
	s_mov_b64 exec, -1
	s_waitcnt vmcnt(29)
	v_and_b32_e32 v124, s6, v24
	v_and_b32_e32 v126, s7, v24
	v_and_b32_e32 v128, s42, v24
	v_lshrrev_b32_e32 v130, 24, v24
	v_and_b32_e32 v132, s6, v25
	v_and_b32_e32 v134, s7, v25
	v_and_b32_e32 v136, s42, v25
	v_lshrrev_b32_e32 v138, 24, v25
	s_waitcnt lgkmcnt(0)
	s_load_dwordx16 s[84:99], s[36:37], 0x1c0 glc
	s_lshl_b32 s30, s68, 12
	s_add_u32 s28, s26, s30
	s_addc_u32 s29, s27, 0
	global_load_dwordx2 v[24:25], v162, s[28:29]
	v_and_b32_e32 v125, s6, v26
	v_and_b32_e32 v127, s7, v26
	v_and_b32_e32 v129, s42, v26
	v_lshrrev_b32_e32 v131, 24, v26
	v_and_b32_e32 v133, s6, v27
	v_and_b32_e32 v135, s7, v27
	v_and_b32_e32 v137, s42, v27
	v_lshrrev_b32_e32 v139, 24, v27
	s_lshl_b32 s30, s69, 12
	s_add_u32 s28, s26, s30
	s_addc_u32 s29, s27, 0
	global_load_dwordx2 v[26:27], v162, s[28:29]
	v_and_b32_e32 v140, s6, v28
	v_and_b32_e32 v142, s7, v28
	v_and_b32_e32 v144, s42, v28
	v_lshrrev_b32_e32 v146, 24, v28
	v_and_b32_e32 v148, s6, v29
	v_and_b32_e32 v150, s7, v29
	v_and_b32_e32 v152, s42, v29
	v_lshrrev_b32_e32 v154, 24, v29
	s_lshl_b32 s30, s70, 12
	s_add_u32 s28, s26, s30
	s_addc_u32 s29, s27, 0
	global_load_dwordx2 v[28:29], v162, s[28:29]
	v_and_b32_e32 v141, s6, v30
	v_and_b32_e32 v143, s7, v30
	v_and_b32_e32 v145, s42, v30
	v_lshrrev_b32_e32 v147, 24, v30
	v_and_b32_e32 v149, s6, v31
	v_and_b32_e32 v151, s7, v31
	v_and_b32_e32 v153, s42, v31
	v_lshrrev_b32_e32 v155, 24, v31
	s_lshl_b32 s30, s71, 12
	s_add_u32 s28, s26, s30
	s_addc_u32 s29, s27, 0
	global_load_dwordx2 v[30:31], v162, s[28:29]
	v_mul_f32_e32 v178, v124, v108
	v_mul_f32_e32 v179, v125, v108
	v_mul_f32_e32 v180, v140, v108
	v_mul_f32_e32 v181, v141, v108
	v_fmac_f32_e32 v178, v126, v109
	v_fmac_f32_e32 v179, v127, v109
	v_fmac_f32_e32 v180, v142, v109
	v_fmac_f32_e32 v181, v143, v109
	v_fmac_f32_e32 v178, v128, v110
	v_fmac_f32_e32 v179, v129, v110
	v_fmac_f32_e32 v180, v144, v110
	v_fmac_f32_e32 v181, v145, v110
	v_fmac_f32_e32 v178, v130, v111
	v_fmac_f32_e32 v179, v131, v111
	v_fmac_f32_e32 v180, v146, v111
	v_fmac_f32_e32 v181, v147, v111
	v_fmac_f32_e32 v178, v132, v112
	v_fmac_f32_e32 v179, v133, v112
	v_fmac_f32_e32 v180, v148, v112
	v_fmac_f32_e32 v181, v149, v112
	v_fmac_f32_e32 v178, v134, v113
	v_fmac_f32_e32 v179, v135, v113
	v_fmac_f32_e32 v180, v150, v113
	v_fmac_f32_e32 v181, v151, v113
	v_fmac_f32_e32 v178, v136, v114
	v_fmac_f32_e32 v179, v137, v114
	v_fmac_f32_e32 v180, v152, v114
	v_fmac_f32_e32 v181, v153, v114
	v_fmac_f32_e32 v178, v138, v115
	v_fmac_f32_e32 v179, v139, v115
	v_fmac_f32_e32 v180, v154, v115
	v_fmac_f32_e32 v181, v155, v115
	s_waitcnt vmcnt(29)
	v_and_b32_e32 v124, s6, v32
	v_and_b32_e32 v126, s7, v32
	v_and_b32_e32 v128, s42, v32
	v_lshrrev_b32_e32 v130, 24, v32
	v_and_b32_e32 v132, s6, v33
	v_and_b32_e32 v134, s7, v33
	v_and_b32_e32 v136, s42, v33
	v_lshrrev_b32_e32 v138, 24, v33
	s_lshl_b32 s30, s72, 12
	s_add_u32 s28, s26, s30
	s_addc_u32 s29, s27, 0
	global_load_dwordx2 v[32:33], v162, s[28:29]
	v_and_b32_e32 v125, s6, v34
	v_and_b32_e32 v127, s7, v34
	v_and_b32_e32 v129, s42, v34
	v_lshrrev_b32_e32 v131, 24, v34
	v_and_b32_e32 v133, s6, v35
	v_and_b32_e32 v135, s7, v35
	v_and_b32_e32 v137, s42, v35
	v_lshrrev_b32_e32 v139, 24, v35
	s_lshl_b32 s30, s73, 12
	s_add_u32 s28, s26, s30
	s_addc_u32 s29, s27, 0
	global_load_dwordx2 v[34:35], v162, s[28:29]
	v_and_b32_e32 v140, s6, v36
	v_and_b32_e32 v142, s7, v36
	v_and_b32_e32 v144, s42, v36
	v_lshrrev_b32_e32 v146, 24, v36
	v_and_b32_e32 v148, s6, v37
	v_and_b32_e32 v150, s7, v37
	v_and_b32_e32 v152, s42, v37
	v_lshrrev_b32_e32 v154, 24, v37
	s_lshl_b32 s30, s74, 12
	s_add_u32 s28, s26, s30
	s_addc_u32 s29, s27, 0
	global_load_dwordx2 v[36:37], v162, s[28:29]
	v_and_b32_e32 v141, s6, v38
	v_and_b32_e32 v143, s7, v38
	v_and_b32_e32 v145, s42, v38
	v_lshrrev_b32_e32 v147, 24, v38
	v_and_b32_e32 v149, s6, v39
	v_and_b32_e32 v151, s7, v39
	v_and_b32_e32 v153, s42, v39
	v_lshrrev_b32_e32 v155, 24, v39
	s_lshl_b32 s30, s75, 12
	s_add_u32 s28, s26, s30
	s_addc_u32 s29, s27, 0
	global_load_dwordx2 v[38:39], v162, s[28:29]
	v_mul_f32_e32 v182, v124, v108
	v_mul_f32_e32 v183, v125, v108
	v_mul_f32_e32 v184, v140, v108
	v_mul_f32_e32 v185, v141, v108
	v_fmac_f32_e32 v182, v126, v109
	v_fmac_f32_e32 v183, v127, v109
	v_fmac_f32_e32 v184, v142, v109
	v_fmac_f32_e32 v185, v143, v109
	v_fmac_f32_e32 v182, v128, v110
	v_fmac_f32_e32 v183, v129, v110
	v_fmac_f32_e32 v184, v144, v110
	v_fmac_f32_e32 v185, v145, v110
	v_fmac_f32_e32 v182, v130, v111
	v_fmac_f32_e32 v183, v131, v111
	v_fmac_f32_e32 v184, v146, v111
	v_fmac_f32_e32 v185, v147, v111
	v_fmac_f32_e32 v182, v132, v112
	v_fmac_f32_e32 v183, v133, v112
	v_fmac_f32_e32 v184, v148, v112
	v_fmac_f32_e32 v185, v149, v112
	v_fmac_f32_e32 v182, v134, v113
	v_fmac_f32_e32 v183, v135, v113
	v_fmac_f32_e32 v184, v150, v113
	v_fmac_f32_e32 v185, v151, v113
	v_fmac_f32_e32 v182, v136, v114
	v_fmac_f32_e32 v183, v137, v114
	v_fmac_f32_e32 v184, v152, v114
	v_fmac_f32_e32 v185, v153, v114
	v_fmac_f32_e32 v182, v138, v115
	v_fmac_f32_e32 v183, v139, v115
	v_fmac_f32_e32 v184, v154, v115
	v_fmac_f32_e32 v185, v155, v115
	s_waitcnt vmcnt(29)
	v_and_b32_e32 v124, s6, v40
	v_and_b32_e32 v126, s7, v40
	v_and_b32_e32 v128, s42, v40
	v_lshrrev_b32_e32 v130, 24, v40
	v_and_b32_e32 v132, s6, v41
	v_and_b32_e32 v134, s7, v41
	v_and_b32_e32 v136, s42, v41
	v_lshrrev_b32_e32 v138, 24, v41
	s_lshl_b32 s30, s76, 12
	s_add_u32 s28, s26, s30
	s_addc_u32 s29, s27, 0
	global_load_dwordx2 v[40:41], v162, s[28:29]
	v_and_b32_e32 v125, s6, v42
	v_and_b32_e32 v127, s7, v42
	v_and_b32_e32 v129, s42, v42
	v_lshrrev_b32_e32 v131, 24, v42
	v_and_b32_e32 v133, s6, v43
	v_and_b32_e32 v135, s7, v43
	v_and_b32_e32 v137, s42, v43
	v_lshrrev_b32_e32 v139, 24, v43
	s_lshl_b32 s30, s77, 12
	s_add_u32 s28, s26, s30
	s_addc_u32 s29, s27, 0
	global_load_dwordx2 v[42:43], v162, s[28:29]
	v_and_b32_e32 v140, s6, v44
	v_and_b32_e32 v142, s7, v44
	v_and_b32_e32 v144, s42, v44
	v_lshrrev_b32_e32 v146, 24, v44
	v_and_b32_e32 v148, s6, v45
	v_and_b32_e32 v150, s7, v45
	v_and_b32_e32 v152, s42, v45
	v_lshrrev_b32_e32 v154, 24, v45
	s_lshl_b32 s30, s78, 12
	s_add_u32 s28, s26, s30
	s_addc_u32 s29, s27, 0
	global_load_dwordx2 v[44:45], v162, s[28:29]
	v_and_b32_e32 v141, s6, v46
	v_and_b32_e32 v143, s7, v46
	v_and_b32_e32 v145, s42, v46
	v_lshrrev_b32_e32 v147, 24, v46
	v_and_b32_e32 v149, s6, v47
	v_and_b32_e32 v151, s7, v47
	v_and_b32_e32 v153, s42, v47
	v_lshrrev_b32_e32 v155, 24, v47
	s_lshl_b32 s30, s79, 12
	s_add_u32 s28, s26, s30
	s_addc_u32 s29, s27, 0
	global_load_dwordx2 v[46:47], v162, s[28:29]
	v_mul_f32_e32 v186, v124, v108
	v_mul_f32_e32 v187, v125, v108
	v_mul_f32_e32 v188, v140, v108
	v_mul_f32_e32 v189, v141, v108
	v_fmac_f32_e32 v186, v126, v109
	v_fmac_f32_e32 v187, v127, v109
	v_fmac_f32_e32 v188, v142, v109
	v_fmac_f32_e32 v189, v143, v109
	v_fmac_f32_e32 v186, v128, v110
	v_fmac_f32_e32 v187, v129, v110
	v_fmac_f32_e32 v188, v144, v110
	v_fmac_f32_e32 v189, v145, v110
	v_fmac_f32_e32 v186, v130, v111
	v_fmac_f32_e32 v187, v131, v111
	v_fmac_f32_e32 v188, v146, v111
	v_fmac_f32_e32 v189, v147, v111
	v_fmac_f32_e32 v186, v132, v112
	v_fmac_f32_e32 v187, v133, v112
	v_fmac_f32_e32 v188, v148, v112
	v_fmac_f32_e32 v189, v149, v112
	v_fmac_f32_e32 v186, v134, v113
	v_fmac_f32_e32 v187, v135, v113
	v_fmac_f32_e32 v188, v150, v113
	v_fmac_f32_e32 v189, v151, v113
	v_fmac_f32_e32 v186, v136, v114
	v_fmac_f32_e32 v187, v137, v114
	v_fmac_f32_e32 v188, v152, v114
	v_fmac_f32_e32 v189, v153, v114
	v_fmac_f32_e32 v186, v138, v115
	v_fmac_f32_e32 v187, v139, v115
	v_fmac_f32_e32 v188, v154, v115
	v_fmac_f32_e32 v189, v155, v115
	s_waitcnt vmcnt(29)
	v_and_b32_e32 v124, s6, v48
	v_and_b32_e32 v126, s7, v48
	v_and_b32_e32 v128, s42, v48
	v_lshrrev_b32_e32 v130, 24, v48
	v_and_b32_e32 v132, s6, v49
	v_and_b32_e32 v134, s7, v49
	v_and_b32_e32 v136, s42, v49
	v_lshrrev_b32_e32 v138, 24, v49
	s_lshl_b32 s30, s80, 12
	s_add_u32 s28, s26, s30
	s_addc_u32 s29, s27, 0
	global_load_dwordx2 v[48:49], v162, s[28:29]
	v_and_b32_e32 v125, s6, v50
	v_and_b32_e32 v127, s7, v50
	v_and_b32_e32 v129, s42, v50
	v_lshrrev_b32_e32 v131, 24, v50
	v_and_b32_e32 v133, s6, v51
	v_and_b32_e32 v135, s7, v51
	v_and_b32_e32 v137, s42, v51
	v_lshrrev_b32_e32 v139, 24, v51
	s_lshl_b32 s30, s81, 12
	s_add_u32 s28, s26, s30
	s_addc_u32 s29, s27, 0
	global_load_dwordx2 v[50:51], v162, s[28:29]
	v_and_b32_e32 v140, s6, v52
	v_and_b32_e32 v142, s7, v52
	v_and_b32_e32 v144, s42, v52
	v_lshrrev_b32_e32 v146, 24, v52
	v_and_b32_e32 v148, s6, v53
	v_and_b32_e32 v150, s7, v53
	v_and_b32_e32 v152, s42, v53
	v_lshrrev_b32_e32 v154, 24, v53
	s_lshl_b32 s30, s82, 12
	s_add_u32 s28, s26, s30
	s_addc_u32 s29, s27, 0
	global_load_dwordx2 v[52:53], v162, s[28:29]
	v_and_b32_e32 v141, s6, v54
	v_and_b32_e32 v143, s7, v54
	v_and_b32_e32 v145, s42, v54
	v_lshrrev_b32_e32 v147, 24, v54
	v_and_b32_e32 v149, s6, v55
	v_and_b32_e32 v151, s7, v55
	v_and_b32_e32 v153, s42, v55
	v_lshrrev_b32_e32 v155, 24, v55
	s_lshl_b32 s30, s83, 12
	s_add_u32 s28, s26, s30
	s_addc_u32 s29, s27, 0
	global_load_dwordx2 v[54:55], v162, s[28:29]
	v_mul_f32_e32 v190, v124, v108
	v_mul_f32_e32 v191, v125, v108
	v_mul_f32_e32 v192, v140, v108
	v_mul_f32_e32 v193, v141, v108
	v_fmac_f32_e32 v190, v126, v109
	v_fmac_f32_e32 v191, v127, v109
	v_fmac_f32_e32 v192, v142, v109
	v_fmac_f32_e32 v193, v143, v109
	v_fmac_f32_e32 v190, v128, v110
	v_fmac_f32_e32 v191, v129, v110
	v_fmac_f32_e32 v192, v144, v110
	v_fmac_f32_e32 v193, v145, v110
	v_fmac_f32_e32 v190, v130, v111
	v_fmac_f32_e32 v191, v131, v111
	v_fmac_f32_e32 v192, v146, v111
	v_fmac_f32_e32 v193, v147, v111
	v_fmac_f32_e32 v190, v132, v112
	v_fmac_f32_e32 v191, v133, v112
	v_fmac_f32_e32 v192, v148, v112
	v_fmac_f32_e32 v193, v149, v112
	v_fmac_f32_e32 v190, v134, v113
	v_fmac_f32_e32 v191, v135, v113
	v_fmac_f32_e32 v192, v150, v113
	v_fmac_f32_e32 v193, v151, v113
	v_fmac_f32_e32 v190, v136, v114
	v_fmac_f32_e32 v191, v137, v114
	v_fmac_f32_e32 v192, v152, v114
	v_fmac_f32_e32 v193, v153, v114
	v_fmac_f32_e32 v190, v138, v115
	v_fmac_f32_e32 v191, v139, v115
	v_fmac_f32_e32 v192, v154, v115
	v_fmac_f32_e32 v193, v155, v115
	s_waitcnt vmcnt(29)
	v_and_b32_e32 v124, s6, v56
	v_and_b32_e32 v126, s7, v56
	v_and_b32_e32 v128, s42, v56
	v_lshrrev_b32_e32 v130, 24, v56
	v_and_b32_e32 v132, s6, v57
	v_and_b32_e32 v134, s7, v57
	v_and_b32_e32 v136, s42, v57
	v_lshrrev_b32_e32 v138, 24, v57
	s_waitcnt lgkmcnt(0)
	s_load_dwordx16 s[68:83], s[38:39], 0x0 glc
	s_lshl_b32 s30, s84, 12
	s_add_u32 s28, s26, s30
	s_addc_u32 s29, s27, 0
	global_load_dwordx2 v[56:57], v162, s[28:29]
	v_and_b32_e32 v125, s6, v58
	v_and_b32_e32 v127, s7, v58
	v_and_b32_e32 v129, s42, v58
	v_lshrrev_b32_e32 v131, 24, v58
	v_and_b32_e32 v133, s6, v59
	v_and_b32_e32 v135, s7, v59
	v_and_b32_e32 v137, s42, v59
	v_lshrrev_b32_e32 v139, 24, v59
	s_lshl_b32 s30, s85, 12
	s_add_u32 s28, s26, s30
	s_addc_u32 s29, s27, 0
	global_load_dwordx2 v[58:59], v162, s[28:29]
	v_and_b32_e32 v140, s6, v60
	v_and_b32_e32 v142, s7, v60
	v_and_b32_e32 v144, s42, v60
	v_lshrrev_b32_e32 v146, 24, v60
	v_and_b32_e32 v148, s6, v61
	v_and_b32_e32 v150, s7, v61
	v_and_b32_e32 v152, s42, v61
	v_lshrrev_b32_e32 v154, 24, v61
	s_lshl_b32 s30, s86, 12
	s_add_u32 s28, s26, s30
	s_addc_u32 s29, s27, 0
	global_load_dwordx2 v[60:61], v162, s[28:29]
	v_and_b32_e32 v141, s6, v62
	v_and_b32_e32 v143, s7, v62
	v_and_b32_e32 v145, s42, v62
	v_lshrrev_b32_e32 v147, 24, v62
	v_and_b32_e32 v149, s6, v63
	v_and_b32_e32 v151, s7, v63
	v_and_b32_e32 v153, s42, v63
	v_lshrrev_b32_e32 v155, 24, v63
	s_lshl_b32 s30, s87, 12
	s_add_u32 s28, s26, s30
	s_addc_u32 s29, s27, 0
	global_load_dwordx2 v[62:63], v162, s[28:29]
	v_mul_f32_e32 v194, v124, v108
	v_mul_f32_e32 v195, v125, v108
	v_mul_f32_e32 v196, v140, v108
	v_mul_f32_e32 v197, v141, v108
	v_fmac_f32_e32 v194, v126, v109
	v_fmac_f32_e32 v195, v127, v109
	v_fmac_f32_e32 v196, v142, v109
	v_fmac_f32_e32 v197, v143, v109
	v_fmac_f32_e32 v194, v128, v110
	v_fmac_f32_e32 v195, v129, v110
	v_fmac_f32_e32 v196, v144, v110
	v_fmac_f32_e32 v197, v145, v110
	v_fmac_f32_e32 v194, v130, v111
	v_fmac_f32_e32 v195, v131, v111
	v_fmac_f32_e32 v196, v146, v111
	v_fmac_f32_e32 v197, v147, v111
	v_fmac_f32_e32 v194, v132, v112
	v_fmac_f32_e32 v195, v133, v112
	v_fmac_f32_e32 v196, v148, v112
	v_fmac_f32_e32 v197, v149, v112
	v_fmac_f32_e32 v194, v134, v113
	v_fmac_f32_e32 v195, v135, v113
	v_fmac_f32_e32 v196, v150, v113
	v_fmac_f32_e32 v197, v151, v113
	v_fmac_f32_e32 v194, v136, v114
	v_fmac_f32_e32 v195, v137, v114
	v_fmac_f32_e32 v196, v152, v114
	v_fmac_f32_e32 v197, v153, v114
	v_fmac_f32_e32 v194, v138, v115
	v_fmac_f32_e32 v195, v139, v115
	v_fmac_f32_e32 v196, v154, v115
	v_fmac_f32_e32 v197, v155, v115
	s_waitcnt vmcnt(29)
	v_and_b32_e32 v124, s6, v64
	v_and_b32_e32 v126, s7, v64
	v_and_b32_e32 v128, s42, v64
	v_lshrrev_b32_e32 v130, 24, v64
	v_and_b32_e32 v132, s6, v65
	v_and_b32_e32 v134, s7, v65
	v_and_b32_e32 v136, s42, v65
	v_lshrrev_b32_e32 v138, 24, v65
	s_lshl_b32 s30, s88, 12
	s_add_u32 s28, s26, s30
	s_addc_u32 s29, s27, 0
	global_load_dwordx2 v[64:65], v162, s[28:29]
	v_and_b32_e32 v125, s6, v66
	v_and_b32_e32 v127, s7, v66
	v_and_b32_e32 v129, s42, v66
	v_lshrrev_b32_e32 v131, 24, v66
	v_and_b32_e32 v133, s6, v67
	v_and_b32_e32 v135, s7, v67
	v_and_b32_e32 v137, s42, v67
	v_lshrrev_b32_e32 v139, 24, v67
	s_lshl_b32 s30, s89, 12
	s_add_u32 s28, s26, s30
	s_addc_u32 s29, s27, 0
	global_load_dwordx2 v[66:67], v162, s[28:29]
	v_and_b32_e32 v140, s6, v68
	v_and_b32_e32 v142, s7, v68
	v_and_b32_e32 v144, s42, v68
	v_lshrrev_b32_e32 v146, 24, v68
	v_and_b32_e32 v148, s6, v69
	v_and_b32_e32 v150, s7, v69
	v_and_b32_e32 v152, s42, v69
	v_lshrrev_b32_e32 v154, 24, v69
	s_lshl_b32 s30, s90, 12
	s_add_u32 s28, s26, s30
	s_addc_u32 s29, s27, 0
	global_load_dwordx2 v[68:69], v162, s[28:29]
	v_and_b32_e32 v141, s6, v70
	v_and_b32_e32 v143, s7, v70
	v_and_b32_e32 v145, s42, v70
	v_lshrrev_b32_e32 v147, 24, v70
	v_and_b32_e32 v149, s6, v71
	v_and_b32_e32 v151, s7, v71
	v_and_b32_e32 v153, s42, v71
	v_lshrrev_b32_e32 v155, 24, v71
	s_lshl_b32 s30, s91, 12
	s_add_u32 s28, s26, s30
	s_addc_u32 s29, s27, 0
	global_load_dwordx2 v[70:71], v162, s[28:29]
	v_mul_f32_e32 v198, v124, v108
	v_mul_f32_e32 v199, v125, v108
	v_mul_f32_e32 v200, v140, v108
	v_mul_f32_e32 v201, v141, v108
	v_fmac_f32_e32 v198, v126, v109
	v_fmac_f32_e32 v199, v127, v109
	v_fmac_f32_e32 v200, v142, v109
	v_fmac_f32_e32 v201, v143, v109
	v_fmac_f32_e32 v198, v128, v110
	v_fmac_f32_e32 v199, v129, v110
	v_fmac_f32_e32 v200, v144, v110
	v_fmac_f32_e32 v201, v145, v110
	v_fmac_f32_e32 v198, v130, v111
	v_fmac_f32_e32 v199, v131, v111
	v_fmac_f32_e32 v200, v146, v111
	v_fmac_f32_e32 v201, v147, v111
	v_fmac_f32_e32 v198, v132, v112
	v_fmac_f32_e32 v199, v133, v112
	v_fmac_f32_e32 v200, v148, v112
	v_fmac_f32_e32 v201, v149, v112
	v_fmac_f32_e32 v198, v134, v113
	v_fmac_f32_e32 v199, v135, v113
	v_fmac_f32_e32 v200, v150, v113
	v_fmac_f32_e32 v201, v151, v113
	v_fmac_f32_e32 v198, v136, v114
	v_fmac_f32_e32 v199, v137, v114
	v_fmac_f32_e32 v200, v152, v114
	v_fmac_f32_e32 v201, v153, v114
	v_fmac_f32_e32 v198, v138, v115
	v_fmac_f32_e32 v199, v139, v115
	v_fmac_f32_e32 v200, v154, v115
	v_fmac_f32_e32 v201, v155, v115
	s_waitcnt vmcnt(29)
	v_and_b32_e32 v124, s6, v72
	v_and_b32_e32 v126, s7, v72
	v_and_b32_e32 v128, s42, v72
	v_lshrrev_b32_e32 v130, 24, v72
	v_and_b32_e32 v132, s6, v73
	v_and_b32_e32 v134, s7, v73
	v_and_b32_e32 v136, s42, v73
	v_lshrrev_b32_e32 v138, 24, v73
	s_lshl_b32 s30, s92, 12
	s_add_u32 s28, s26, s30
	s_addc_u32 s29, s27, 0
	global_load_dwordx2 v[72:73], v162, s[28:29]
	v_and_b32_e32 v125, s6, v74
	v_and_b32_e32 v127, s7, v74
	v_and_b32_e32 v129, s42, v74
	v_lshrrev_b32_e32 v131, 24, v74
	v_and_b32_e32 v133, s6, v75
	v_and_b32_e32 v135, s7, v75
	v_and_b32_e32 v137, s42, v75
	v_lshrrev_b32_e32 v139, 24, v75
	s_lshl_b32 s30, s93, 12
	s_add_u32 s28, s26, s30
	s_addc_u32 s29, s27, 0
	global_load_dwordx2 v[74:75], v162, s[28:29]
	v_and_b32_e32 v140, s6, v76
	v_and_b32_e32 v142, s7, v76
	v_and_b32_e32 v144, s42, v76
	v_lshrrev_b32_e32 v146, 24, v76
	v_and_b32_e32 v148, s6, v77
	v_and_b32_e32 v150, s7, v77
	v_and_b32_e32 v152, s42, v77
	v_lshrrev_b32_e32 v154, 24, v77
	s_lshl_b32 s30, s94, 12
	s_add_u32 s28, s26, s30
	s_addc_u32 s29, s27, 0
	global_load_dwordx2 v[76:77], v162, s[28:29]
	v_and_b32_e32 v141, s6, v78
	v_and_b32_e32 v143, s7, v78
	v_and_b32_e32 v145, s42, v78
	v_lshrrev_b32_e32 v147, 24, v78
	v_and_b32_e32 v149, s6, v79
	v_and_b32_e32 v151, s7, v79
	v_and_b32_e32 v153, s42, v79
	v_lshrrev_b32_e32 v155, 24, v79
	s_lshl_b32 s30, s95, 12
	s_add_u32 s28, s26, s30
	s_addc_u32 s29, s27, 0
	global_load_dwordx2 v[78:79], v162, s[28:29]
	v_mul_f32_e32 v202, v124, v108
	v_mul_f32_e32 v203, v125, v108
	v_mul_f32_e32 v204, v140, v108
	v_mul_f32_e32 v205, v141, v108
	v_fmac_f32_e32 v202, v126, v109
	v_fmac_f32_e32 v203, v127, v109
	v_fmac_f32_e32 v204, v142, v109
	v_fmac_f32_e32 v205, v143, v109
	v_fmac_f32_e32 v202, v128, v110
	v_fmac_f32_e32 v203, v129, v110
	v_fmac_f32_e32 v204, v144, v110
	v_fmac_f32_e32 v205, v145, v110
	v_fmac_f32_e32 v202, v130, v111
	v_fmac_f32_e32 v203, v131, v111
	v_fmac_f32_e32 v204, v146, v111
	v_fmac_f32_e32 v205, v147, v111
	v_fmac_f32_e32 v202, v132, v112
	v_fmac_f32_e32 v203, v133, v112
	v_fmac_f32_e32 v204, v148, v112
	v_fmac_f32_e32 v205, v149, v112
	v_fmac_f32_e32 v202, v134, v113
	v_fmac_f32_e32 v203, v135, v113
	v_fmac_f32_e32 v204, v150, v113
	v_fmac_f32_e32 v205, v151, v113
	v_fmac_f32_e32 v202, v136, v114
	v_fmac_f32_e32 v203, v137, v114
	v_fmac_f32_e32 v204, v152, v114
	v_fmac_f32_e32 v205, v153, v114
	v_fmac_f32_e32 v202, v138, v115
	v_fmac_f32_e32 v203, v139, v115
	v_fmac_f32_e32 v204, v154, v115
	v_fmac_f32_e32 v205, v155, v115
	s_waitcnt vmcnt(29)
	v_and_b32_e32 v124, s6, v80
	v_and_b32_e32 v126, s7, v80
	v_and_b32_e32 v128, s42, v80
	v_lshrrev_b32_e32 v130, 24, v80
	v_and_b32_e32 v132, s6, v81
	v_and_b32_e32 v134, s7, v81
	v_and_b32_e32 v136, s42, v81
	v_lshrrev_b32_e32 v138, 24, v81
	s_lshl_b32 s30, s96, 12
	s_add_u32 s28, s26, s30
	s_addc_u32 s29, s27, 0
	global_load_dwordx2 v[80:81], v162, s[28:29]
	v_and_b32_e32 v125, s6, v82
	v_and_b32_e32 v127, s7, v82
	v_and_b32_e32 v129, s42, v82
	v_lshrrev_b32_e32 v131, 24, v82
	v_and_b32_e32 v133, s6, v83
	v_and_b32_e32 v135, s7, v83
	v_and_b32_e32 v137, s42, v83
	v_lshrrev_b32_e32 v139, 24, v83
	s_lshl_b32 s30, s97, 12
	s_add_u32 s28, s26, s30
	s_addc_u32 s29, s27, 0
	global_load_dwordx2 v[82:83], v162, s[28:29]
	v_and_b32_e32 v140, s6, v84
	v_and_b32_e32 v142, s7, v84
	v_and_b32_e32 v144, s42, v84
	v_lshrrev_b32_e32 v146, 24, v84
	v_and_b32_e32 v148, s6, v85
	v_and_b32_e32 v150, s7, v85
	v_and_b32_e32 v152, s42, v85
	v_lshrrev_b32_e32 v154, 24, v85
	s_lshl_b32 s30, s98, 12
	s_add_u32 s28, s26, s30
	s_addc_u32 s29, s27, 0
	global_load_dwordx2 v[84:85], v162, s[28:29]
	v_and_b32_e32 v141, s6, v86
	v_and_b32_e32 v143, s7, v86
	v_and_b32_e32 v145, s42, v86
	v_lshrrev_b32_e32 v147, 24, v86
	v_and_b32_e32 v149, s6, v87
	v_and_b32_e32 v151, s7, v87
	v_and_b32_e32 v153, s42, v87
	v_lshrrev_b32_e32 v155, 24, v87
	s_lshl_b32 s30, s99, 12
	s_add_u32 s28, s26, s30
	s_addc_u32 s29, s27, 0
	global_load_dwordx2 v[86:87], v162, s[28:29]
	v_mul_f32_e32 v206, v124, v108
	v_mul_f32_e32 v207, v125, v108
	v_mul_f32_e32 v208, v140, v108
	v_mul_f32_e32 v209, v141, v108
	v_fmac_f32_e32 v206, v126, v109
	v_fmac_f32_e32 v207, v127, v109
	v_fmac_f32_e32 v208, v142, v109
	v_fmac_f32_e32 v209, v143, v109
	v_fmac_f32_e32 v206, v128, v110
	v_fmac_f32_e32 v207, v129, v110
	v_fmac_f32_e32 v208, v144, v110
	v_fmac_f32_e32 v209, v145, v110
	v_fmac_f32_e32 v206, v130, v111
	v_fmac_f32_e32 v207, v131, v111
	v_fmac_f32_e32 v208, v146, v111
	v_fmac_f32_e32 v209, v147, v111
	v_fmac_f32_e32 v206, v132, v112
	v_fmac_f32_e32 v207, v133, v112
	v_fmac_f32_e32 v208, v148, v112
	v_fmac_f32_e32 v209, v149, v112
	v_fmac_f32_e32 v206, v134, v113
	v_fmac_f32_e32 v207, v135, v113
	v_fmac_f32_e32 v208, v150, v113
	v_fmac_f32_e32 v209, v151, v113
	v_fmac_f32_e32 v206, v136, v114
	v_fmac_f32_e32 v207, v137, v114
	v_fmac_f32_e32 v208, v152, v114
	v_fmac_f32_e32 v209, v153, v114
	v_fmac_f32_e32 v206, v138, v115
	v_fmac_f32_e32 v207, v139, v115
	v_fmac_f32_e32 v208, v154, v115
	v_fmac_f32_e32 v209, v155, v115
	v_permlane32_swap_b32_e32 v178, v194
	v_permlane32_swap_b32_e32 v179, v195
	v_permlane32_swap_b32_e32 v180, v196
	v_permlane32_swap_b32_e32 v181, v197
	v_permlane32_swap_b32_e32 v182, v198
	v_permlane32_swap_b32_e32 v183, v199
	v_permlane32_swap_b32_e32 v184, v200
	v_permlane32_swap_b32_e32 v185, v201
	v_permlane32_swap_b32_e32 v186, v202
	v_permlane32_swap_b32_e32 v187, v203
	v_permlane32_swap_b32_e32 v188, v204
	v_permlane32_swap_b32_e32 v189, v205
	v_permlane32_swap_b32_e32 v190, v206
	v_permlane32_swap_b32_e32 v191, v207
	v_permlane32_swap_b32_e32 v192, v208
	v_permlane32_swap_b32_e32 v193, v209
	v_add_f32_e32 v178, v178, v194
	v_add_f32_e32 v179, v179, v195
	v_add_f32_e32 v180, v180, v196
	v_add_f32_e32 v181, v181, v197
	v_add_f32_e32 v182, v182, v198
	v_add_f32_e32 v183, v183, v199
	v_add_f32_e32 v184, v184, v200
	v_add_f32_e32 v185, v185, v201
	v_add_f32_e32 v186, v186, v202
	v_add_f32_e32 v187, v187, v203
	v_add_f32_e32 v188, v188, v204
	v_add_f32_e32 v189, v189, v205
	v_add_f32_e32 v190, v190, v206
	v_add_f32_e32 v191, v191, v207
	v_add_f32_e32 v192, v192, v208
	v_add_f32_e32 v193, v193, v209
	v_permlane16_swap_b32_e32 v178, v186
	v_permlane16_swap_b32_e32 v179, v187
	v_permlane16_swap_b32_e32 v180, v188
	v_permlane16_swap_b32_e32 v181, v189
	v_permlane16_swap_b32_e32 v182, v190
	v_permlane16_swap_b32_e32 v183, v191
	v_permlane16_swap_b32_e32 v184, v192
	v_permlane16_swap_b32_e32 v185, v193
	v_add_f32_e32 v178, v178, v186
	v_add_f32_e32 v179, v179, v187
	v_add_f32_e32 v180, v180, v188
	v_add_f32_e32 v181, v181, v189
	v_add_f32_e32 v182, v182, v190
	v_add_f32_e32 v183, v183, v191
	v_add_f32_e32 v184, v184, v192
	v_add_f32_e32 v185, v185, v193
	v_cndmask_b32_e64 v2, v178, v182, s[8:9]
	v_cndmask_b32_e64 v3, v179, v183, s[8:9]
	v_cndmask_b32_e64 v4, v180, v184, s[8:9]
	v_cndmask_b32_e64 v5, v181, v185, s[8:9]
	v_cndmask_b32_e64 v6, v182, v178, s[8:9]
	v_cndmask_b32_e64 v7, v183, v179, s[8:9]
	v_cndmask_b32_e64 v8, v184, v180, s[8:9]
	v_cndmask_b32_e64 v9, v185, v181, s[8:9]
	v_add_f32_dpp v6, v2, v6 row_ror:8 row_mask:0xf bank_mask:0xf
	v_add_f32_dpp v7, v3, v7 row_ror:8 row_mask:0xf bank_mask:0xf
	v_add_f32_dpp v8, v4, v8 row_ror:8 row_mask:0xf bank_mask:0xf
	v_add_f32_dpp v9, v5, v9 row_ror:8 row_mask:0xf bank_mask:0xf
	v_cndmask_b32_e64 v2, v6, v8, s[10:11]
	v_cndmask_b32_e64 v3, v7, v9, s[10:11]
	v_cndmask_b32_e64 v4, v8, v6, s[10:11]
	v_cndmask_b32_e64 v5, v9, v7, s[10:11]
	v_add_f32_dpp v4, v2, v4 row_half_mirror row_mask:0xf bank_mask:0xf
	v_add_f32_dpp v5, v3, v5 row_half_mirror row_mask:0xf bank_mask:0xf
	v_cndmask_b32_e64 v2, v4, v5, s[14:15]
	v_cndmask_b32_e64 v3, v5, v4, s[14:15]
	s_nop 0
	v_add_f32_dpp v3, v2, v3 quad_perm:[2,3,0,1] row_mask:0xf bank_mask:0xf
	s_nop 1
	v_add_f32_dpp v11, v3, v3 quad_perm:[1,0,3,2] row_mask:0xf bank_mask:0xf
	v_mul_f32_e32 v11, 0x58000000, v11
	s_mov_b64 exec, s[2:3]
	global_store_dword v[22:23], v11, off offset:256
	s_mov_b64 exec, -1
	s_waitcnt vmcnt(29)
	v_and_b32_e32 v124, s6, v24
	v_and_b32_e32 v126, s7, v24
	v_and_b32_e32 v128, s42, v24
	v_lshrrev_b32_e32 v130, 24, v24
	v_and_b32_e32 v132, s6, v25
	v_and_b32_e32 v134, s7, v25
	v_and_b32_e32 v136, s42, v25
	v_lshrrev_b32_e32 v138, 24, v25
	v_and_b32_e32 v125, s6, v26
	v_and_b32_e32 v127, s7, v26
	v_and_b32_e32 v129, s42, v26
	v_lshrrev_b32_e32 v131, 24, v26
	v_and_b32_e32 v133, s6, v27
	v_and_b32_e32 v135, s7, v27
	v_and_b32_e32 v137, s42, v27
	v_lshrrev_b32_e32 v139, 24, v27
	v_and_b32_e32 v140, s6, v28
	v_and_b32_e32 v142, s7, v28
	v_and_b32_e32 v144, s42, v28
	v_lshrrev_b32_e32 v146, 24, v28
	v_and_b32_e32 v148, s6, v29
	v_and_b32_e32 v150, s7, v29
	v_and_b32_e32 v152, s42, v29
	v_lshrrev_b32_e32 v154, 24, v29
	v_and_b32_e32 v141, s6, v30
	v_and_b32_e32 v143, s7, v30
	v_and_b32_e32 v145, s42, v30
	v_lshrrev_b32_e32 v147, 24, v30
	v_and_b32_e32 v149, s6, v31
	v_and_b32_e32 v151, s7, v31
	v_and_b32_e32 v153, s42, v31
	v_lshrrev_b32_e32 v155, 24, v31
	v_mul_f32_e32 v178, v124, v108
	v_mul_f32_e32 v179, v125, v108
	v_mul_f32_e32 v180, v140, v108
	v_mul_f32_e32 v181, v141, v108
	v_fmac_f32_e32 v178, v126, v109
	v_fmac_f32_e32 v179, v127, v109
	v_fmac_f32_e32 v180, v142, v109
	v_fmac_f32_e32 v181, v143, v109
	v_fmac_f32_e32 v178, v128, v110
	v_fmac_f32_e32 v179, v129, v110
	v_fmac_f32_e32 v180, v144, v110
	v_fmac_f32_e32 v181, v145, v110
	v_fmac_f32_e32 v178, v130, v111
	v_fmac_f32_e32 v179, v131, v111
	v_fmac_f32_e32 v180, v146, v111
	v_fmac_f32_e32 v181, v147, v111
	v_fmac_f32_e32 v178, v132, v112
	v_fmac_f32_e32 v179, v133, v112
	v_fmac_f32_e32 v180, v148, v112
	v_fmac_f32_e32 v181, v149, v112
	v_fmac_f32_e32 v178, v134, v113
	v_fmac_f32_e32 v179, v135, v113
	v_fmac_f32_e32 v180, v150, v113
	v_fmac_f32_e32 v181, v151, v113
	v_fmac_f32_e32 v178, v136, v114
	v_fmac_f32_e32 v179, v137, v114
	v_fmac_f32_e32 v180, v152, v114
	v_fmac_f32_e32 v181, v153, v114
	v_fmac_f32_e32 v178, v138, v115
	v_fmac_f32_e32 v179, v139, v115
	v_fmac_f32_e32 v180, v154, v115
	v_fmac_f32_e32 v181, v155, v115
	s_waitcnt vmcnt(25)
	v_and_b32_e32 v124, s6, v32
	v_and_b32_e32 v126, s7, v32
	v_and_b32_e32 v128, s42, v32
	v_lshrrev_b32_e32 v130, 24, v32
	v_and_b32_e32 v132, s6, v33
	v_and_b32_e32 v134, s7, v33
	v_and_b32_e32 v136, s42, v33
	v_lshrrev_b32_e32 v138, 24, v33
	v_and_b32_e32 v125, s6, v34
	v_and_b32_e32 v127, s7, v34
	v_and_b32_e32 v129, s42, v34
	v_lshrrev_b32_e32 v131, 24, v34
	v_and_b32_e32 v133, s6, v35
	v_and_b32_e32 v135, s7, v35
	v_and_b32_e32 v137, s42, v35
	v_lshrrev_b32_e32 v139, 24, v35
	v_and_b32_e32 v140, s6, v36
	v_and_b32_e32 v142, s7, v36
	v_and_b32_e32 v144, s42, v36
	v_lshrrev_b32_e32 v146, 24, v36
	v_and_b32_e32 v148, s6, v37
	v_and_b32_e32 v150, s7, v37
	v_and_b32_e32 v152, s42, v37
	v_lshrrev_b32_e32 v154, 24, v37
	v_and_b32_e32 v141, s6, v38
	v_and_b32_e32 v143, s7, v38
	v_and_b32_e32 v145, s42, v38
	v_lshrrev_b32_e32 v147, 24, v38
	v_and_b32_e32 v149, s6, v39
	v_and_b32_e32 v151, s7, v39
	v_and_b32_e32 v153, s42, v39
	v_lshrrev_b32_e32 v155, 24, v39
	v_mul_f32_e32 v182, v124, v108
	v_mul_f32_e32 v183, v125, v108
	v_mul_f32_e32 v184, v140, v108
	v_mul_f32_e32 v185, v141, v108
	v_fmac_f32_e32 v182, v126, v109
	v_fmac_f32_e32 v183, v127, v109
	v_fmac_f32_e32 v184, v142, v109
	v_fmac_f32_e32 v185, v143, v109
	v_fmac_f32_e32 v182, v128, v110
	v_fmac_f32_e32 v183, v129, v110
	v_fmac_f32_e32 v184, v144, v110
	v_fmac_f32_e32 v185, v145, v110
	v_fmac_f32_e32 v182, v130, v111
	v_fmac_f32_e32 v183, v131, v111
	v_fmac_f32_e32 v184, v146, v111
	v_fmac_f32_e32 v185, v147, v111
	v_fmac_f32_e32 v182, v132, v112
	v_fmac_f32_e32 v183, v133, v112
	v_fmac_f32_e32 v184, v148, v112
	v_fmac_f32_e32 v185, v149, v112
	v_fmac_f32_e32 v182, v134, v113
	v_fmac_f32_e32 v183, v135, v113
	v_fmac_f32_e32 v184, v150, v113
	v_fmac_f32_e32 v185, v151, v113
	v_fmac_f32_e32 v182, v136, v114
	v_fmac_f32_e32 v183, v137, v114
	v_fmac_f32_e32 v184, v152, v114
	v_fmac_f32_e32 v185, v153, v114
	v_fmac_f32_e32 v182, v138, v115
	v_fmac_f32_e32 v183, v139, v115
	v_fmac_f32_e32 v184, v154, v115
	v_fmac_f32_e32 v185, v155, v115
	s_waitcnt vmcnt(21)
	v_and_b32_e32 v124, s6, v40
	v_and_b32_e32 v126, s7, v40
	v_and_b32_e32 v128, s42, v40
	v_lshrrev_b32_e32 v130, 24, v40
	v_and_b32_e32 v132, s6, v41
	v_and_b32_e32 v134, s7, v41
	v_and_b32_e32 v136, s42, v41
	v_lshrrev_b32_e32 v138, 24, v41
	v_and_b32_e32 v125, s6, v42
	v_and_b32_e32 v127, s7, v42
	v_and_b32_e32 v129, s42, v42
	v_lshrrev_b32_e32 v131, 24, v42
	v_and_b32_e32 v133, s6, v43
	v_and_b32_e32 v135, s7, v43
	v_and_b32_e32 v137, s42, v43
	v_lshrrev_b32_e32 v139, 24, v43
	v_and_b32_e32 v140, s6, v44
	v_and_b32_e32 v142, s7, v44
	v_and_b32_e32 v144, s42, v44
	v_lshrrev_b32_e32 v146, 24, v44
	v_and_b32_e32 v148, s6, v45
	v_and_b32_e32 v150, s7, v45
	v_and_b32_e32 v152, s42, v45
	v_lshrrev_b32_e32 v154, 24, v45
	v_and_b32_e32 v141, s6, v46
	v_and_b32_e32 v143, s7, v46
	v_and_b32_e32 v145, s42, v46
	v_lshrrev_b32_e32 v147, 24, v46
	v_and_b32_e32 v149, s6, v47
	v_and_b32_e32 v151, s7, v47
	v_and_b32_e32 v153, s42, v47
	v_lshrrev_b32_e32 v155, 24, v47
	v_mul_f32_e32 v186, v124, v108
	v_mul_f32_e32 v187, v125, v108
	v_mul_f32_e32 v188, v140, v108
	v_mul_f32_e32 v189, v141, v108
	v_fmac_f32_e32 v186, v126, v109
	v_fmac_f32_e32 v187, v127, v109
	v_fmac_f32_e32 v188, v142, v109
	v_fmac_f32_e32 v189, v143, v109
	v_fmac_f32_e32 v186, v128, v110
	v_fmac_f32_e32 v187, v129, v110
	v_fmac_f32_e32 v188, v144, v110
	v_fmac_f32_e32 v189, v145, v110
	v_fmac_f32_e32 v186, v130, v111
	v_fmac_f32_e32 v187, v131, v111
	v_fmac_f32_e32 v188, v146, v111
	v_fmac_f32_e32 v189, v147, v111
	v_fmac_f32_e32 v186, v132, v112
	v_fmac_f32_e32 v187, v133, v112
	v_fmac_f32_e32 v188, v148, v112
	v_fmac_f32_e32 v189, v149, v112
	v_fmac_f32_e32 v186, v134, v113
	v_fmac_f32_e32 v187, v135, v113
	v_fmac_f32_e32 v188, v150, v113
	v_fmac_f32_e32 v189, v151, v113
	v_fmac_f32_e32 v186, v136, v114
	v_fmac_f32_e32 v187, v137, v114
	v_fmac_f32_e32 v188, v152, v114
	v_fmac_f32_e32 v189, v153, v114
	v_fmac_f32_e32 v186, v138, v115
	v_fmac_f32_e32 v187, v139, v115
	v_fmac_f32_e32 v188, v154, v115
	v_fmac_f32_e32 v189, v155, v115
	s_waitcnt vmcnt(17)
	v_and_b32_e32 v124, s6, v48
	v_and_b32_e32 v126, s7, v48
	v_and_b32_e32 v128, s42, v48
	v_lshrrev_b32_e32 v130, 24, v48
	v_and_b32_e32 v132, s6, v49
	v_and_b32_e32 v134, s7, v49
	v_and_b32_e32 v136, s42, v49
	v_lshrrev_b32_e32 v138, 24, v49
	v_and_b32_e32 v125, s6, v50
	v_and_b32_e32 v127, s7, v50
	v_and_b32_e32 v129, s42, v50
	v_lshrrev_b32_e32 v131, 24, v50
	v_and_b32_e32 v133, s6, v51
	v_and_b32_e32 v135, s7, v51
	v_and_b32_e32 v137, s42, v51
	v_lshrrev_b32_e32 v139, 24, v51
	v_and_b32_e32 v140, s6, v52
	v_and_b32_e32 v142, s7, v52
	v_and_b32_e32 v144, s42, v52
	v_lshrrev_b32_e32 v146, 24, v52
	v_and_b32_e32 v148, s6, v53
	v_and_b32_e32 v150, s7, v53
	v_and_b32_e32 v152, s42, v53
	v_lshrrev_b32_e32 v154, 24, v53
	v_and_b32_e32 v141, s6, v54
	v_and_b32_e32 v143, s7, v54
	v_and_b32_e32 v145, s42, v54
	v_lshrrev_b32_e32 v147, 24, v54
	v_and_b32_e32 v149, s6, v55
	v_and_b32_e32 v151, s7, v55
	v_and_b32_e32 v153, s42, v55
	v_lshrrev_b32_e32 v155, 24, v55
	v_mul_f32_e32 v190, v124, v108
	v_mul_f32_e32 v191, v125, v108
	v_mul_f32_e32 v192, v140, v108
	v_mul_f32_e32 v193, v141, v108
	v_fmac_f32_e32 v190, v126, v109
	v_fmac_f32_e32 v191, v127, v109
	v_fmac_f32_e32 v192, v142, v109
	v_fmac_f32_e32 v193, v143, v109
	v_fmac_f32_e32 v190, v128, v110
	v_fmac_f32_e32 v191, v129, v110
	v_fmac_f32_e32 v192, v144, v110
	v_fmac_f32_e32 v193, v145, v110
	v_fmac_f32_e32 v190, v130, v111
	v_fmac_f32_e32 v191, v131, v111
	v_fmac_f32_e32 v192, v146, v111
	v_fmac_f32_e32 v193, v147, v111
	v_fmac_f32_e32 v190, v132, v112
	v_fmac_f32_e32 v191, v133, v112
	v_fmac_f32_e32 v192, v148, v112
	v_fmac_f32_e32 v193, v149, v112
	v_fmac_f32_e32 v190, v134, v113
	v_fmac_f32_e32 v191, v135, v113
	v_fmac_f32_e32 v192, v150, v113
	v_fmac_f32_e32 v193, v151, v113
	v_fmac_f32_e32 v190, v136, v114
	v_fmac_f32_e32 v191, v137, v114
	v_fmac_f32_e32 v192, v152, v114
	v_fmac_f32_e32 v193, v153, v114
	v_fmac_f32_e32 v190, v138, v115
	v_fmac_f32_e32 v191, v139, v115
	v_fmac_f32_e32 v192, v154, v115
	v_fmac_f32_e32 v193, v155, v115
	s_waitcnt vmcnt(13)
	v_and_b32_e32 v124, s6, v56
	v_and_b32_e32 v126, s7, v56
	v_and_b32_e32 v128, s42, v56
	v_lshrrev_b32_e32 v130, 24, v56
	v_and_b32_e32 v132, s6, v57
	v_and_b32_e32 v134, s7, v57
	v_and_b32_e32 v136, s42, v57
	v_lshrrev_b32_e32 v138, 24, v57
	v_and_b32_e32 v125, s6, v58
	v_and_b32_e32 v127, s7, v58
	v_and_b32_e32 v129, s42, v58
	v_lshrrev_b32_e32 v131, 24, v58
	v_and_b32_e32 v133, s6, v59
	v_and_b32_e32 v135, s7, v59
	v_and_b32_e32 v137, s42, v59
	v_lshrrev_b32_e32 v139, 24, v59
	v_and_b32_e32 v140, s6, v60
	v_and_b32_e32 v142, s7, v60
	v_and_b32_e32 v144, s42, v60
	v_lshrrev_b32_e32 v146, 24, v60
	v_and_b32_e32 v148, s6, v61
	v_and_b32_e32 v150, s7, v61
	v_and_b32_e32 v152, s42, v61
	v_lshrrev_b32_e32 v154, 24, v61
	v_and_b32_e32 v141, s6, v62
	v_and_b32_e32 v143, s7, v62
	v_and_b32_e32 v145, s42, v62
	v_lshrrev_b32_e32 v147, 24, v62
	v_and_b32_e32 v149, s6, v63
	v_and_b32_e32 v151, s7, v63
	v_and_b32_e32 v153, s42, v63
	v_lshrrev_b32_e32 v155, 24, v63
	v_mul_f32_e32 v194, v124, v108
	v_mul_f32_e32 v195, v125, v108
	v_mul_f32_e32 v196, v140, v108
	v_mul_f32_e32 v197, v141, v108
	v_fmac_f32_e32 v194, v126, v109
	v_fmac_f32_e32 v195, v127, v109
	v_fmac_f32_e32 v196, v142, v109
	v_fmac_f32_e32 v197, v143, v109
	v_fmac_f32_e32 v194, v128, v110
	v_fmac_f32_e32 v195, v129, v110
	v_fmac_f32_e32 v196, v144, v110
	v_fmac_f32_e32 v197, v145, v110
	v_fmac_f32_e32 v194, v130, v111
	v_fmac_f32_e32 v195, v131, v111
	v_fmac_f32_e32 v196, v146, v111
	v_fmac_f32_e32 v197, v147, v111
	v_fmac_f32_e32 v194, v132, v112
	v_fmac_f32_e32 v195, v133, v112
	v_fmac_f32_e32 v196, v148, v112
	v_fmac_f32_e32 v197, v149, v112
	v_fmac_f32_e32 v194, v134, v113
	v_fmac_f32_e32 v195, v135, v113
	v_fmac_f32_e32 v196, v150, v113
	v_fmac_f32_e32 v197, v151, v113
	v_fmac_f32_e32 v194, v136, v114
	v_fmac_f32_e32 v195, v137, v114
	v_fmac_f32_e32 v196, v152, v114
	v_fmac_f32_e32 v197, v153, v114
	v_fmac_f32_e32 v194, v138, v115
	v_fmac_f32_e32 v195, v139, v115
	v_fmac_f32_e32 v196, v154, v115
	v_fmac_f32_e32 v197, v155, v115
	s_waitcnt vmcnt(9)
	v_and_b32_e32 v124, s6, v64
	v_and_b32_e32 v126, s7, v64
	v_and_b32_e32 v128, s42, v64
	v_lshrrev_b32_e32 v130, 24, v64
	v_and_b32_e32 v132, s6, v65
	v_and_b32_e32 v134, s7, v65
	v_and_b32_e32 v136, s42, v65
	v_lshrrev_b32_e32 v138, 24, v65
	v_and_b32_e32 v125, s6, v66
	v_and_b32_e32 v127, s7, v66
	v_and_b32_e32 v129, s42, v66
	v_lshrrev_b32_e32 v131, 24, v66
	v_and_b32_e32 v133, s6, v67
	v_and_b32_e32 v135, s7, v67
	v_and_b32_e32 v137, s42, v67
	v_lshrrev_b32_e32 v139, 24, v67
	v_and_b32_e32 v140, s6, v68
	v_and_b32_e32 v142, s7, v68
	v_and_b32_e32 v144, s42, v68
	v_lshrrev_b32_e32 v146, 24, v68
	v_and_b32_e32 v148, s6, v69
	v_and_b32_e32 v150, s7, v69
	v_and_b32_e32 v152, s42, v69
	v_lshrrev_b32_e32 v154, 24, v69
	v_and_b32_e32 v141, s6, v70
	v_and_b32_e32 v143, s7, v70
	v_and_b32_e32 v145, s42, v70
	v_lshrrev_b32_e32 v147, 24, v70
	v_and_b32_e32 v149, s6, v71
	v_and_b32_e32 v151, s7, v71
	v_and_b32_e32 v153, s42, v71
	v_lshrrev_b32_e32 v155, 24, v71
	v_mul_f32_e32 v198, v124, v108
	v_mul_f32_e32 v199, v125, v108
	v_mul_f32_e32 v200, v140, v108
	v_mul_f32_e32 v201, v141, v108
	v_fmac_f32_e32 v198, v126, v109
	v_fmac_f32_e32 v199, v127, v109
	v_fmac_f32_e32 v200, v142, v109
	v_fmac_f32_e32 v201, v143, v109
	v_fmac_f32_e32 v198, v128, v110
	v_fmac_f32_e32 v199, v129, v110
	v_fmac_f32_e32 v200, v144, v110
	v_fmac_f32_e32 v201, v145, v110
	v_fmac_f32_e32 v198, v130, v111
	v_fmac_f32_e32 v199, v131, v111
	v_fmac_f32_e32 v200, v146, v111
	v_fmac_f32_e32 v201, v147, v111
	v_fmac_f32_e32 v198, v132, v112
	v_fmac_f32_e32 v199, v133, v112
	v_fmac_f32_e32 v200, v148, v112
	v_fmac_f32_e32 v201, v149, v112
	v_fmac_f32_e32 v198, v134, v113
	v_fmac_f32_e32 v199, v135, v113
	v_fmac_f32_e32 v200, v150, v113
	v_fmac_f32_e32 v201, v151, v113
	v_fmac_f32_e32 v198, v136, v114
	v_fmac_f32_e32 v199, v137, v114
	v_fmac_f32_e32 v200, v152, v114
	v_fmac_f32_e32 v201, v153, v114
	v_fmac_f32_e32 v198, v138, v115
	v_fmac_f32_e32 v199, v139, v115
	v_fmac_f32_e32 v200, v154, v115
	v_fmac_f32_e32 v201, v155, v115
	s_waitcnt vmcnt(5)
	v_and_b32_e32 v124, s6, v72
	v_and_b32_e32 v126, s7, v72
	v_and_b32_e32 v128, s42, v72
	v_lshrrev_b32_e32 v130, 24, v72
	v_and_b32_e32 v132, s6, v73
	v_and_b32_e32 v134, s7, v73
	v_and_b32_e32 v136, s42, v73
	v_lshrrev_b32_e32 v138, 24, v73
	v_and_b32_e32 v125, s6, v74
	v_and_b32_e32 v127, s7, v74
	v_and_b32_e32 v129, s42, v74
	v_lshrrev_b32_e32 v131, 24, v74
	v_and_b32_e32 v133, s6, v75
	v_and_b32_e32 v135, s7, v75
	v_and_b32_e32 v137, s42, v75
	v_lshrrev_b32_e32 v139, 24, v75
	v_and_b32_e32 v140, s6, v76
	v_and_b32_e32 v142, s7, v76
	v_and_b32_e32 v144, s42, v76
	v_lshrrev_b32_e32 v146, 24, v76
	v_and_b32_e32 v148, s6, v77
	v_and_b32_e32 v150, s7, v77
	v_and_b32_e32 v152, s42, v77
	v_lshrrev_b32_e32 v154, 24, v77
	v_and_b32_e32 v141, s6, v78
	v_and_b32_e32 v143, s7, v78
	v_and_b32_e32 v145, s42, v78
	v_lshrrev_b32_e32 v147, 24, v78
	v_and_b32_e32 v149, s6, v79
	v_and_b32_e32 v151, s7, v79
	v_and_b32_e32 v153, s42, v79
	v_lshrrev_b32_e32 v155, 24, v79
	v_mul_f32_e32 v202, v124, v108
	v_mul_f32_e32 v203, v125, v108
	v_mul_f32_e32 v204, v140, v108
	v_mul_f32_e32 v205, v141, v108
	v_fmac_f32_e32 v202, v126, v109
	v_fmac_f32_e32 v203, v127, v109
	v_fmac_f32_e32 v204, v142, v109
	v_fmac_f32_e32 v205, v143, v109
	v_fmac_f32_e32 v202, v128, v110
	v_fmac_f32_e32 v203, v129, v110
	v_fmac_f32_e32 v204, v144, v110
	v_fmac_f32_e32 v205, v145, v110
	v_fmac_f32_e32 v202, v130, v111
	v_fmac_f32_e32 v203, v131, v111
	v_fmac_f32_e32 v204, v146, v111
	v_fmac_f32_e32 v205, v147, v111
	v_fmac_f32_e32 v202, v132, v112
	v_fmac_f32_e32 v203, v133, v112
	v_fmac_f32_e32 v204, v148, v112
	v_fmac_f32_e32 v205, v149, v112
	v_fmac_f32_e32 v202, v134, v113
	v_fmac_f32_e32 v203, v135, v113
	v_fmac_f32_e32 v204, v150, v113
	v_fmac_f32_e32 v205, v151, v113
	v_fmac_f32_e32 v202, v136, v114
	v_fmac_f32_e32 v203, v137, v114
	v_fmac_f32_e32 v204, v152, v114
	v_fmac_f32_e32 v205, v153, v114
	v_fmac_f32_e32 v202, v138, v115
	v_fmac_f32_e32 v203, v139, v115
	v_fmac_f32_e32 v204, v154, v115
	v_fmac_f32_e32 v205, v155, v115
	s_waitcnt vmcnt(1)
	v_and_b32_e32 v124, s6, v80
	v_and_b32_e32 v126, s7, v80
	v_and_b32_e32 v128, s42, v80
	v_lshrrev_b32_e32 v130, 24, v80
	v_and_b32_e32 v132, s6, v81
	v_and_b32_e32 v134, s7, v81
	v_and_b32_e32 v136, s42, v81
	v_lshrrev_b32_e32 v138, 24, v81
	v_and_b32_e32 v125, s6, v82
	v_and_b32_e32 v127, s7, v82
	v_and_b32_e32 v129, s42, v82
	v_lshrrev_b32_e32 v131, 24, v82
	v_and_b32_e32 v133, s6, v83
	v_and_b32_e32 v135, s7, v83
	v_and_b32_e32 v137, s42, v83
	v_lshrrev_b32_e32 v139, 24, v83
	v_and_b32_e32 v140, s6, v84
	v_and_b32_e32 v142, s7, v84
	v_and_b32_e32 v144, s42, v84
	v_lshrrev_b32_e32 v146, 24, v84
	v_and_b32_e32 v148, s6, v85
	v_and_b32_e32 v150, s7, v85
	v_and_b32_e32 v152, s42, v85
	v_lshrrev_b32_e32 v154, 24, v85
	v_and_b32_e32 v141, s6, v86
	v_and_b32_e32 v143, s7, v86
	v_and_b32_e32 v145, s42, v86
	v_lshrrev_b32_e32 v147, 24, v86
	v_and_b32_e32 v149, s6, v87
	v_and_b32_e32 v151, s7, v87
	v_and_b32_e32 v153, s42, v87
	v_lshrrev_b32_e32 v155, 24, v87
	v_mul_f32_e32 v206, v124, v108
	v_mul_f32_e32 v207, v125, v108
	v_mul_f32_e32 v208, v140, v108
	v_mul_f32_e32 v209, v141, v108
	v_fmac_f32_e32 v206, v126, v109
	v_fmac_f32_e32 v207, v127, v109
	v_fmac_f32_e32 v208, v142, v109
	v_fmac_f32_e32 v209, v143, v109
	v_fmac_f32_e32 v206, v128, v110
	v_fmac_f32_e32 v207, v129, v110
	v_fmac_f32_e32 v208, v144, v110
	v_fmac_f32_e32 v209, v145, v110
	v_fmac_f32_e32 v206, v130, v111
	v_fmac_f32_e32 v207, v131, v111
	v_fmac_f32_e32 v208, v146, v111
	v_fmac_f32_e32 v209, v147, v111
	v_fmac_f32_e32 v206, v132, v112
	v_fmac_f32_e32 v207, v133, v112
	v_fmac_f32_e32 v208, v148, v112
	v_fmac_f32_e32 v209, v149, v112
	v_fmac_f32_e32 v206, v134, v113
	v_fmac_f32_e32 v207, v135, v113
	v_fmac_f32_e32 v208, v150, v113
	v_fmac_f32_e32 v209, v151, v113
	v_fmac_f32_e32 v206, v136, v114
	v_fmac_f32_e32 v207, v137, v114
	v_fmac_f32_e32 v208, v152, v114
	v_fmac_f32_e32 v209, v153, v114
	v_fmac_f32_e32 v206, v138, v115
	v_fmac_f32_e32 v207, v139, v115
	v_fmac_f32_e32 v208, v154, v115
	v_fmac_f32_e32 v209, v155, v115
	s_waitcnt lgkmcnt(0)
	s_load_dwordx16 s[84:99], s[38:39], 0x40 glc
	s_lshl_b32 s30, s68, 12
	s_add_u32 s28, s26, s30
	s_addc_u32 s29, s27, 0
	global_load_dwordx2 v[24:25], v162, s[28:29]
	s_lshl_b32 s30, s69, 12
	s_add_u32 s28, s26, s30
	s_addc_u32 s29, s27, 0
	global_load_dwordx2 v[26:27], v162, s[28:29]
	s_lshl_b32 s30, s70, 12
	s_add_u32 s28, s26, s30
	s_addc_u32 s29, s27, 0
	global_load_dwordx2 v[28:29], v162, s[28:29]
	s_lshl_b32 s30, s71, 12
	s_add_u32 s28, s26, s30
	s_addc_u32 s29, s27, 0
	global_load_dwordx2 v[30:31], v162, s[28:29]
	s_lshl_b32 s30, s72, 12
	s_add_u32 s28, s26, s30
	s_addc_u32 s29, s27, 0
	global_load_dwordx2 v[32:33], v162, s[28:29]
	s_lshl_b32 s30, s73, 12
	s_add_u32 s28, s26, s30
	s_addc_u32 s29, s27, 0
	global_load_dwordx2 v[34:35], v162, s[28:29]
	s_lshl_b32 s30, s74, 12
	s_add_u32 s28, s26, s30
	s_addc_u32 s29, s27, 0
	global_load_dwordx2 v[36:37], v162, s[28:29]
	s_lshl_b32 s30, s75, 12
	s_add_u32 s28, s26, s30
	s_addc_u32 s29, s27, 0
	global_load_dwordx2 v[38:39], v162, s[28:29]
	s_lshl_b32 s30, s76, 12
	s_add_u32 s28, s26, s30
	s_addc_u32 s29, s27, 0
	global_load_dwordx2 v[40:41], v162, s[28:29]
	s_lshl_b32 s30, s77, 12
	s_add_u32 s28, s26, s30
	s_addc_u32 s29, s27, 0
	global_load_dwordx2 v[42:43], v162, s[28:29]
	s_lshl_b32 s30, s78, 12
	s_add_u32 s28, s26, s30
	s_addc_u32 s29, s27, 0
	global_load_dwordx2 v[44:45], v162, s[28:29]
	s_lshl_b32 s30, s79, 12
	s_add_u32 s28, s26, s30
	s_addc_u32 s29, s27, 0
	global_load_dwordx2 v[46:47], v162, s[28:29]
	s_lshl_b32 s30, s80, 12
	s_add_u32 s28, s26, s30
	s_addc_u32 s29, s27, 0
	global_load_dwordx2 v[48:49], v162, s[28:29]
	s_lshl_b32 s30, s81, 12
	s_add_u32 s28, s26, s30
	s_addc_u32 s29, s27, 0
	global_load_dwordx2 v[50:51], v162, s[28:29]
	s_lshl_b32 s30, s82, 12
	s_add_u32 s28, s26, s30
	s_addc_u32 s29, s27, 0
	global_load_dwordx2 v[52:53], v162, s[28:29]
	s_lshl_b32 s30, s83, 12
	s_add_u32 s28, s26, s30
	s_addc_u32 s29, s27, 0
	global_load_dwordx2 v[54:55], v162, s[28:29]
	s_waitcnt lgkmcnt(0)
	s_load_dwordx16 s[68:83], s[38:39], 0x80 glc
	s_lshl_b32 s30, s84, 12
	s_add_u32 s28, s26, s30
	s_addc_u32 s29, s27, 0
	global_load_dwordx2 v[56:57], v162, s[28:29]
	s_lshl_b32 s30, s85, 12
	s_add_u32 s28, s26, s30
	s_addc_u32 s29, s27, 0
	global_load_dwordx2 v[58:59], v162, s[28:29]
	s_lshl_b32 s30, s86, 12
	s_add_u32 s28, s26, s30
	s_addc_u32 s29, s27, 0
	global_load_dwordx2 v[60:61], v162, s[28:29]
	s_lshl_b32 s30, s87, 12
	s_add_u32 s28, s26, s30
	s_addc_u32 s29, s27, 0
	global_load_dwordx2 v[62:63], v162, s[28:29]
	s_lshl_b32 s30, s88, 12
	s_add_u32 s28, s26, s30
	s_addc_u32 s29, s27, 0
	global_load_dwordx2 v[64:65], v162, s[28:29]
	s_lshl_b32 s30, s89, 12
	s_add_u32 s28, s26, s30
	s_addc_u32 s29, s27, 0
	global_load_dwordx2 v[66:67], v162, s[28:29]
	s_lshl_b32 s30, s90, 12
	s_add_u32 s28, s26, s30
	s_addc_u32 s29, s27, 0
	global_load_dwordx2 v[68:69], v162, s[28:29]
	s_lshl_b32 s30, s91, 12
	s_add_u32 s28, s26, s30
	s_addc_u32 s29, s27, 0
	global_load_dwordx2 v[70:71], v162, s[28:29]
	s_lshl_b32 s30, s92, 12
	s_add_u32 s28, s26, s30
	s_addc_u32 s29, s27, 0
	global_load_dwordx2 v[72:73], v162, s[28:29]
	s_lshl_b32 s30, s93, 12
	s_add_u32 s28, s26, s30
	s_addc_u32 s29, s27, 0
	global_load_dwordx2 v[74:75], v162, s[28:29]
	s_lshl_b32 s30, s94, 12
	s_add_u32 s28, s26, s30
	s_addc_u32 s29, s27, 0
	global_load_dwordx2 v[76:77], v162, s[28:29]
	s_lshl_b32 s30, s95, 12
	s_add_u32 s28, s26, s30
	s_addc_u32 s29, s27, 0
	global_load_dwordx2 v[78:79], v162, s[28:29]
	s_lshl_b32 s30, s96, 12
	s_add_u32 s28, s26, s30
	s_addc_u32 s29, s27, 0
	global_load_dwordx2 v[80:81], v162, s[28:29]
	s_lshl_b32 s30, s97, 12
	s_add_u32 s28, s26, s30
	s_addc_u32 s29, s27, 0
	global_load_dwordx2 v[82:83], v162, s[28:29]
	s_lshl_b32 s30, s98, 12
	s_add_u32 s28, s26, s30
	s_addc_u32 s29, s27, 0
	global_load_dwordx2 v[84:85], v162, s[28:29]
	s_lshl_b32 s30, s99, 12
	s_add_u32 s28, s26, s30
	s_addc_u32 s29, s27, 0
	global_load_dwordx2 v[86:87], v162, s[28:29]
	v_permlane32_swap_b32_e32 v178, v194
	v_permlane32_swap_b32_e32 v179, v195
	v_permlane32_swap_b32_e32 v180, v196
	v_permlane32_swap_b32_e32 v181, v197
	v_permlane32_swap_b32_e32 v182, v198
	v_permlane32_swap_b32_e32 v183, v199
	v_permlane32_swap_b32_e32 v184, v200
	v_permlane32_swap_b32_e32 v185, v201
	v_permlane32_swap_b32_e32 v186, v202
	v_permlane32_swap_b32_e32 v187, v203
	v_permlane32_swap_b32_e32 v188, v204
	v_permlane32_swap_b32_e32 v189, v205
	v_permlane32_swap_b32_e32 v190, v206
	v_permlane32_swap_b32_e32 v191, v207
	v_permlane32_swap_b32_e32 v192, v208
	v_permlane32_swap_b32_e32 v193, v209
	v_add_f32_e32 v178, v178, v194
	v_add_f32_e32 v179, v179, v195
	v_add_f32_e32 v180, v180, v196
	v_add_f32_e32 v181, v181, v197
	v_add_f32_e32 v182, v182, v198
	v_add_f32_e32 v183, v183, v199
	v_add_f32_e32 v184, v184, v200
	v_add_f32_e32 v185, v185, v201
	v_add_f32_e32 v186, v186, v202
	v_add_f32_e32 v187, v187, v203
	v_add_f32_e32 v188, v188, v204
	v_add_f32_e32 v189, v189, v205
	v_add_f32_e32 v190, v190, v206
	v_add_f32_e32 v191, v191, v207
	v_add_f32_e32 v192, v192, v208
	v_add_f32_e32 v193, v193, v209
	v_permlane16_swap_b32_e32 v178, v186
	v_permlane16_swap_b32_e32 v179, v187
	v_permlane16_swap_b32_e32 v180, v188
	v_permlane16_swap_b32_e32 v181, v189
	v_permlane16_swap_b32_e32 v182, v190
	v_permlane16_swap_b32_e32 v183, v191
	v_permlane16_swap_b32_e32 v184, v192
	v_permlane16_swap_b32_e32 v185, v193
	v_add_f32_e32 v178, v178, v186
	v_add_f32_e32 v179, v179, v187
	v_add_f32_e32 v180, v180, v188
	v_add_f32_e32 v181, v181, v189
	v_add_f32_e32 v182, v182, v190
	v_add_f32_e32 v183, v183, v191
	v_add_f32_e32 v184, v184, v192
	v_add_f32_e32 v185, v185, v193
	v_cndmask_b32_e64 v2, v178, v182, s[8:9]
	v_cndmask_b32_e64 v3, v179, v183, s[8:9]
	v_cndmask_b32_e64 v4, v180, v184, s[8:9]
	v_cndmask_b32_e64 v5, v181, v185, s[8:9]
	v_cndmask_b32_e64 v6, v182, v178, s[8:9]
	v_cndmask_b32_e64 v7, v183, v179, s[8:9]
	v_cndmask_b32_e64 v8, v184, v180, s[8:9]
	v_cndmask_b32_e64 v9, v185, v181, s[8:9]
	v_add_f32_dpp v6, v2, v6 row_ror:8 row_mask:0xf bank_mask:0xf
	v_add_f32_dpp v7, v3, v7 row_ror:8 row_mask:0xf bank_mask:0xf
	v_add_f32_dpp v8, v4, v8 row_ror:8 row_mask:0xf bank_mask:0xf
	v_add_f32_dpp v9, v5, v9 row_ror:8 row_mask:0xf bank_mask:0xf
	v_cndmask_b32_e64 v2, v6, v8, s[10:11]
	v_cndmask_b32_e64 v3, v7, v9, s[10:11]
	v_cndmask_b32_e64 v4, v8, v6, s[10:11]
	v_cndmask_b32_e64 v5, v9, v7, s[10:11]
	v_add_f32_dpp v4, v2, v4 row_half_mirror row_mask:0xf bank_mask:0xf
	v_add_f32_dpp v5, v3, v5 row_half_mirror row_mask:0xf bank_mask:0xf
	v_cndmask_b32_e64 v2, v4, v5, s[14:15]
	v_cndmask_b32_e64 v3, v5, v4, s[14:15]
	s_nop 0
	v_add_f32_dpp v3, v2, v3 quad_perm:[2,3,0,1] row_mask:0xf bank_mask:0xf
	s_nop 1
	v_add_f32_dpp v11, v3, v3 quad_perm:[1,0,3,2] row_mask:0xf bank_mask:0xf
	v_mul_f32_e32 v11, 0x58000000, v11
	s_mov_b64 exec, s[2:3]
	global_store_dword v[22:23], v11, off offset:384
	s_mov_b64 exec, -1
	s_add_i32 s16, s16, 1
	s_cmp_lt_i32 s16, s17
	s_cbranch_scc1 .Lpa_tok
	s_waitcnt vmcnt(0)
	s_waitcnt vmcnt(0)
	v_cmp_eq_u32_e32 vcc, 0, v0
	s_waitcnt vmcnt(0) lgkmcnt(0)
	s_barrier
	s_and_saveexec_b64 s[2:3], vcc
	s_cbranch_execz .Lgbb_1444
	v_readlane_b32 s4, v237, 5
	s_waitcnt vmcnt(0) expcnt(0) lgkmcnt(0)
	s_nop 0
	v_mov_b32_e32 v1, s4
	ds_read_b32 v3, v1
	ds_read_b32 v1, v1 offset:4
	s_waitcnt lgkmcnt(1)
	v_cmp_ne_u32_e32 vcc, 0, v3
	s_branch .Lgbb_1412
	v_readlane_b32 s4, v237, 2
	v_readlane_b32 s5, v237, 3
	s_load_dwordx2 s[8:9], s[6:7], 0x4
	s_lshl_b64 s[4:5], s[4:5], 2
	v_readlane_b32 s6, v237, 0
	s_add_u32 s4, s6, s4
	v_readlane_b32 s6, v237, 1
	s_addc_u32 s5, s6, s5
	s_add_u32 s6, s4, 0x1000
	s_addc_u32 s7, s5, 0
	s_waitcnt lgkmcnt(0)
	s_mul_i32 s20, s8, s38
	s_add_u32 s8, s4, 0x1100
	s_mul_i32 s20, s20, s9
	s_addc_u32 s9, s5, 0
	s_add_u32 s10, s4, 0x1200
	s_addc_u32 s11, s5, 0
	s_add_u32 s12, s4, 0x1300
	s_addc_u32 s13, s5, 0
	s_mov_b32 s21, 1
	v_mov_b32_e32 v17, 0
	s_branch .Lgbb_1400

.Lgbb_1444:
	s_or_b64 exec, exec, s[2:3]
	s_waitcnt lgkmcnt(0)
	s_barrier
	s_mov_b64 exec, -1
	v_and_b32_e32 v1, 63, v0
	v_readfirstlane_b32 s16, v0
	s_load_dwordx2 s[12:13], s[0:1], 0xc0
	s_lshr_b32 s16, s16, 6
	s_and_b32 s18, s33, 7
	s_lshr_b32 s19, s33, 3
	s_lshl_b32 s19, s19, 8
	s_lshl_b32 s16, s16, 5
	s_add_i32 s16, s16, s19
	s_add_i32 s17, s16, 32
	s_add_i32 s24, s17, -1
	s_lshl_b32 s19, s18, 9
	v_lshl_add_u32 v162, v1, 3, s19
	v_mov_b32_e32 v163, 0
	s_mov_b32 s31, 0
	v_mov_b32_e32 v4, v1
	v_mov_b32_e32 v5, 0
	s_mov_b32 s101, 0
	s_mov_b32 s100, 0x400000
	s_mov_b32 s41, 0x378e98ab
	s_mov_b32 s42, 0x3b7cd369
	s_mov_b32 s43, 0xbcc618b2
	s_mov_b32 s44, 0x3dda74e4
	s_mov_b32 s45, 0x3f228afd
	s_mov_b32 s46, 0x3e03c728
	s_mov_b32 s47, 0xbfb8aa3b
	s_mov_b32 s48, 0x42ce8ed0
	s_mov_b32 s49, 0xc2b17218
	s_mov_b32 s50, 0x7fffffff
	v_mov_b32_e32 v97, 0x43000000
	v_mov_b32_e32 v250, 0x3ba10414
	v_mov_b32_e32 v251, 0xb9c68948
	v_mov_b32_e32 v252, 0x7f800000
	s_load_dwordx2 s[4:5], s[0:1], 0xb8
	s_waitcnt lgkmcnt(0)
	s_add_u32 s26, s12, 0x17c00000
	s_addc_u32 s27, s13, 0
	s_add_u32 s20, s12, 0x100000
	s_addc_u32 s21, s13, 0
	v_lshl_add_u64 v[172:173], v[162:163], 1, s[20:21]
	s_add_u32 s20, s12, 0x4da00000
	s_addc_u32 s21, s13, 0
	v_lshl_add_u64 v[174:175], v[4:5], 2, s[20:21]
	s_add_u32 s20, s12, 0x4de00000
	s_addc_u32 s21, s13, 0
	v_lshl_add_u64 v[176:177], v[4:5], 2, s[20:21]
	s_add_u32 s20, s12, 0x23c00000
	s_addc_u32 s21, s13, 0
	v_lshl_add_u64 v[210:211], v[4:5], 2, s[20:21]
	s_add_u32 s20, s12, 0x25c00000
	s_addc_u32 s21, s13, 0
	v_and_b32_e32 v6, 7, v1
	v_mov_b32_e32 v7, 0
	v_lshlrev_b32_e32 v6, 20, v6
	v_lshl_add_u64 v[212:213], v[6:7], 0, s[20:21]
	v_lshl_add_u64 v[214:215], v[162:163], 2, s[4:5]
	s_add_u32 s66, s12, 0x1fe00000
	s_addc_u32 s67, s13, 0
	s_add_u32 s64, s12, 0x38d80000
	s_addc_u32 s65, s13, 0
	s_add_u32 s60, s12, 0x38d90000
	s_addc_u32 s61, s13, 0
	s_lshl_b32 s19, s18, 20
	s_add_u32 s62, s12, 0x26c00000
	s_addc_u32 s63, s13, 0
	s_add_u32 s62, s62, s19
	s_addc_u32 s63, s63, 0
	v_mov_b32_e32 v19, 0
	s_mov_b32 s2, 0x55555555
	s_mov_b32 s3, 0x55555555
	s_mov_b32 s6, 0xff
	s_mov_b32 s7, 0xff00
	s_mov_b32 s8, 0xff0000
	s_lshl_b32 s30, s16, 13
	v_lshl_add_u64 v[160:161], v[172:173], 0, s[30:31]
	global_load_dwordx4 v[116:119], v[160:161], off
	s_lshl_b32 s30, s16, 9
	v_lshl_add_u64 v[160:161], v[174:175], 0, s[30:31]
	global_load_dword v122, v[160:161], off
	global_load_dword v123, v[160:161], off offset:256
	v_lshl_add_u64 v[160:161], v[176:177], 0, s[30:31]
	global_load_dword v216, v[160:161], off
	global_load_dword v217, v[160:161], off offset:256
	v_lshl_add_u64 v[160:161], v[210:211], 0, s[30:31]
	global_load_dword v218, v[160:161], off
	global_load_dword v226, v[160:161], off offset:256
	v_lshl_add_u64 v[160:161], v[160:161], 0, s[100:101]
	global_load_dword v219, v[160:161], off
	global_load_dword v227, v[160:161], off offset:256
	v_lshl_add_u64 v[160:161], v[160:161], 0, s[100:101]
	global_load_dword v220, v[160:161], off
	global_load_dword v228, v[160:161], off offset:256
	v_lshl_add_u64 v[160:161], v[160:161], 0, s[100:101]
	global_load_dword v221, v[160:161], off
	global_load_dword v229, v[160:161], off offset:256
	v_lshl_add_u64 v[160:161], v[160:161], 0, s[100:101]
	global_load_dword v222, v[160:161], off
	global_load_dword v230, v[160:161], off offset:256
	v_lshl_add_u64 v[160:161], v[160:161], 0, s[100:101]
	global_load_dword v223, v[160:161], off
	global_load_dword v231, v[160:161], off offset:256
	v_lshl_add_u64 v[160:161], v[160:161], 0, s[100:101]
	global_load_dword v224, v[160:161], off
	global_load_dword v232, v[160:161], off offset:256
	v_lshl_add_u64 v[160:161], v[160:161], 0, s[100:101]
	global_load_dword v225, v[160:161], off
	global_load_dword v233, v[160:161], off offset:256
	s_lshl_b32 s30, s16, 7
	v_lshl_add_u64 v[160:161], v[212:213], 0, s[30:31]
	global_load_dword v234, v[160:161], off
	s_lshl_b32 s30, s16, 2
	s_add_u32 s28, s66, s30
	s_addc_u32 s29, s67, 0
	global_load_dword v235, v19, s[28:29]
	s_waitcnt vmcnt(0)
	v_lshlrev_b32_e32 v16, 2, v122
	v_lshlrev_b32_e32 v17, 2, v123
	global_load_dword v238, v16, s[64:65]
	global_load_dword v240, v16, s[60:61]
	global_load_dword v239, v17, s[64:65]
	global_load_dword v241, v17, s[60:61]
	s_waitcnt vmcnt(0)
	s_add_u32 s22, s12, 0x4da00000
	s_addc_u32 s23, s13, 0
	s_lshl_b32 s30, s16, 9
	s_add_u32 s36, s22, s30
	s_addc_u32 s37, s23, 0
	s_load_dwordx16 s[68:83], s[36:37], 0x0 glc
	s_load_dwordx16 s[84:99], s[36:37], 0x40 glc
	s_waitcnt lgkmcnt(0)
	s_lshl_b32 s30, s68, 12
	s_add_u32 s28, s26, s30
	s_addc_u32 s29, s27, 0
	global_load_dwordx2 v[24:25], v162, s[28:29]
	s_lshl_b32 s30, s69, 12
	s_add_u32 s28, s26, s30
	s_addc_u32 s29, s27, 0
	global_load_dwordx2 v[26:27], v162, s[28:29]
	s_lshl_b32 s30, s70, 12
	s_add_u32 s28, s26, s30
	s_addc_u32 s29, s27, 0
	global_load_dwordx2 v[28:29], v162, s[28:29]
	s_lshl_b32 s30, s71, 12
	s_add_u32 s28, s26, s30
	s_addc_u32 s29, s27, 0
	global_load_dwordx2 v[30:31], v162, s[28:29]
	s_lshl_b32 s30, s72, 12
	s_add_u32 s28, s26, s30
	s_addc_u32 s29, s27, 0
	global_load_dwordx2 v[32:33], v162, s[28:29]
	s_lshl_b32 s30, s73, 12
	s_add_u32 s28, s26, s30
	s_addc_u32 s29, s27, 0
	global_load_dwordx2 v[34:35], v162, s[28:29]
	s_lshl_b32 s30, s74, 12
	s_add_u32 s28, s26, s30
	s_addc_u32 s29, s27, 0
	global_load_dwordx2 v[36:37], v162, s[28:29]
	s_lshl_b32 s30, s75, 12
	s_add_u32 s28, s26, s30
	s_addc_u32 s29, s27, 0
	global_load_dwordx2 v[38:39], v162, s[28:29]
	s_lshl_b32 s30, s76, 12
	s_add_u32 s28, s26, s30
	s_addc_u32 s29, s27, 0
	global_load_dwordx2 v[40:41], v162, s[28:29]
	s_lshl_b32 s30, s77, 12
	s_add_u32 s28, s26, s30
	s_addc_u32 s29, s27, 0
	global_load_dwordx2 v[42:43], v162, s[28:29]
	s_lshl_b32 s30, s78, 12
	s_add_u32 s28, s26, s30
	s_addc_u32 s29, s27, 0
	global_load_dwordx2 v[44:45], v162, s[28:29]
	s_lshl_b32 s30, s79, 12
	s_add_u32 s28, s26, s30
	s_addc_u32 s29, s27, 0
	global_load_dwordx2 v[46:47], v162, s[28:29]
	s_lshl_b32 s30, s80, 12
	s_add_u32 s28, s26, s30
	s_addc_u32 s29, s27, 0
	global_load_dwordx2 v[48:49], v162, s[28:29]
	s_lshl_b32 s30, s81, 12
	s_add_u32 s28, s26, s30
	s_addc_u32 s29, s27, 0
	global_load_dwordx2 v[50:51], v162, s[28:29]
	s_lshl_b32 s30, s82, 12
	s_add_u32 s28, s26, s30
	s_addc_u32 s29, s27, 0
	global_load_dwordx2 v[52:53], v162, s[28:29]
	s_lshl_b32 s30, s83, 12
	s_add_u32 s28, s26, s30
	s_addc_u32 s29, s27, 0
	global_load_dwordx2 v[54:55], v162, s[28:29]
	s_lshl_b32 s30, s84, 12
	s_add_u32 s28, s26, s30
	s_addc_u32 s29, s27, 0
	global_load_dwordx2 v[56:57], v162, s[28:29]
	s_lshl_b32 s30, s85, 12
	s_add_u32 s28, s26, s30
	s_addc_u32 s29, s27, 0
	global_load_dwordx2 v[58:59], v162, s[28:29]
	s_lshl_b32 s30, s86, 12
	s_add_u32 s28, s26, s30
	s_addc_u32 s29, s27, 0
	global_load_dwordx2 v[60:61], v162, s[28:29]
	s_lshl_b32 s30, s87, 12
	s_add_u32 s28, s26, s30
	s_addc_u32 s29, s27, 0
	global_load_dwordx2 v[62:63], v162, s[28:29]
	s_lshl_b32 s30, s88, 12
	s_add_u32 s28, s26, s30
	s_addc_u32 s29, s27, 0
	global_load_dwordx2 v[64:65], v162, s[28:29]
	s_lshl_b32 s30, s89, 12
	s_add_u32 s28, s26, s30
	s_addc_u32 s29, s27, 0
	global_load_dwordx2 v[66:67], v162, s[28:29]
	s_lshl_b32 s30, s90, 12
	s_add_u32 s28, s26, s30
	s_addc_u32 s29, s27, 0
	global_load_dwordx2 v[68:69], v162, s[28:29]
	s_lshl_b32 s30, s91, 12
	s_add_u32 s28, s26, s30
	s_addc_u32 s29, s27, 0
	global_load_dwordx2 v[70:71], v162, s[28:29]
	s_lshl_b32 s30, s92, 12
	s_add_u32 s28, s26, s30
	s_addc_u32 s29, s27, 0
	global_load_dwordx2 v[72:73], v162, s[28:29]
	s_lshl_b32 s30, s93, 12
	s_add_u32 s28, s26, s30
	s_addc_u32 s29, s27, 0
	global_load_dwordx2 v[74:75], v162, s[28:29]
	s_lshl_b32 s30, s94, 12
	s_add_u32 s28, s26, s30
	s_addc_u32 s29, s27, 0
	global_load_dwordx2 v[76:77], v162, s[28:29]
	s_lshl_b32 s30, s95, 12
	s_add_u32 s28, s26, s30
	s_addc_u32 s29, s27, 0
	global_load_dwordx2 v[78:79], v162, s[28:29]
	s_lshl_b32 s30, s96, 12
	s_add_u32 s28, s26, s30
	s_addc_u32 s29, s27, 0
	global_load_dwordx2 v[80:81], v162, s[28:29]
	s_lshl_b32 s30, s97, 12
	s_add_u32 s28, s26, s30
	s_addc_u32 s29, s27, 0
	global_load_dwordx2 v[82:83], v162, s[28:29]
	s_lshl_b32 s30, s98, 12
	s_add_u32 s28, s26, s30
	s_addc_u32 s29, s27, 0
	global_load_dwordx2 v[84:85], v162, s[28:29]
	s_lshl_b32 s30, s99, 12
	s_add_u32 s28, s26, s30
	s_addc_u32 s29, s27, 0
	global_load_dwordx2 v[86:87], v162, s[28:29]
	s_load_dwordx16 s[68:83], s[36:37], 0x80 glc

.Lerfa1_1476:
	s_andn2_saveexec_b64 s[34:35], s[34:35]
	v_mul_f32_e32 v12, v11, v11
	v_fmamk_f32 v13, v12, 0xba1345e1, v250
	v_fmaak_f32 v13, v12, v13, 0xbcdac9b8
	v_fmaak_f32 v13, v12, v13, 0x3de703be
	v_fmaak_f32 v13, v12, v13, 0xbec09330
	v_fmaak_f32 v12, v12, v13, 0x3e0375d0
	v_fma_f32 v12, |v11|, v12, |v11|
	s_or_b64 exec, exec, s[34:35]
	v_bfi_b32 v11, s50, v12, v11
	v_mul_f32_e32 v10, 0.5, v10
	v_add_f32_e32 v11, 1.0, v11
	v_mul_f32_e32 v10, v10, v11
	v_mul_f32_e32 v10, v164, v10
	v_mul_f32_e32 v10, v249, v10
	v_mov_b32_e32 v247, v10
	v_add_f32_e32 v16, v246, v247
	s_nop 1
	v_add_f32_dpp v17, v16, v16 quad_perm:[1,0,3,2] row_mask:0xf bank_mask:0xf
	s_nop 1
	v_add_f32_dpp v16, v17, v17 quad_perm:[2,3,0,1] row_mask:0xf bank_mask:0xf
	s_nop 1
	v_add_f32_dpp v17, v16, v16 row_half_mirror row_mask:0xf bank_mask:0xf
	s_nop 1
	v_add_f32_dpp v16, v17, v17 row_ror:8 row_mask:0xf bank_mask:0xf
	v_mov_b32_e32 v17, v16
	s_nop 1
	v_permlane16_swap_b32_e32 v16, v17
	v_add_f32_e32 v16, v16, v17
	v_mov_b32_e32 v17, v16
	s_nop 1
	v_permlane32_swap_b32_e32 v16, v17
	v_add_f32_e32 v16, v16, v17
	v_mul_f32_e32 v248, 0xc3000000, v16
	v_mul_f32_e32 v246, 0x71800000, v246
	v_mul_f32_e32 v247, 0x71800000, v247
	v_mov_b32_e32 v242, v116
	v_mov_b32_e32 v243, v117
	v_mov_b32_e32 v244, v118
	v_mov_b32_e32 v245, v119
	v_mov_b32_e32 v120, v122
	v_mov_b32_e32 v121, v123
	s_lshl_b32 s30, s16, 14
	v_lshl_add_u64 v[20:21], v[214:215], 0, s[30:31]
	s_add_i32 s18, s16, 1
	s_min_i32 s18, s18, s24
	s_lshl_b32 s30, s16, 9
	s_add_u32 s36, s22, s30
	s_addc_u32 s37, s23, 0
	s_lshl_b32 s30, s18, 9
	s_add_u32 s38, s22, s30
	s_addc_u32 s39, s23, 0
	s_lshl_b32 s30, s18, 13
	v_lshl_add_u64 v[160:161], v[172:173], 0, s[30:31]
	global_load_dwordx4 v[116:119], v[160:161], off
	s_lshl_b32 s30, s18, 9
	v_lshl_add_u64 v[160:161], v[174:175], 0, s[30:31]
	global_load_dword v122, v[160:161], off
	global_load_dword v123, v[160:161], off offset:256
	v_lshl_add_u64 v[160:161], v[176:177], 0, s[30:31]
	global_load_dword v216, v[160:161], off
	global_load_dword v217, v[160:161], off offset:256
	v_lshl_add_u64 v[160:161], v[210:211], 0, s[30:31]
	global_load_dword v218, v[160:161], off
	global_load_dword v226, v[160:161], off offset:256
	v_lshl_add_u64 v[160:161], v[160:161], 0, s[100:101]
	global_load_dword v219, v[160:161], off
	global_load_dword v227, v[160:161], off offset:256
	v_lshl_add_u64 v[160:161], v[160:161], 0, s[100:101]
	global_load_dword v220, v[160:161], off
	global_load_dword v228, v[160:161], off offset:256
	v_lshl_add_u64 v[160:161], v[160:161], 0, s[100:101]
	global_load_dword v221, v[160:161], off
	global_load_dword v229, v[160:161], off offset:256
	v_lshl_add_u64 v[160:161], v[160:161], 0, s[100:101]
	global_load_dword v222, v[160:161], off
	global_load_dword v230, v[160:161], off offset:256
	v_lshl_add_u64 v[160:161], v[160:161], 0, s[100:101]
	global_load_dword v223, v[160:161], off
	global_load_dword v231, v[160:161], off offset:256
	v_lshl_add_u64 v[160:161], v[160:161], 0, s[100:101]
	global_load_dword v224, v[160:161], off
	global_load_dword v232, v[160:161], off offset:256
	v_lshl_add_u64 v[160:161], v[160:161], 0, s[100:101]
	global_load_dword v225, v[160:161], off
	global_load_dword v233, v[160:161], off offset:256
	s_lshl_b32 s30, s18, 7
	v_lshl_add_u64 v[160:161], v[212:213], 0, s[30:31]
	global_load_dword v234, v[160:161], off
	s_lshl_b32 s30, s18, 2
	s_add_u32 s28, s66, s30
	s_addc_u32 s29, s67, 0
	global_load_dword v235, v19, s[28:29]
	v_mov_b32_e32 v178, 0
	v_mov_b32_e32 v179, 0
	v_mov_b32_e32 v180, 0
	v_mov_b32_e32 v181, 0
	v_mov_b32_e32 v182, 0
	v_mov_b32_e32 v183, 0
	v_mov_b32_e32 v184, 0
	v_mov_b32_e32 v185, 0
	s_waitcnt vmcnt(51)
	v_readlane_b32 s25, v246, 0
	v_and_b32_e32 v124, s6, v24
	v_and_b32_e32 v125, s7, v24
	v_and_b32_e32 v126, s8, v24
	v_lshrrev_b32_e32 v127, 24, v24
	v_and_b32_e32 v128, s6, v25
	v_and_b32_e32 v129, s7, v25
	v_and_b32_e32 v130, s8, v25
	v_lshrrev_b32_e32 v131, 24, v25
	s_waitcnt lgkmcnt(0)
	s_load_dwordx16 s[84:99], s[36:37], 0xc0 glc
	s_lshl_b32 s30, s68, 12
	s_add_u32 s28, s26, s30
	s_addc_u32 s29, s27, 0
	global_load_dwordx2 v[24:25], v162, s[28:29]
	v_fmac_f32_e32 v178, s25, v124
	v_fmac_f32_e32 v179, s25, v125
	v_fmac_f32_e32 v180, s25, v126
	v_fmac_f32_e32 v181, s25, v127
	v_fmac_f32_e32 v182, s25, v128
	v_fmac_f32_e32 v183, s25, v129
	v_fmac_f32_e32 v184, s25, v130
	v_fmac_f32_e32 v185, s25, v131
	v_readlane_b32 s25, v246, 1
	v_and_b32_e32 v132, s6, v26
	v_and_b32_e32 v133, s7, v26
	v_and_b32_e32 v134, s8, v26
	v_lshrrev_b32_e32 v135, 24, v26
	v_and_b32_e32 v136, s6, v27
	v_and_b32_e32 v137, s7, v27
	v_and_b32_e32 v138, s8, v27
	v_lshrrev_b32_e32 v139, 24, v27
	s_lshl_b32 s30, s69, 12
	s_add_u32 s28, s26, s30
	s_addc_u32 s29, s27, 0
	global_load_dwordx2 v[26:27], v162, s[28:29]
	v_fmac_f32_e32 v178, s25, v132
	v_fmac_f32_e32 v179, s25, v133
	v_fmac_f32_e32 v180, s25, v134
	v_fmac_f32_e32 v181, s25, v135
	v_fmac_f32_e32 v182, s25, v136
	v_fmac_f32_e32 v183, s25, v137
	v_fmac_f32_e32 v184, s25, v138
	v_fmac_f32_e32 v185, s25, v139
	v_readlane_b32 s25, v246, 2
	v_and_b32_e32 v124, s6, v28
	v_and_b32_e32 v125, s7, v28
	v_and_b32_e32 v126, s8, v28
	v_lshrrev_b32_e32 v127, 24, v28
	v_and_b32_e32 v128, s6, v29
	v_and_b32_e32 v129, s7, v29
	v_and_b32_e32 v130, s8, v29
	v_lshrrev_b32_e32 v131, 24, v29
	s_lshl_b32 s30, s70, 12
	s_add_u32 s28, s26, s30
	s_addc_u32 s29, s27, 0
	global_load_dwordx2 v[28:29], v162, s[28:29]
	v_fmac_f32_e32 v178, s25, v124
	v_fmac_f32_e32 v179, s25, v125
	v_fmac_f32_e32 v180, s25, v126
	v_fmac_f32_e32 v181, s25, v127
	v_fmac_f32_e32 v182, s25, v128
	v_fmac_f32_e32 v183, s25, v129
	v_fmac_f32_e32 v184, s25, v130
	v_fmac_f32_e32 v185, s25, v131
	v_readlane_b32 s25, v246, 3
	v_and_b32_e32 v132, s6, v30
	v_and_b32_e32 v133, s7, v30
	v_and_b32_e32 v134, s8, v30
	v_lshrrev_b32_e32 v135, 24, v30
	v_and_b32_e32 v136, s6, v31
	v_and_b32_e32 v137, s7, v31
	v_and_b32_e32 v138, s8, v31
	v_lshrrev_b32_e32 v139, 24, v31
	s_lshl_b32 s30, s71, 12
	s_add_u32 s28, s26, s30
	s_addc_u32 s29, s27, 0
	global_load_dwordx2 v[30:31], v162, s[28:29]
	v_fmac_f32_e32 v178, s25, v132
	v_fmac_f32_e32 v179, s25, v133
	v_fmac_f32_e32 v180, s25, v134
	v_fmac_f32_e32 v181, s25, v135
	v_fmac_f32_e32 v182, s25, v136
	v_fmac_f32_e32 v183, s25, v137
	v_fmac_f32_e32 v184, s25, v138
	v_fmac_f32_e32 v185, s25, v139
	s_waitcnt vmcnt(51)
	v_readlane_b32 s25, v246, 4
	v_and_b32_e32 v124, s6, v32
	v_and_b32_e32 v125, s7, v32
	v_and_b32_e32 v126, s8, v32
	v_lshrrev_b32_e32 v127, 24, v32
	v_and_b32_e32 v128, s6, v33
	v_and_b32_e32 v129, s7, v33
	v_and_b32_e32 v130, s8, v33
	v_lshrrev_b32_e32 v131, 24, v33
	s_lshl_b32 s30, s72, 12
	s_add_u32 s28, s26, s30
	s_addc_u32 s29, s27, 0
	global_load_dwordx2 v[32:33], v162, s[28:29]
	v_fmac_f32_e32 v178, s25, v124
	v_fmac_f32_e32 v179, s25, v125
	v_fmac_f32_e32 v180, s25, v126
	v_fmac_f32_e32 v181, s25, v127
	v_fmac_f32_e32 v182, s25, v128
	v_fmac_f32_e32 v183, s25, v129
	v_fmac_f32_e32 v184, s25, v130
	v_fmac_f32_e32 v185, s25, v131
	v_readlane_b32 s25, v246, 5
	v_and_b32_e32 v132, s6, v34
	v_and_b32_e32 v133, s7, v34
	v_and_b32_e32 v134, s8, v34
	v_lshrrev_b32_e32 v135, 24, v34
	v_and_b32_e32 v136, s6, v35
	v_and_b32_e32 v137, s7, v35
	v_and_b32_e32 v138, s8, v35
	v_lshrrev_b32_e32 v139, 24, v35
	s_lshl_b32 s30, s73, 12
	s_add_u32 s28, s26, s30
	s_addc_u32 s29, s27, 0
	global_load_dwordx2 v[34:35], v162, s[28:29]
	v_fmac_f32_e32 v178, s25, v132
	v_fmac_f32_e32 v179, s25, v133
	v_fmac_f32_e32 v180, s25, v134
	v_fmac_f32_e32 v181, s25, v135
	v_fmac_f32_e32 v182, s25, v136
	v_fmac_f32_e32 v183, s25, v137
	v_fmac_f32_e32 v184, s25, v138
	v_fmac_f32_e32 v185, s25, v139
	v_readlane_b32 s25, v246, 6
	v_and_b32_e32 v124, s6, v36
	v_and_b32_e32 v125, s7, v36
	v_and_b32_e32 v126, s8, v36
	v_lshrrev_b32_e32 v127, 24, v36
	v_and_b32_e32 v128, s6, v37
	v_and_b32_e32 v129, s7, v37
	v_and_b32_e32 v130, s8, v37
	v_lshrrev_b32_e32 v131, 24, v37
	s_lshl_b32 s30, s74, 12
	s_add_u32 s28, s26, s30
	s_addc_u32 s29, s27, 0
	global_load_dwordx2 v[36:37], v162, s[28:29]
	v_fmac_f32_e32 v178, s25, v124
	v_fmac_f32_e32 v179, s25, v125
	v_fmac_f32_e32 v180, s25, v126
	v_fmac_f32_e32 v181, s25, v127
	v_fmac_f32_e32 v182, s25, v128
	v_fmac_f32_e32 v183, s25, v129
	v_fmac_f32_e32 v184, s25, v130
	v_fmac_f32_e32 v185, s25, v131
	v_readlane_b32 s25, v246, 7
	v_and_b32_e32 v132, s6, v38
	v_and_b32_e32 v133, s7, v38
	v_and_b32_e32 v134, s8, v38
	v_lshrrev_b32_e32 v135, 24, v38
	v_and_b32_e32 v136, s6, v39
	v_and_b32_e32 v137, s7, v39
	v_and_b32_e32 v138, s8, v39
	v_lshrrev_b32_e32 v139, 24, v39
	s_lshl_b32 s30, s75, 12
	s_add_u32 s28, s26, s30
	s_addc_u32 s29, s27, 0
	global_load_dwordx2 v[38:39], v162, s[28:29]
	v_fmac_f32_e32 v178, s25, v132
	v_fmac_f32_e32 v179, s25, v133
	v_fmac_f32_e32 v180, s25, v134
	v_fmac_f32_e32 v181, s25, v135
	v_fmac_f32_e32 v182, s25, v136
	v_fmac_f32_e32 v183, s25, v137
	v_fmac_f32_e32 v184, s25, v138
	v_fmac_f32_e32 v185, s25, v139
	s_waitcnt vmcnt(51)
	v_readlane_b32 s25, v246, 8
	v_and_b32_e32 v124, s6, v40
	v_and_b32_e32 v125, s7, v40
	v_and_b32_e32 v126, s8, v40
	v_lshrrev_b32_e32 v127, 24, v40
	v_and_b32_e32 v128, s6, v41
	v_and_b32_e32 v129, s7, v41
	v_and_b32_e32 v130, s8, v41
	v_lshrrev_b32_e32 v131, 24, v41
	s_lshl_b32 s30, s76, 12
	s_add_u32 s28, s26, s30
	s_addc_u32 s29, s27, 0
	global_load_dwordx2 v[40:41], v162, s[28:29]
	v_fmac_f32_e32 v178, s25, v124
	v_fmac_f32_e32 v179, s25, v125
	v_fmac_f32_e32 v180, s25, v126
	v_fmac_f32_e32 v181, s25, v127
	v_fmac_f32_e32 v182, s25, v128
	v_fmac_f32_e32 v183, s25, v129
	v_fmac_f32_e32 v184, s25, v130
	v_fmac_f32_e32 v185, s25, v131
	v_readlane_b32 s25, v246, 9
	v_and_b32_e32 v132, s6, v42
	v_and_b32_e32 v133, s7, v42
	v_and_b32_e32 v134, s8, v42
	v_lshrrev_b32_e32 v135, 24, v42
	v_and_b32_e32 v136, s6, v43
	v_and_b32_e32 v137, s7, v43
	v_and_b32_e32 v138, s8, v43
	v_lshrrev_b32_e32 v139, 24, v43
	s_lshl_b32 s30, s77, 12
	s_add_u32 s28, s26, s30
	s_addc_u32 s29, s27, 0
	global_load_dwordx2 v[42:43], v162, s[28:29]
	v_fmac_f32_e32 v178, s25, v132
	v_fmac_f32_e32 v179, s25, v133
	v_fmac_f32_e32 v180, s25, v134
	v_fmac_f32_e32 v181, s25, v135
	v_fmac_f32_e32 v182, s25, v136
	v_fmac_f32_e32 v183, s25, v137
	v_fmac_f32_e32 v184, s25, v138
	v_fmac_f32_e32 v185, s25, v139
	v_readlane_b32 s25, v246, 10
	v_and_b32_e32 v124, s6, v44
	v_and_b32_e32 v125, s7, v44
	v_and_b32_e32 v126, s8, v44
	v_lshrrev_b32_e32 v127, 24, v44
	v_and_b32_e32 v128, s6, v45
	v_and_b32_e32 v129, s7, v45
	v_and_b32_e32 v130, s8, v45
	v_lshrrev_b32_e32 v131, 24, v45
	s_lshl_b32 s30, s78, 12
	s_add_u32 s28, s26, s30
	s_addc_u32 s29, s27, 0
	global_load_dwordx2 v[44:45], v162, s[28:29]
	v_fmac_f32_e32 v178, s25, v124
	v_fmac_f32_e32 v179, s25, v125
	v_fmac_f32_e32 v180, s25, v126
	v_fmac_f32_e32 v181, s25, v127
	v_fmac_f32_e32 v182, s25, v128
	v_fmac_f32_e32 v183, s25, v129
	v_fmac_f32_e32 v184, s25, v130
	v_fmac_f32_e32 v185, s25, v131
	v_readlane_b32 s25, v246, 11
	v_and_b32_e32 v132, s6, v46
	v_and_b32_e32 v133, s7, v46
	v_and_b32_e32 v134, s8, v46
	v_lshrrev_b32_e32 v135, 24, v46
	v_and_b32_e32 v136, s6, v47
	v_and_b32_e32 v137, s7, v47
	v_and_b32_e32 v138, s8, v47
	v_lshrrev_b32_e32 v139, 24, v47
	s_lshl_b32 s30, s79, 12
	s_add_u32 s28, s26, s30
	s_addc_u32 s29, s27, 0
	global_load_dwordx2 v[46:47], v162, s[28:29]
	v_fmac_f32_e32 v178, s25, v132
	v_fmac_f32_e32 v179, s25, v133
	v_fmac_f32_e32 v180, s25, v134
	v_fmac_f32_e32 v181, s25, v135
	v_fmac_f32_e32 v182, s25, v136
	v_fmac_f32_e32 v183, s25, v137
	v_fmac_f32_e32 v184, s25, v138
	v_fmac_f32_e32 v185, s25, v139
	s_waitcnt vmcnt(51)
	v_readlane_b32 s25, v246, 12
	v_and_b32_e32 v124, s6, v48
	v_and_b32_e32 v125, s7, v48
	v_and_b32_e32 v126, s8, v48
	v_lshrrev_b32_e32 v127, 24, v48
	v_and_b32_e32 v128, s6, v49
	v_and_b32_e32 v129, s7, v49
	v_and_b32_e32 v130, s8, v49
	v_lshrrev_b32_e32 v131, 24, v49
	s_lshl_b32 s30, s80, 12
	s_add_u32 s28, s26, s30
	s_addc_u32 s29, s27, 0
	global_load_dwordx2 v[48:49], v162, s[28:29]
	v_fmac_f32_e32 v178, s25, v124
	v_fmac_f32_e32 v179, s25, v125
	v_fmac_f32_e32 v180, s25, v126
	v_fmac_f32_e32 v181, s25, v127
	v_fmac_f32_e32 v182, s25, v128
	v_fmac_f32_e32 v183, s25, v129
	v_fmac_f32_e32 v184, s25, v130
	v_fmac_f32_e32 v185, s25, v131
	v_readlane_b32 s25, v246, 13
	v_and_b32_e32 v132, s6, v50
	v_and_b32_e32 v133, s7, v50
	v_and_b32_e32 v134, s8, v50
	v_lshrrev_b32_e32 v135, 24, v50
	v_and_b32_e32 v136, s6, v51
	v_and_b32_e32 v137, s7, v51
	v_and_b32_e32 v138, s8, v51
	v_lshrrev_b32_e32 v139, 24, v51
	s_lshl_b32 s30, s81, 12
	s_add_u32 s28, s26, s30
	s_addc_u32 s29, s27, 0
	global_load_dwordx2 v[50:51], v162, s[28:29]
	v_fmac_f32_e32 v178, s25, v132
	v_fmac_f32_e32 v179, s25, v133
	v_fmac_f32_e32 v180, s25, v134
	v_fmac_f32_e32 v181, s25, v135
	v_fmac_f32_e32 v182, s25, v136
	v_fmac_f32_e32 v183, s25, v137
	v_fmac_f32_e32 v184, s25, v138
	v_fmac_f32_e32 v185, s25, v139
	v_readlane_b32 s25, v246, 14
	v_and_b32_e32 v124, s6, v52
	v_and_b32_e32 v125, s7, v52
	v_and_b32_e32 v126, s8, v52
	v_lshrrev_b32_e32 v127, 24, v52
	v_and_b32_e32 v128, s6, v53
	v_and_b32_e32 v129, s7, v53
	v_and_b32_e32 v130, s8, v53
	v_lshrrev_b32_e32 v131, 24, v53
	s_lshl_b32 s30, s82, 12
	s_add_u32 s28, s26, s30
	s_addc_u32 s29, s27, 0
	global_load_dwordx2 v[52:53], v162, s[28:29]
	v_fmac_f32_e32 v178, s25, v124
	v_fmac_f32_e32 v179, s25, v125
	v_fmac_f32_e32 v180, s25, v126
	v_fmac_f32_e32 v181, s25, v127
	v_fmac_f32_e32 v182, s25, v128
	v_fmac_f32_e32 v183, s25, v129
	v_fmac_f32_e32 v184, s25, v130
	v_fmac_f32_e32 v185, s25, v131
	v_readlane_b32 s25, v246, 15
	v_and_b32_e32 v132, s6, v54
	v_and_b32_e32 v133, s7, v54
	v_and_b32_e32 v134, s8, v54
	v_lshrrev_b32_e32 v135, 24, v54
	v_and_b32_e32 v136, s6, v55
	v_and_b32_e32 v137, s7, v55
	v_and_b32_e32 v138, s8, v55
	v_lshrrev_b32_e32 v139, 24, v55
	s_lshl_b32 s30, s83, 12
	s_add_u32 s28, s26, s30
	s_addc_u32 s29, s27, 0
	global_load_dwordx2 v[54:55], v162, s[28:29]
	v_fmac_f32_e32 v178, s25, v132
	v_fmac_f32_e32 v179, s25, v133
	v_fmac_f32_e32 v180, s25, v134
	v_fmac_f32_e32 v181, s25, v135
	v_fmac_f32_e32 v182, s25, v136
	v_fmac_f32_e32 v183, s25, v137
	v_fmac_f32_e32 v184, s25, v138
	v_fmac_f32_e32 v185, s25, v139
	s_waitcnt vmcnt(51)
	v_readlane_b32 s25, v246, 16
	v_and_b32_e32 v124, s6, v56
	v_and_b32_e32 v125, s7, v56
	v_and_b32_e32 v126, s8, v56
	v_lshrrev_b32_e32 v127, 24, v56
	v_and_b32_e32 v128, s6, v57
	v_and_b32_e32 v129, s7, v57
	v_and_b32_e32 v130, s8, v57
	v_lshrrev_b32_e32 v131, 24, v57
	s_waitcnt lgkmcnt(0)
	s_load_dwordx16 s[68:83], s[36:37], 0x100 glc
	s_lshl_b32 s30, s84, 12
	s_add_u32 s28, s26, s30
	s_addc_u32 s29, s27, 0
	global_load_dwordx2 v[56:57], v162, s[28:29]
	v_fmac_f32_e32 v178, s25, v124
	v_fmac_f32_e32 v179, s25, v125
	v_fmac_f32_e32 v180, s25, v126
	v_fmac_f32_e32 v181, s25, v127
	v_fmac_f32_e32 v182, s25, v128
	v_fmac_f32_e32 v183, s25, v129
	v_fmac_f32_e32 v184, s25, v130
	v_fmac_f32_e32 v185, s25, v131
	v_readlane_b32 s25, v246, 17
	v_and_b32_e32 v132, s6, v58
	v_and_b32_e32 v133, s7, v58
	v_and_b32_e32 v134, s8, v58
	v_lshrrev_b32_e32 v135, 24, v58
	v_and_b32_e32 v136, s6, v59
	v_and_b32_e32 v137, s7, v59
	v_and_b32_e32 v138, s8, v59
	v_lshrrev_b32_e32 v139, 24, v59
	s_lshl_b32 s30, s85, 12
	s_add_u32 s28, s26, s30
	s_addc_u32 s29, s27, 0
	global_load_dwordx2 v[58:59], v162, s[28:29]
	v_fmac_f32_e32 v178, s25, v132
	v_fmac_f32_e32 v179, s25, v133
	v_fmac_f32_e32 v180, s25, v134
	v_fmac_f32_e32 v181, s25, v135
	v_fmac_f32_e32 v182, s25, v136
	v_fmac_f32_e32 v183, s25, v137
	v_fmac_f32_e32 v184, s25, v138
	v_fmac_f32_e32 v185, s25, v139
	v_readlane_b32 s25, v246, 18
	v_and_b32_e32 v124, s6, v60
	v_and_b32_e32 v125, s7, v60
	v_and_b32_e32 v126, s8, v60
	v_lshrrev_b32_e32 v127, 24, v60
	v_and_b32_e32 v128, s6, v61
	v_and_b32_e32 v129, s7, v61
	v_and_b32_e32 v130, s8, v61
	v_lshrrev_b32_e32 v131, 24, v61
	s_lshl_b32 s30, s86, 12
	s_add_u32 s28, s26, s30
	s_addc_u32 s29, s27, 0
	global_load_dwordx2 v[60:61], v162, s[28:29]
	v_fmac_f32_e32 v178, s25, v124
	v_fmac_f32_e32 v179, s25, v125
	v_fmac_f32_e32 v180, s25, v126
	v_fmac_f32_e32 v181, s25, v127
	v_fmac_f32_e32 v182, s25, v128
	v_fmac_f32_e32 v183, s25, v129
	v_fmac_f32_e32 v184, s25, v130
	v_fmac_f32_e32 v185, s25, v131
	v_readlane_b32 s25, v246, 19
	v_and_b32_e32 v132, s6, v62
	v_and_b32_e32 v133, s7, v62
	v_and_b32_e32 v134, s8, v62
	v_lshrrev_b32_e32 v135, 24, v62
	v_and_b32_e32 v136, s6, v63
	v_and_b32_e32 v137, s7, v63
	v_and_b32_e32 v138, s8, v63
	v_lshrrev_b32_e32 v139, 24, v63
	s_lshl_b32 s30, s87, 12
	s_add_u32 s28, s26, s30
	s_addc_u32 s29, s27, 0
	global_load_dwordx2 v[62:63], v162, s[28:29]
	v_fmac_f32_e32 v178, s25, v132
	v_fmac_f32_e32 v179, s25, v133
	v_fmac_f32_e32 v180, s25, v134
	v_fmac_f32_e32 v181, s25, v135
	v_fmac_f32_e32 v182, s25, v136
	v_fmac_f32_e32 v183, s25, v137
	v_fmac_f32_e32 v184, s25, v138
	v_fmac_f32_e32 v185, s25, v139
	s_waitcnt vmcnt(51)
	v_readlane_b32 s25, v246, 20
	v_and_b32_e32 v124, s6, v64
	v_and_b32_e32 v125, s7, v64
	v_and_b32_e32 v126, s8, v64
	v_lshrrev_b32_e32 v127, 24, v64
	v_and_b32_e32 v128, s6, v65
	v_and_b32_e32 v129, s7, v65
	v_and_b32_e32 v130, s8, v65
	v_lshrrev_b32_e32 v131, 24, v65
	s_lshl_b32 s30, s88, 12
	s_add_u32 s28, s26, s30
	s_addc_u32 s29, s27, 0
	global_load_dwordx2 v[64:65], v162, s[28:29]
	v_fmac_f32_e32 v178, s25, v124
	v_fmac_f32_e32 v179, s25, v125
	v_fmac_f32_e32 v180, s25, v126
	v_fmac_f32_e32 v181, s25, v127
	v_fmac_f32_e32 v182, s25, v128
	v_fmac_f32_e32 v183, s25, v129
	v_fmac_f32_e32 v184, s25, v130
	v_fmac_f32_e32 v185, s25, v131
	v_readlane_b32 s25, v246, 21
	v_and_b32_e32 v132, s6, v66
	v_and_b32_e32 v133, s7, v66
	v_and_b32_e32 v134, s8, v66
	v_lshrrev_b32_e32 v135, 24, v66
	v_and_b32_e32 v136, s6, v67
	v_and_b32_e32 v137, s7, v67
	v_and_b32_e32 v138, s8, v67
	v_lshrrev_b32_e32 v139, 24, v67
	s_lshl_b32 s30, s89, 12
	s_add_u32 s28, s26, s30
	s_addc_u32 s29, s27, 0
	global_load_dwordx2 v[66:67], v162, s[28:29]
	v_fmac_f32_e32 v178, s25, v132
	v_fmac_f32_e32 v179, s25, v133
	v_fmac_f32_e32 v180, s25, v134
	v_fmac_f32_e32 v181, s25, v135
	v_fmac_f32_e32 v182, s25, v136
	v_fmac_f32_e32 v183, s25, v137
	v_fmac_f32_e32 v184, s25, v138
	v_fmac_f32_e32 v185, s25, v139
	v_readlane_b32 s25, v246, 22
	v_and_b32_e32 v124, s6, v68
	v_and_b32_e32 v125, s7, v68
	v_and_b32_e32 v126, s8, v68
	v_lshrrev_b32_e32 v127, 24, v68
	v_and_b32_e32 v128, s6, v69
	v_and_b32_e32 v129, s7, v69
	v_and_b32_e32 v130, s8, v69
	v_lshrrev_b32_e32 v131, 24, v69
	s_lshl_b32 s30, s90, 12
	s_add_u32 s28, s26, s30
	s_addc_u32 s29, s27, 0
	global_load_dwordx2 v[68:69], v162, s[28:29]
	v_fmac_f32_e32 v178, s25, v124
	v_fmac_f32_e32 v179, s25, v125
	v_fmac_f32_e32 v180, s25, v126
	v_fmac_f32_e32 v181, s25, v127
	v_fmac_f32_e32 v182, s25, v128
	v_fmac_f32_e32 v183, s25, v129
	v_fmac_f32_e32 v184, s25, v130
	v_fmac_f32_e32 v185, s25, v131
	v_readlane_b32 s25, v246, 23
	v_and_b32_e32 v132, s6, v70
	v_and_b32_e32 v133, s7, v70
	v_and_b32_e32 v134, s8, v70
	v_lshrrev_b32_e32 v135, 24, v70
	v_and_b32_e32 v136, s6, v71
	v_and_b32_e32 v137, s7, v71
	v_and_b32_e32 v138, s8, v71
	v_lshrrev_b32_e32 v139, 24, v71
	s_lshl_b32 s30, s91, 12
	s_add_u32 s28, s26, s30
	s_addc_u32 s29, s27, 0
	global_load_dwordx2 v[70:71], v162, s[28:29]
	v_fmac_f32_e32 v178, s25, v132
	v_fmac_f32_e32 v179, s25, v133
	v_fmac_f32_e32 v180, s25, v134
	v_fmac_f32_e32 v181, s25, v135
	v_fmac_f32_e32 v182, s25, v136
	v_fmac_f32_e32 v183, s25, v137
	v_fmac_f32_e32 v184, s25, v138
	v_fmac_f32_e32 v185, s25, v139
	s_waitcnt vmcnt(51)
	v_readlane_b32 s25, v246, 24
	v_and_b32_e32 v124, s6, v72
	v_and_b32_e32 v125, s7, v72
	v_and_b32_e32 v126, s8, v72
	v_lshrrev_b32_e32 v127, 24, v72
	v_and_b32_e32 v128, s6, v73
	v_and_b32_e32 v129, s7, v73
	v_and_b32_e32 v130, s8, v73
	v_lshrrev_b32_e32 v131, 24, v73
	s_lshl_b32 s30, s92, 12
	s_add_u32 s28, s26, s30
	s_addc_u32 s29, s27, 0
	global_load_dwordx2 v[72:73], v162, s[28:29]
	v_fmac_f32_e32 v178, s25, v124
	v_fmac_f32_e32 v179, s25, v125
	v_fmac_f32_e32 v180, s25, v126
	v_fmac_f32_e32 v181, s25, v127
	v_fmac_f32_e32 v182, s25, v128
	v_fmac_f32_e32 v183, s25, v129
	v_fmac_f32_e32 v184, s25, v130
	v_fmac_f32_e32 v185, s25, v131
	v_readlane_b32 s25, v246, 25
	v_and_b32_e32 v132, s6, v74
	v_and_b32_e32 v133, s7, v74
	v_and_b32_e32 v134, s8, v74
	v_lshrrev_b32_e32 v135, 24, v74
	v_and_b32_e32 v136, s6, v75
	v_and_b32_e32 v137, s7, v75
	v_and_b32_e32 v138, s8, v75
	v_lshrrev_b32_e32 v139, 24, v75
	s_lshl_b32 s30, s93, 12
	s_add_u32 s28, s26, s30
	s_addc_u32 s29, s27, 0
	global_load_dwordx2 v[74:75], v162, s[28:29]
	v_fmac_f32_e32 v178, s25, v132
	v_fmac_f32_e32 v179, s25, v133
	v_fmac_f32_e32 v180, s25, v134
	v_fmac_f32_e32 v181, s25, v135
	v_fmac_f32_e32 v182, s25, v136
	v_fmac_f32_e32 v183, s25, v137
	v_fmac_f32_e32 v184, s25, v138
	v_fmac_f32_e32 v185, s25, v139
	v_readlane_b32 s25, v246, 26
	v_and_b32_e32 v124, s6, v76
	v_and_b32_e32 v125, s7, v76
	v_and_b32_e32 v126, s8, v76
	v_lshrrev_b32_e32 v127, 24, v76
	v_and_b32_e32 v128, s6, v77
	v_and_b32_e32 v129, s7, v77
	v_and_b32_e32 v130, s8, v77
	v_lshrrev_b32_e32 v131, 24, v77
	s_lshl_b32 s30, s94, 12
	s_add_u32 s28, s26, s30
	s_addc_u32 s29, s27, 0
	global_load_dwordx2 v[76:77], v162, s[28:29]
	v_fmac_f32_e32 v178, s25, v124
	v_fmac_f32_e32 v179, s25, v125
	v_fmac_f32_e32 v180, s25, v126
	v_fmac_f32_e32 v181, s25, v127
	v_fmac_f32_e32 v182, s25, v128
	v_fmac_f32_e32 v183, s25, v129
	v_fmac_f32_e32 v184, s25, v130
	v_fmac_f32_e32 v185, s25, v131
	v_readlane_b32 s25, v246, 27
	v_and_b32_e32 v132, s6, v78
	v_and_b32_e32 v133, s7, v78
	v_and_b32_e32 v134, s8, v78
	v_lshrrev_b32_e32 v135, 24, v78
	v_and_b32_e32 v136, s6, v79
	v_and_b32_e32 v137, s7, v79
	v_and_b32_e32 v138, s8, v79
	v_lshrrev_b32_e32 v139, 24, v79
	s_lshl_b32 s30, s95, 12
	s_add_u32 s28, s26, s30
	s_addc_u32 s29, s27, 0
	global_load_dwordx2 v[78:79], v162, s[28:29]
	v_fmac_f32_e32 v178, s25, v132
	v_fmac_f32_e32 v179, s25, v133
	v_fmac_f32_e32 v180, s25, v134
	v_fmac_f32_e32 v181, s25, v135
	v_fmac_f32_e32 v182, s25, v136
	v_fmac_f32_e32 v183, s25, v137
	v_fmac_f32_e32 v184, s25, v138
	v_fmac_f32_e32 v185, s25, v139
	s_waitcnt vmcnt(51)
	v_readlane_b32 s25, v246, 28
	v_and_b32_e32 v124, s6, v80
	v_and_b32_e32 v125, s7, v80
	v_and_b32_e32 v126, s8, v80
	v_lshrrev_b32_e32 v127, 24, v80
	v_and_b32_e32 v128, s6, v81
	v_and_b32_e32 v129, s7, v81
	v_and_b32_e32 v130, s8, v81
	v_lshrrev_b32_e32 v131, 24, v81
	s_lshl_b32 s30, s96, 12
	s_add_u32 s28, s26, s30
	s_addc_u32 s29, s27, 0
	global_load_dwordx2 v[80:81], v162, s[28:29]
	v_fmac_f32_e32 v178, s25, v124
	v_fmac_f32_e32 v179, s25, v125
	v_fmac_f32_e32 v180, s25, v126
	v_fmac_f32_e32 v181, s25, v127
	v_fmac_f32_e32 v182, s25, v128
	v_fmac_f32_e32 v183, s25, v129
	v_fmac_f32_e32 v184, s25, v130
	v_fmac_f32_e32 v185, s25, v131
	v_readlane_b32 s25, v246, 29
	v_and_b32_e32 v132, s6, v82
	v_and_b32_e32 v133, s7, v82
	v_and_b32_e32 v134, s8, v82
	v_lshrrev_b32_e32 v135, 24, v82
	v_and_b32_e32 v136, s6, v83
	v_and_b32_e32 v137, s7, v83
	v_and_b32_e32 v138, s8, v83
	v_lshrrev_b32_e32 v139, 24, v83
	s_lshl_b32 s30, s97, 12
	s_add_u32 s28, s26, s30
	s_addc_u32 s29, s27, 0
	global_load_dwordx2 v[82:83], v162, s[28:29]
	v_fmac_f32_e32 v178, s25, v132
	v_fmac_f32_e32 v179, s25, v133
	v_fmac_f32_e32 v180, s25, v134
	v_fmac_f32_e32 v181, s25, v135
	v_fmac_f32_e32 v182, s25, v136
	v_fmac_f32_e32 v183, s25, v137
	v_fmac_f32_e32 v184, s25, v138
	v_fmac_f32_e32 v185, s25, v139
	v_readlane_b32 s25, v246, 30
	v_and_b32_e32 v124, s6, v84
	v_and_b32_e32 v125, s7, v84
	v_and_b32_e32 v126, s8, v84
	v_lshrrev_b32_e32 v127, 24, v84
	v_and_b32_e32 v128, s6, v85
	v_and_b32_e32 v129, s7, v85
	v_and_b32_e32 v130, s8, v85
	v_lshrrev_b32_e32 v131, 24, v85
	s_lshl_b32 s30, s98, 12
	s_add_u32 s28, s26, s30
	s_addc_u32 s29, s27, 0
	global_load_dwordx2 v[84:85], v162, s[28:29]
	v_fmac_f32_e32 v178, s25, v124
	v_fmac_f32_e32 v179, s25, v125
	v_fmac_f32_e32 v180, s25, v126
	v_fmac_f32_e32 v181, s25, v127
	v_fmac_f32_e32 v182, s25, v128
	v_fmac_f32_e32 v183, s25, v129
	v_fmac_f32_e32 v184, s25, v130
	v_fmac_f32_e32 v185, s25, v131
	v_readlane_b32 s25, v246, 31
	v_and_b32_e32 v132, s6, v86
	v_and_b32_e32 v133, s7, v86
	v_and_b32_e32 v134, s8, v86
	v_lshrrev_b32_e32 v135, 24, v86
	v_and_b32_e32 v136, s6, v87
	v_and_b32_e32 v137, s7, v87
	v_and_b32_e32 v138, s8, v87
	v_lshrrev_b32_e32 v139, 24, v87
	s_lshl_b32 s30, s99, 12
	s_add_u32 s28, s26, s30
	s_addc_u32 s29, s27, 0
	global_load_dwordx2 v[86:87], v162, s[28:29]
	v_fmac_f32_e32 v178, s25, v132
	v_fmac_f32_e32 v179, s25, v133
	v_fmac_f32_e32 v180, s25, v134
	v_fmac_f32_e32 v181, s25, v135
	v_fmac_f32_e32 v182, s25, v136
	v_fmac_f32_e32 v183, s25, v137
	v_fmac_f32_e32 v184, s25, v138
	v_fmac_f32_e32 v185, s25, v139
	s_waitcnt vmcnt(28)
	v_readlane_b32 s25, v246, 32
	v_and_b32_e32 v124, s6, v24
	v_and_b32_e32 v125, s7, v24
	v_and_b32_e32 v126, s8, v24
	v_lshrrev_b32_e32 v127, 24, v24
	v_and_b32_e32 v128, s6, v25
	v_and_b32_e32 v129, s7, v25
	v_and_b32_e32 v130, s8, v25
	v_lshrrev_b32_e32 v131, 24, v25
	s_waitcnt lgkmcnt(0)
	s_load_dwordx16 s[84:99], s[36:37], 0x140 glc
	s_lshl_b32 s30, s68, 12
	s_add_u32 s28, s26, s30
	s_addc_u32 s29, s27, 0
	global_load_dwordx2 v[24:25], v162, s[28:29]
	v_fmac_f32_e32 v178, s25, v124
	v_fmac_f32_e32 v179, s25, v125
	v_fmac_f32_e32 v180, s25, v126
	v_fmac_f32_e32 v181, s25, v127
	v_fmac_f32_e32 v182, s25, v128
	v_fmac_f32_e32 v183, s25, v129
	v_fmac_f32_e32 v184, s25, v130
	v_fmac_f32_e32 v185, s25, v131
	v_readlane_b32 s25, v246, 33
	v_and_b32_e32 v132, s6, v26
	v_and_b32_e32 v133, s7, v26
	v_and_b32_e32 v134, s8, v26
	v_lshrrev_b32_e32 v135, 24, v26
	v_and_b32_e32 v136, s6, v27
	v_and_b32_e32 v137, s7, v27
	v_and_b32_e32 v138, s8, v27
	v_lshrrev_b32_e32 v139, 24, v27
	s_lshl_b32 s30, s69, 12
	s_add_u32 s28, s26, s30
	s_addc_u32 s29, s27, 0
	global_load_dwordx2 v[26:27], v162, s[28:29]
	v_fmac_f32_e32 v178, s25, v132
	v_fmac_f32_e32 v179, s25, v133
	v_fmac_f32_e32 v180, s25, v134
	v_fmac_f32_e32 v181, s25, v135
	v_fmac_f32_e32 v182, s25, v136
	v_fmac_f32_e32 v183, s25, v137
	v_fmac_f32_e32 v184, s25, v138
	v_fmac_f32_e32 v185, s25, v139
	v_readlane_b32 s25, v246, 34
	v_and_b32_e32 v124, s6, v28
	v_and_b32_e32 v125, s7, v28
	v_and_b32_e32 v126, s8, v28
	v_lshrrev_b32_e32 v127, 24, v28
	v_and_b32_e32 v128, s6, v29
	v_and_b32_e32 v129, s7, v29
	v_and_b32_e32 v130, s8, v29
	v_lshrrev_b32_e32 v131, 24, v29
	s_lshl_b32 s30, s70, 12
	s_add_u32 s28, s26, s30
	s_addc_u32 s29, s27, 0
	global_load_dwordx2 v[28:29], v162, s[28:29]
	v_fmac_f32_e32 v178, s25, v124
	v_fmac_f32_e32 v179, s25, v125
	v_fmac_f32_e32 v180, s25, v126
	v_fmac_f32_e32 v181, s25, v127
	v_fmac_f32_e32 v182, s25, v128
	v_fmac_f32_e32 v183, s25, v129
	v_fmac_f32_e32 v184, s25, v130
	v_fmac_f32_e32 v185, s25, v131
	v_readlane_b32 s25, v246, 35
	v_and_b32_e32 v132, s6, v30
	v_and_b32_e32 v133, s7, v30
	v_and_b32_e32 v134, s8, v30
	v_lshrrev_b32_e32 v135, 24, v30
	v_and_b32_e32 v136, s6, v31
	v_and_b32_e32 v137, s7, v31
	v_and_b32_e32 v138, s8, v31
	v_lshrrev_b32_e32 v139, 24, v31
	s_lshl_b32 s30, s71, 12
	s_add_u32 s28, s26, s30
	s_addc_u32 s29, s27, 0
	global_load_dwordx2 v[30:31], v162, s[28:29]
	v_fmac_f32_e32 v178, s25, v132
	v_fmac_f32_e32 v179, s25, v133
	v_fmac_f32_e32 v180, s25, v134
	v_fmac_f32_e32 v181, s25, v135
	v_fmac_f32_e32 v182, s25, v136
	v_fmac_f32_e32 v183, s25, v137
	v_fmac_f32_e32 v184, s25, v138
	v_fmac_f32_e32 v185, s25, v139
	s_waitcnt vmcnt(28)
	v_readlane_b32 s25, v246, 36
	v_and_b32_e32 v124, s6, v32
	v_and_b32_e32 v125, s7, v32
	v_and_b32_e32 v126, s8, v32
	v_lshrrev_b32_e32 v127, 24, v32
	v_and_b32_e32 v128, s6, v33
	v_and_b32_e32 v129, s7, v33
	v_and_b32_e32 v130, s8, v33
	v_lshrrev_b32_e32 v131, 24, v33
	s_lshl_b32 s30, s72, 12
	s_add_u32 s28, s26, s30
	s_addc_u32 s29, s27, 0
	global_load_dwordx2 v[32:33], v162, s[28:29]
	v_fmac_f32_e32 v178, s25, v124
	v_fmac_f32_e32 v179, s25, v125
	v_fmac_f32_e32 v180, s25, v126
	v_fmac_f32_e32 v181, s25, v127
	v_fmac_f32_e32 v182, s25, v128
	v_fmac_f32_e32 v183, s25, v129
	v_fmac_f32_e32 v184, s25, v130
	v_fmac_f32_e32 v185, s25, v131
	v_readlane_b32 s25, v246, 37
	v_and_b32_e32 v132, s6, v34
	v_and_b32_e32 v133, s7, v34
	v_and_b32_e32 v134, s8, v34
	v_lshrrev_b32_e32 v135, 24, v34
	v_and_b32_e32 v136, s6, v35
	v_and_b32_e32 v137, s7, v35
	v_and_b32_e32 v138, s8, v35
	v_lshrrev_b32_e32 v139, 24, v35
	s_lshl_b32 s30, s73, 12
	s_add_u32 s28, s26, s30
	s_addc_u32 s29, s27, 0
	global_load_dwordx2 v[34:35], v162, s[28:29]
	v_fmac_f32_e32 v178, s25, v132
	v_fmac_f32_e32 v179, s25, v133
	v_fmac_f32_e32 v180, s25, v134
	v_fmac_f32_e32 v181, s25, v135
	v_fmac_f32_e32 v182, s25, v136
	v_fmac_f32_e32 v183, s25, v137
	v_fmac_f32_e32 v184, s25, v138
	v_fmac_f32_e32 v185, s25, v139
	v_readlane_b32 s25, v246, 38
	v_and_b32_e32 v124, s6, v36
	v_and_b32_e32 v125, s7, v36
	v_and_b32_e32 v126, s8, v36
	v_lshrrev_b32_e32 v127, 24, v36
	v_and_b32_e32 v128, s6, v37
	v_and_b32_e32 v129, s7, v37
	v_and_b32_e32 v130, s8, v37
	v_lshrrev_b32_e32 v131, 24, v37
	s_lshl_b32 s30, s74, 12
	s_add_u32 s28, s26, s30
	s_addc_u32 s29, s27, 0
	global_load_dwordx2 v[36:37], v162, s[28:29]
	v_fmac_f32_e32 v178, s25, v124
	v_fmac_f32_e32 v179, s25, v125
	v_fmac_f32_e32 v180, s25, v126
	v_fmac_f32_e32 v181, s25, v127
	v_fmac_f32_e32 v182, s25, v128
	v_fmac_f32_e32 v183, s25, v129
	v_fmac_f32_e32 v184, s25, v130
	v_fmac_f32_e32 v185, s25, v131
	v_readlane_b32 s25, v246, 39
	v_and_b32_e32 v132, s6, v38
	v_and_b32_e32 v133, s7, v38
	v_and_b32_e32 v134, s8, v38
	v_lshrrev_b32_e32 v135, 24, v38
	v_and_b32_e32 v136, s6, v39
	v_and_b32_e32 v137, s7, v39
	v_and_b32_e32 v138, s8, v39
	v_lshrrev_b32_e32 v139, 24, v39
	s_lshl_b32 s30, s75, 12
	s_add_u32 s28, s26, s30
	s_addc_u32 s29, s27, 0
	global_load_dwordx2 v[38:39], v162, s[28:29]
	v_fmac_f32_e32 v178, s25, v132
	v_fmac_f32_e32 v179, s25, v133
	v_fmac_f32_e32 v180, s25, v134
	v_fmac_f32_e32 v181, s25, v135
	v_fmac_f32_e32 v182, s25, v136
	v_fmac_f32_e32 v183, s25, v137
	v_fmac_f32_e32 v184, s25, v138
	v_fmac_f32_e32 v185, s25, v139
	s_waitcnt vmcnt(28)
	v_readlane_b32 s25, v246, 40
	v_and_b32_e32 v124, s6, v40
	v_and_b32_e32 v125, s7, v40
	v_and_b32_e32 v126, s8, v40
	v_lshrrev_b32_e32 v127, 24, v40
	v_and_b32_e32 v128, s6, v41
	v_and_b32_e32 v129, s7, v41
	v_and_b32_e32 v130, s8, v41
	v_lshrrev_b32_e32 v131, 24, v41
	s_lshl_b32 s30, s76, 12
	s_add_u32 s28, s26, s30
	s_addc_u32 s29, s27, 0
	global_load_dwordx2 v[40:41], v162, s[28:29]
	v_fmac_f32_e32 v178, s25, v124
	v_fmac_f32_e32 v179, s25, v125
	v_fmac_f32_e32 v180, s25, v126
	v_fmac_f32_e32 v181, s25, v127
	v_fmac_f32_e32 v182, s25, v128
	v_fmac_f32_e32 v183, s25, v129
	v_fmac_f32_e32 v184, s25, v130
	v_fmac_f32_e32 v185, s25, v131
	v_readlane_b32 s25, v246, 41
	v_and_b32_e32 v132, s6, v42
	v_and_b32_e32 v133, s7, v42
	v_and_b32_e32 v134, s8, v42
	v_lshrrev_b32_e32 v135, 24, v42
	v_and_b32_e32 v136, s6, v43
	v_and_b32_e32 v137, s7, v43
	v_and_b32_e32 v138, s8, v43
	v_lshrrev_b32_e32 v139, 24, v43
	s_lshl_b32 s30, s77, 12
	s_add_u32 s28, s26, s30
	s_addc_u32 s29, s27, 0
	global_load_dwordx2 v[42:43], v162, s[28:29]
	v_fmac_f32_e32 v178, s25, v132
	v_fmac_f32_e32 v179, s25, v133
	v_fmac_f32_e32 v180, s25, v134
	v_fmac_f32_e32 v181, s25, v135
	v_fmac_f32_e32 v182, s25, v136
	v_fmac_f32_e32 v183, s25, v137
	v_fmac_f32_e32 v184, s25, v138
	v_fmac_f32_e32 v185, s25, v139
	v_readlane_b32 s25, v246, 42
	v_and_b32_e32 v124, s6, v44
	v_and_b32_e32 v125, s7, v44
	v_and_b32_e32 v126, s8, v44
	v_lshrrev_b32_e32 v127, 24, v44
	v_and_b32_e32 v128, s6, v45
	v_and_b32_e32 v129, s7, v45
	v_and_b32_e32 v130, s8, v45
	v_lshrrev_b32_e32 v131, 24, v45
	s_lshl_b32 s30, s78, 12
	s_add_u32 s28, s26, s30
	s_addc_u32 s29, s27, 0
	global_load_dwordx2 v[44:45], v162, s[28:29]
	v_fmac_f32_e32 v178, s25, v124
	v_fmac_f32_e32 v179, s25, v125
	v_fmac_f32_e32 v180, s25, v126
	v_fmac_f32_e32 v181, s25, v127
	v_fmac_f32_e32 v182, s25, v128
	v_fmac_f32_e32 v183, s25, v129
	v_fmac_f32_e32 v184, s25, v130
	v_fmac_f32_e32 v185, s25, v131
	v_readlane_b32 s25, v246, 43
	v_and_b32_e32 v132, s6, v46
	v_and_b32_e32 v133, s7, v46
	v_and_b32_e32 v134, s8, v46
	v_lshrrev_b32_e32 v135, 24, v46
	v_and_b32_e32 v136, s6, v47
	v_and_b32_e32 v137, s7, v47
	v_and_b32_e32 v138, s8, v47
	v_lshrrev_b32_e32 v139, 24, v47
	s_lshl_b32 s30, s79, 12
	s_add_u32 s28, s26, s30
	s_addc_u32 s29, s27, 0
	global_load_dwordx2 v[46:47], v162, s[28:29]
	v_fmac_f32_e32 v178, s25, v132
	v_fmac_f32_e32 v179, s25, v133
	v_fmac_f32_e32 v180, s25, v134
	v_fmac_f32_e32 v181, s25, v135
	v_fmac_f32_e32 v182, s25, v136
	v_fmac_f32_e32 v183, s25, v137
	v_fmac_f32_e32 v184, s25, v138
	v_fmac_f32_e32 v185, s25, v139
	s_waitcnt vmcnt(28)
	v_readlane_b32 s25, v246, 44
	v_and_b32_e32 v124, s6, v48
	v_and_b32_e32 v125, s7, v48
	v_and_b32_e32 v126, s8, v48
	v_lshrrev_b32_e32 v127, 24, v48
	v_and_b32_e32 v128, s6, v49
	v_and_b32_e32 v129, s7, v49
	v_and_b32_e32 v130, s8, v49
	v_lshrrev_b32_e32 v131, 24, v49
	s_lshl_b32 s30, s80, 12
	s_add_u32 s28, s26, s30
	s_addc_u32 s29, s27, 0
	global_load_dwordx2 v[48:49], v162, s[28:29]
	v_fmac_f32_e32 v178, s25, v124
	v_fmac_f32_e32 v179, s25, v125
	v_fmac_f32_e32 v180, s25, v126
	v_fmac_f32_e32 v181, s25, v127
	v_fmac_f32_e32 v182, s25, v128
	v_fmac_f32_e32 v183, s25, v129
	v_fmac_f32_e32 v184, s25, v130
	v_fmac_f32_e32 v185, s25, v131
	v_readlane_b32 s25, v246, 45
	v_and_b32_e32 v132, s6, v50
	v_and_b32_e32 v133, s7, v50
	v_and_b32_e32 v134, s8, v50
	v_lshrrev_b32_e32 v135, 24, v50
	v_and_b32_e32 v136, s6, v51
	v_and_b32_e32 v137, s7, v51
	v_and_b32_e32 v138, s8, v51
	v_lshrrev_b32_e32 v139, 24, v51
	s_lshl_b32 s30, s81, 12
	s_add_u32 s28, s26, s30
	s_addc_u32 s29, s27, 0
	global_load_dwordx2 v[50:51], v162, s[28:29]
	v_fmac_f32_e32 v178, s25, v132
	v_fmac_f32_e32 v179, s25, v133
	v_fmac_f32_e32 v180, s25, v134
	v_fmac_f32_e32 v181, s25, v135
	v_fmac_f32_e32 v182, s25, v136
	v_fmac_f32_e32 v183, s25, v137
	v_fmac_f32_e32 v184, s25, v138
	v_fmac_f32_e32 v185, s25, v139
	v_readlane_b32 s25, v246, 46
	v_and_b32_e32 v124, s6, v52
	v_and_b32_e32 v125, s7, v52
	v_and_b32_e32 v126, s8, v52
	v_lshrrev_b32_e32 v127, 24, v52
	v_and_b32_e32 v128, s6, v53
	v_and_b32_e32 v129, s7, v53
	v_and_b32_e32 v130, s8, v53
	v_lshrrev_b32_e32 v131, 24, v53
	s_lshl_b32 s30, s82, 12
	s_add_u32 s28, s26, s30
	s_addc_u32 s29, s27, 0
	global_load_dwordx2 v[52:53], v162, s[28:29]
	v_fmac_f32_e32 v178, s25, v124
	v_fmac_f32_e32 v179, s25, v125
	v_fmac_f32_e32 v180, s25, v126
	v_fmac_f32_e32 v181, s25, v127
	v_fmac_f32_e32 v182, s25, v128
	v_fmac_f32_e32 v183, s25, v129
	v_fmac_f32_e32 v184, s25, v130
	v_fmac_f32_e32 v185, s25, v131
	v_readlane_b32 s25, v246, 47
	v_and_b32_e32 v132, s6, v54
	v_and_b32_e32 v133, s7, v54
	v_and_b32_e32 v134, s8, v54
	v_lshrrev_b32_e32 v135, 24, v54
	v_and_b32_e32 v136, s6, v55
	v_and_b32_e32 v137, s7, v55
	v_and_b32_e32 v138, s8, v55
	v_lshrrev_b32_e32 v139, 24, v55
	s_lshl_b32 s30, s83, 12
	s_add_u32 s28, s26, s30
	s_addc_u32 s29, s27, 0
	global_load_dwordx2 v[54:55], v162, s[28:29]
	v_fmac_f32_e32 v178, s25, v132
	v_fmac_f32_e32 v179, s25, v133
	v_fmac_f32_e32 v180, s25, v134
	v_fmac_f32_e32 v181, s25, v135
	v_fmac_f32_e32 v182, s25, v136
	v_fmac_f32_e32 v183, s25, v137
	v_fmac_f32_e32 v184, s25, v138
	v_fmac_f32_e32 v185, s25, v139
	s_waitcnt vmcnt(28)
	v_readlane_b32 s25, v246, 48
	v_and_b32_e32 v124, s6, v56
	v_and_b32_e32 v125, s7, v56
	v_and_b32_e32 v126, s8, v56
	v_lshrrev_b32_e32 v127, 24, v56
	v_and_b32_e32 v128, s6, v57
	v_and_b32_e32 v129, s7, v57
	v_and_b32_e32 v130, s8, v57
	v_lshrrev_b32_e32 v131, 24, v57
	s_waitcnt lgkmcnt(0)
	s_load_dwordx16 s[68:83], s[36:37], 0x180 glc
	s_lshl_b32 s30, s84, 12
	s_add_u32 s28, s26, s30
	s_addc_u32 s29, s27, 0
	global_load_dwordx2 v[56:57], v162, s[28:29]
	v_fmac_f32_e32 v178, s25, v124
	v_fmac_f32_e32 v179, s25, v125
	v_fmac_f32_e32 v180, s25, v126
	v_fmac_f32_e32 v181, s25, v127
	v_fmac_f32_e32 v182, s25, v128
	v_fmac_f32_e32 v183, s25, v129
	v_fmac_f32_e32 v184, s25, v130
	v_fmac_f32_e32 v185, s25, v131
	v_readlane_b32 s25, v246, 49
	v_and_b32_e32 v132, s6, v58
	v_and_b32_e32 v133, s7, v58
	v_and_b32_e32 v134, s8, v58
	v_lshrrev_b32_e32 v135, 24, v58
	v_and_b32_e32 v136, s6, v59
	v_and_b32_e32 v137, s7, v59
	v_and_b32_e32 v138, s8, v59
	v_lshrrev_b32_e32 v139, 24, v59
	s_lshl_b32 s30, s85, 12
	s_add_u32 s28, s26, s30
	s_addc_u32 s29, s27, 0
	global_load_dwordx2 v[58:59], v162, s[28:29]
	v_fmac_f32_e32 v178, s25, v132
	v_fmac_f32_e32 v179, s25, v133
	v_fmac_f32_e32 v180, s25, v134
	v_fmac_f32_e32 v181, s25, v135
	v_fmac_f32_e32 v182, s25, v136
	v_fmac_f32_e32 v183, s25, v137
	v_fmac_f32_e32 v184, s25, v138
	v_fmac_f32_e32 v185, s25, v139
	v_readlane_b32 s25, v246, 50
	v_and_b32_e32 v124, s6, v60
	v_and_b32_e32 v125, s7, v60
	v_and_b32_e32 v126, s8, v60
	v_lshrrev_b32_e32 v127, 24, v60
	v_and_b32_e32 v128, s6, v61
	v_and_b32_e32 v129, s7, v61
	v_and_b32_e32 v130, s8, v61
	v_lshrrev_b32_e32 v131, 24, v61
	s_lshl_b32 s30, s86, 12
	s_add_u32 s28, s26, s30
	s_addc_u32 s29, s27, 0
	global_load_dwordx2 v[60:61], v162, s[28:29]
	v_fmac_f32_e32 v178, s25, v124
	v_fmac_f32_e32 v179, s25, v125
	v_fmac_f32_e32 v180, s25, v126
	v_fmac_f32_e32 v181, s25, v127
	v_fmac_f32_e32 v182, s25, v128
	v_fmac_f32_e32 v183, s25, v129
	v_fmac_f32_e32 v184, s25, v130
	v_fmac_f32_e32 v185, s25, v131
	v_readlane_b32 s25, v246, 51
	v_and_b32_e32 v132, s6, v62
	v_and_b32_e32 v133, s7, v62
	v_and_b32_e32 v134, s8, v62
	v_lshrrev_b32_e32 v135, 24, v62
	v_and_b32_e32 v136, s6, v63
	v_and_b32_e32 v137, s7, v63
	v_and_b32_e32 v138, s8, v63
	v_lshrrev_b32_e32 v139, 24, v63
	s_lshl_b32 s30, s87, 12
	s_add_u32 s28, s26, s30
	s_addc_u32 s29, s27, 0
	global_load_dwordx2 v[62:63], v162, s[28:29]
	v_fmac_f32_e32 v178, s25, v132
	v_fmac_f32_e32 v179, s25, v133
	v_fmac_f32_e32 v180, s25, v134
	v_fmac_f32_e32 v181, s25, v135
	v_fmac_f32_e32 v182, s25, v136
	v_fmac_f32_e32 v183, s25, v137
	v_fmac_f32_e32 v184, s25, v138
	v_fmac_f32_e32 v185, s25, v139
	s_waitcnt vmcnt(28)
	v_readlane_b32 s25, v246, 52
	v_and_b32_e32 v124, s6, v64
	v_and_b32_e32 v125, s7, v64
	v_and_b32_e32 v126, s8, v64
	v_lshrrev_b32_e32 v127, 24, v64
	v_and_b32_e32 v128, s6, v65
	v_and_b32_e32 v129, s7, v65
	v_and_b32_e32 v130, s8, v65
	v_lshrrev_b32_e32 v131, 24, v65
	s_lshl_b32 s30, s88, 12
	s_add_u32 s28, s26, s30
	s_addc_u32 s29, s27, 0
	global_load_dwordx2 v[64:65], v162, s[28:29]
	v_fmac_f32_e32 v178, s25, v124
	v_fmac_f32_e32 v179, s25, v125
	v_fmac_f32_e32 v180, s25, v126
	v_fmac_f32_e32 v181, s25, v127
	v_fmac_f32_e32 v182, s25, v128
	v_fmac_f32_e32 v183, s25, v129
	v_fmac_f32_e32 v184, s25, v130
	v_fmac_f32_e32 v185, s25, v131
	v_readlane_b32 s25, v246, 53
	v_and_b32_e32 v132, s6, v66
	v_and_b32_e32 v133, s7, v66
	v_and_b32_e32 v134, s8, v66
	v_lshrrev_b32_e32 v135, 24, v66
	v_and_b32_e32 v136, s6, v67
	v_and_b32_e32 v137, s7, v67
	v_and_b32_e32 v138, s8, v67
	v_lshrrev_b32_e32 v139, 24, v67
	s_lshl_b32 s30, s89, 12
	s_add_u32 s28, s26, s30
	s_addc_u32 s29, s27, 0
	global_load_dwordx2 v[66:67], v162, s[28:29]
	v_fmac_f32_e32 v178, s25, v132
	v_fmac_f32_e32 v179, s25, v133
	v_fmac_f32_e32 v180, s25, v134
	v_fmac_f32_e32 v181, s25, v135
	v_fmac_f32_e32 v182, s25, v136
	v_fmac_f32_e32 v183, s25, v137
	v_fmac_f32_e32 v184, s25, v138
	v_fmac_f32_e32 v185, s25, v139
	v_readlane_b32 s25, v246, 54
	v_and_b32_e32 v124, s6, v68
	v_and_b32_e32 v125, s7, v68
	v_and_b32_e32 v126, s8, v68
	v_lshrrev_b32_e32 v127, 24, v68
	v_and_b32_e32 v128, s6, v69
	v_and_b32_e32 v129, s7, v69
	v_and_b32_e32 v130, s8, v69
	v_lshrrev_b32_e32 v131, 24, v69
	s_lshl_b32 s30, s90, 12
	s_add_u32 s28, s26, s30
	s_addc_u32 s29, s27, 0
	global_load_dwordx2 v[68:69], v162, s[28:29]
	v_fmac_f32_e32 v178, s25, v124
	v_fmac_f32_e32 v179, s25, v125
	v_fmac_f32_e32 v180, s25, v126
	v_fmac_f32_e32 v181, s25, v127
	v_fmac_f32_e32 v182, s25, v128
	v_fmac_f32_e32 v183, s25, v129
	v_fmac_f32_e32 v184, s25, v130
	v_fmac_f32_e32 v185, s25, v131
	v_readlane_b32 s25, v246, 55
	v_and_b32_e32 v132, s6, v70
	v_and_b32_e32 v133, s7, v70
	v_and_b32_e32 v134, s8, v70
	v_lshrrev_b32_e32 v135, 24, v70
	v_and_b32_e32 v136, s6, v71
	v_and_b32_e32 v137, s7, v71
	v_and_b32_e32 v138, s8, v71
	v_lshrrev_b32_e32 v139, 24, v71
	s_lshl_b32 s30, s91, 12
	s_add_u32 s28, s26, s30
	s_addc_u32 s29, s27, 0
	global_load_dwordx2 v[70:71], v162, s[28:29]
	v_fmac_f32_e32 v178, s25, v132
	v_fmac_f32_e32 v179, s25, v133
	v_fmac_f32_e32 v180, s25, v134
	v_fmac_f32_e32 v181, s25, v135
	v_fmac_f32_e32 v182, s25, v136
	v_fmac_f32_e32 v183, s25, v137
	v_fmac_f32_e32 v184, s25, v138
	v_fmac_f32_e32 v185, s25, v139
	s_waitcnt vmcnt(28)
	v_readlane_b32 s25, v246, 56
	v_and_b32_e32 v124, s6, v72
	v_and_b32_e32 v125, s7, v72
	v_and_b32_e32 v126, s8, v72
	v_lshrrev_b32_e32 v127, 24, v72
	v_and_b32_e32 v128, s6, v73
	v_and_b32_e32 v129, s7, v73
	v_and_b32_e32 v130, s8, v73
	v_lshrrev_b32_e32 v131, 24, v73
	s_lshl_b32 s30, s92, 12
	s_add_u32 s28, s26, s30
	s_addc_u32 s29, s27, 0
	global_load_dwordx2 v[72:73], v162, s[28:29]
	v_fmac_f32_e32 v178, s25, v124
	v_fmac_f32_e32 v179, s25, v125
	v_fmac_f32_e32 v180, s25, v126
	v_fmac_f32_e32 v181, s25, v127
	v_fmac_f32_e32 v182, s25, v128
	v_fmac_f32_e32 v183, s25, v129
	v_fmac_f32_e32 v184, s25, v130
	v_fmac_f32_e32 v185, s25, v131
	v_readlane_b32 s25, v246, 57
	v_and_b32_e32 v132, s6, v74
	v_and_b32_e32 v133, s7, v74
	v_and_b32_e32 v134, s8, v74
	v_lshrrev_b32_e32 v135, 24, v74
	v_and_b32_e32 v136, s6, v75
	v_and_b32_e32 v137, s7, v75
	v_and_b32_e32 v138, s8, v75
	v_lshrrev_b32_e32 v139, 24, v75
	s_lshl_b32 s30, s93, 12
	s_add_u32 s28, s26, s30
	s_addc_u32 s29, s27, 0
	global_load_dwordx2 v[74:75], v162, s[28:29]
	v_fmac_f32_e32 v178, s25, v132
	v_fmac_f32_e32 v179, s25, v133
	v_fmac_f32_e32 v180, s25, v134
	v_fmac_f32_e32 v181, s25, v135
	v_fmac_f32_e32 v182, s25, v136
	v_fmac_f32_e32 v183, s25, v137
	v_fmac_f32_e32 v184, s25, v138
	v_fmac_f32_e32 v185, s25, v139
	v_readlane_b32 s25, v246, 58
	v_and_b32_e32 v124, s6, v76
	v_and_b32_e32 v125, s7, v76
	v_and_b32_e32 v126, s8, v76
	v_lshrrev_b32_e32 v127, 24, v76
	v_and_b32_e32 v128, s6, v77
	v_and_b32_e32 v129, s7, v77
	v_and_b32_e32 v130, s8, v77
	v_lshrrev_b32_e32 v131, 24, v77
	s_lshl_b32 s30, s94, 12
	s_add_u32 s28, s26, s30
	s_addc_u32 s29, s27, 0
	global_load_dwordx2 v[76:77], v162, s[28:29]
	v_fmac_f32_e32 v178, s25, v124
	v_fmac_f32_e32 v179, s25, v125
	v_fmac_f32_e32 v180, s25, v126
	v_fmac_f32_e32 v181, s25, v127
	v_fmac_f32_e32 v182, s25, v128
	v_fmac_f32_e32 v183, s25, v129
	v_fmac_f32_e32 v184, s25, v130
	v_fmac_f32_e32 v185, s25, v131
	v_readlane_b32 s25, v246, 59
	v_and_b32_e32 v132, s6, v78
	v_and_b32_e32 v133, s7, v78
	v_and_b32_e32 v134, s8, v78
	v_lshrrev_b32_e32 v135, 24, v78
	v_and_b32_e32 v136, s6, v79
	v_and_b32_e32 v137, s7, v79
	v_and_b32_e32 v138, s8, v79
	v_lshrrev_b32_e32 v139, 24, v79
	s_lshl_b32 s30, s95, 12
	s_add_u32 s28, s26, s30
	s_addc_u32 s29, s27, 0
	global_load_dwordx2 v[78:79], v162, s[28:29]
	v_fmac_f32_e32 v178, s25, v132
	v_fmac_f32_e32 v179, s25, v133
	v_fmac_f32_e32 v180, s25, v134
	v_fmac_f32_e32 v181, s25, v135
	v_fmac_f32_e32 v182, s25, v136
	v_fmac_f32_e32 v183, s25, v137
	v_fmac_f32_e32 v184, s25, v138
	v_fmac_f32_e32 v185, s25, v139
	s_waitcnt vmcnt(28)
	v_readlane_b32 s25, v246, 60
	v_and_b32_e32 v124, s6, v80
	v_and_b32_e32 v125, s7, v80
	v_and_b32_e32 v126, s8, v80
	v_lshrrev_b32_e32 v127, 24, v80
	v_and_b32_e32 v128, s6, v81
	v_and_b32_e32 v129, s7, v81
	v_and_b32_e32 v130, s8, v81
	v_lshrrev_b32_e32 v131, 24, v81
	s_lshl_b32 s30, s96, 12
	s_add_u32 s28, s26, s30
	s_addc_u32 s29, s27, 0
	global_load_dwordx2 v[80:81], v162, s[28:29]
	v_fmac_f32_e32 v178, s25, v124
	v_fmac_f32_e32 v179, s25, v125
	v_fmac_f32_e32 v180, s25, v126
	v_fmac_f32_e32 v181, s25, v127
	v_fmac_f32_e32 v182, s25, v128
	v_fmac_f32_e32 v183, s25, v129
	v_fmac_f32_e32 v184, s25, v130
	v_fmac_f32_e32 v185, s25, v131
	v_readlane_b32 s25, v246, 61
	v_and_b32_e32 v132, s6, v82
	v_and_b32_e32 v133, s7, v82
	v_and_b32_e32 v134, s8, v82
	v_lshrrev_b32_e32 v135, 24, v82
	v_and_b32_e32 v136, s6, v83
	v_and_b32_e32 v137, s7, v83
	v_and_b32_e32 v138, s8, v83
	v_lshrrev_b32_e32 v139, 24, v83
	s_lshl_b32 s30, s97, 12
	s_add_u32 s28, s26, s30
	s_addc_u32 s29, s27, 0
	global_load_dwordx2 v[82:83], v162, s[28:29]
	v_fmac_f32_e32 v178, s25, v132
	v_fmac_f32_e32 v179, s25, v133
	v_fmac_f32_e32 v180, s25, v134
	v_fmac_f32_e32 v181, s25, v135
	v_fmac_f32_e32 v182, s25, v136
	v_fmac_f32_e32 v183, s25, v137
	v_fmac_f32_e32 v184, s25, v138
	v_fmac_f32_e32 v185, s25, v139
	v_readlane_b32 s25, v246, 62
	v_and_b32_e32 v124, s6, v84
	v_and_b32_e32 v125, s7, v84
	v_and_b32_e32 v126, s8, v84
	v_lshrrev_b32_e32 v127, 24, v84
	v_and_b32_e32 v128, s6, v85
	v_and_b32_e32 v129, s7, v85
	v_and_b32_e32 v130, s8, v85
	v_lshrrev_b32_e32 v131, 24, v85
	s_lshl_b32 s30, s98, 12
	s_add_u32 s28, s26, s30
	s_addc_u32 s29, s27, 0
	global_load_dwordx2 v[84:85], v162, s[28:29]
	v_fmac_f32_e32 v178, s25, v124
	v_fmac_f32_e32 v179, s25, v125
	v_fmac_f32_e32 v180, s25, v126
	v_fmac_f32_e32 v181, s25, v127
	v_fmac_f32_e32 v182, s25, v128
	v_fmac_f32_e32 v183, s25, v129
	v_fmac_f32_e32 v184, s25, v130
	v_fmac_f32_e32 v185, s25, v131
	v_readlane_b32 s25, v246, 63
	v_and_b32_e32 v132, s6, v86
	v_and_b32_e32 v133, s7, v86
	v_and_b32_e32 v134, s8, v86
	v_lshrrev_b32_e32 v135, 24, v86
	v_and_b32_e32 v136, s6, v87
	v_and_b32_e32 v137, s7, v87
	v_and_b32_e32 v138, s8, v87
	v_lshrrev_b32_e32 v139, 24, v87
	s_lshl_b32 s30, s99, 12
	s_add_u32 s28, s26, s30
	s_addc_u32 s29, s27, 0
	global_load_dwordx2 v[86:87], v162, s[28:29]
	v_fmac_f32_e32 v178, s25, v132
	v_fmac_f32_e32 v179, s25, v133
	v_fmac_f32_e32 v180, s25, v134
	v_fmac_f32_e32 v181, s25, v135
	v_fmac_f32_e32 v182, s25, v136
	v_fmac_f32_e32 v183, s25, v137
	v_fmac_f32_e32 v184, s25, v138
	v_fmac_f32_e32 v185, s25, v139
	s_waitcnt vmcnt(28)
	v_readlane_b32 s25, v247, 0
	v_and_b32_e32 v124, s6, v24
	v_and_b32_e32 v125, s7, v24
	v_and_b32_e32 v126, s8, v24
	v_lshrrev_b32_e32 v127, 24, v24
	v_and_b32_e32 v128, s6, v25
	v_and_b32_e32 v129, s7, v25
	v_and_b32_e32 v130, s8, v25
	v_lshrrev_b32_e32 v131, 24, v25
	s_waitcnt lgkmcnt(0)
	s_load_dwordx16 s[84:99], s[36:37], 0x1c0 glc
	s_lshl_b32 s30, s68, 12
	s_add_u32 s28, s26, s30
	s_addc_u32 s29, s27, 0
	global_load_dwordx2 v[24:25], v162, s[28:29]
	v_lshlrev_b32_e32 v16, 2, v122
	v_lshlrev_b32_e32 v17, 2, v123
	global_load_dword v238, v16, s[64:65]
	global_load_dword v240, v16, s[60:61]
	global_load_dword v239, v17, s[64:65]
	global_load_dword v241, v17, s[60:61]
	v_fmac_f32_e32 v178, s25, v124
	v_fmac_f32_e32 v179, s25, v125
	v_fmac_f32_e32 v180, s25, v126
	v_fmac_f32_e32 v181, s25, v127
	v_fmac_f32_e32 v182, s25, v128
	v_fmac_f32_e32 v183, s25, v129
	v_fmac_f32_e32 v184, s25, v130
	v_fmac_f32_e32 v185, s25, v131
	v_readlane_b32 s25, v247, 1
	v_and_b32_e32 v132, s6, v26
	v_and_b32_e32 v133, s7, v26
	v_and_b32_e32 v134, s8, v26
	v_lshrrev_b32_e32 v135, 24, v26
	v_and_b32_e32 v136, s6, v27
	v_and_b32_e32 v137, s7, v27
	v_and_b32_e32 v138, s8, v27
	v_lshrrev_b32_e32 v139, 24, v27
	s_lshl_b32 s30, s69, 12
	s_add_u32 s28, s26, s30
	s_addc_u32 s29, s27, 0
	global_load_dwordx2 v[26:27], v162, s[28:29]
	v_fmac_f32_e32 v178, s25, v132
	v_fmac_f32_e32 v179, s25, v133
	v_fmac_f32_e32 v180, s25, v134
	v_fmac_f32_e32 v181, s25, v135
	v_fmac_f32_e32 v182, s25, v136
	v_fmac_f32_e32 v183, s25, v137
	v_fmac_f32_e32 v184, s25, v138
	v_fmac_f32_e32 v185, s25, v139
	v_readlane_b32 s25, v247, 2
	v_and_b32_e32 v124, s6, v28
	v_and_b32_e32 v125, s7, v28
	v_and_b32_e32 v126, s8, v28
	v_lshrrev_b32_e32 v127, 24, v28
	v_and_b32_e32 v128, s6, v29
	v_and_b32_e32 v129, s7, v29
	v_and_b32_e32 v130, s8, v29
	v_lshrrev_b32_e32 v131, 24, v29
	s_lshl_b32 s30, s70, 12
	s_add_u32 s28, s26, s30
	s_addc_u32 s29, s27, 0
	global_load_dwordx2 v[28:29], v162, s[28:29]
	v_fmac_f32_e32 v178, s25, v124
	v_fmac_f32_e32 v179, s25, v125
	v_fmac_f32_e32 v180, s25, v126
	v_fmac_f32_e32 v181, s25, v127
	v_fmac_f32_e32 v182, s25, v128
	v_fmac_f32_e32 v183, s25, v129
	v_fmac_f32_e32 v184, s25, v130
	v_fmac_f32_e32 v185, s25, v131
	v_readlane_b32 s25, v247, 3
	v_and_b32_e32 v132, s6, v30
	v_and_b32_e32 v133, s7, v30
	v_and_b32_e32 v134, s8, v30
	v_lshrrev_b32_e32 v135, 24, v30
	v_and_b32_e32 v136, s6, v31
	v_and_b32_e32 v137, s7, v31
	v_and_b32_e32 v138, s8, v31
	v_lshrrev_b32_e32 v139, 24, v31
	s_lshl_b32 s30, s71, 12
	s_add_u32 s28, s26, s30
	s_addc_u32 s29, s27, 0
	global_load_dwordx2 v[30:31], v162, s[28:29]
	v_fmac_f32_e32 v178, s25, v132
	v_fmac_f32_e32 v179, s25, v133
	v_fmac_f32_e32 v180, s25, v134
	v_fmac_f32_e32 v181, s25, v135
	v_fmac_f32_e32 v182, s25, v136
	v_fmac_f32_e32 v183, s25, v137
	v_fmac_f32_e32 v184, s25, v138
	v_fmac_f32_e32 v185, s25, v139
	s_waitcnt vmcnt(32)
	v_readlane_b32 s25, v247, 4
	v_and_b32_e32 v124, s6, v32
	v_and_b32_e32 v125, s7, v32
	v_and_b32_e32 v126, s8, v32
	v_lshrrev_b32_e32 v127, 24, v32
	v_and_b32_e32 v128, s6, v33
	v_and_b32_e32 v129, s7, v33
	v_and_b32_e32 v130, s8, v33
	v_lshrrev_b32_e32 v131, 24, v33
	s_lshl_b32 s30, s72, 12
	s_add_u32 s28, s26, s30
	s_addc_u32 s29, s27, 0
	global_load_dwordx2 v[32:33], v162, s[28:29]
	v_fmac_f32_e32 v178, s25, v124
	v_fmac_f32_e32 v179, s25, v125
	v_fmac_f32_e32 v180, s25, v126
	v_fmac_f32_e32 v181, s25, v127
	v_fmac_f32_e32 v182, s25, v128
	v_fmac_f32_e32 v183, s25, v129
	v_fmac_f32_e32 v184, s25, v130
	v_fmac_f32_e32 v185, s25, v131
	v_readlane_b32 s25, v247, 5
	v_and_b32_e32 v132, s6, v34
	v_and_b32_e32 v133, s7, v34
	v_and_b32_e32 v134, s8, v34
	v_lshrrev_b32_e32 v135, 24, v34
	v_and_b32_e32 v136, s6, v35
	v_and_b32_e32 v137, s7, v35
	v_and_b32_e32 v138, s8, v35
	v_lshrrev_b32_e32 v139, 24, v35
	s_lshl_b32 s30, s73, 12
	s_add_u32 s28, s26, s30
	s_addc_u32 s29, s27, 0
	global_load_dwordx2 v[34:35], v162, s[28:29]
	v_fmac_f32_e32 v178, s25, v132
	v_fmac_f32_e32 v179, s25, v133
	v_fmac_f32_e32 v180, s25, v134
	v_fmac_f32_e32 v181, s25, v135
	v_fmac_f32_e32 v182, s25, v136
	v_fmac_f32_e32 v183, s25, v137
	v_fmac_f32_e32 v184, s25, v138
	v_fmac_f32_e32 v185, s25, v139
	v_readlane_b32 s25, v247, 6
	v_and_b32_e32 v124, s6, v36
	v_and_b32_e32 v125, s7, v36
	v_and_b32_e32 v126, s8, v36
	v_lshrrev_b32_e32 v127, 24, v36
	v_and_b32_e32 v128, s6, v37
	v_and_b32_e32 v129, s7, v37
	v_and_b32_e32 v130, s8, v37
	v_lshrrev_b32_e32 v131, 24, v37
	s_lshl_b32 s30, s74, 12
	s_add_u32 s28, s26, s30
	s_addc_u32 s29, s27, 0
	global_load_dwordx2 v[36:37], v162, s[28:29]
	v_fmac_f32_e32 v178, s25, v124
	v_fmac_f32_e32 v179, s25, v125
	v_fmac_f32_e32 v180, s25, v126
	v_fmac_f32_e32 v181, s25, v127
	v_fmac_f32_e32 v182, s25, v128
	v_fmac_f32_e32 v183, s25, v129
	v_fmac_f32_e32 v184, s25, v130
	v_fmac_f32_e32 v185, s25, v131
	v_readlane_b32 s25, v247, 7
	v_and_b32_e32 v132, s6, v38
	v_and_b32_e32 v133, s7, v38
	v_and_b32_e32 v134, s8, v38
	v_lshrrev_b32_e32 v135, 24, v38
	v_and_b32_e32 v136, s6, v39
	v_and_b32_e32 v137, s7, v39
	v_and_b32_e32 v138, s8, v39
	v_lshrrev_b32_e32 v139, 24, v39
	s_lshl_b32 s30, s75, 12
	s_add_u32 s28, s26, s30
	s_addc_u32 s29, s27, 0
	global_load_dwordx2 v[38:39], v162, s[28:29]
	v_fmac_f32_e32 v178, s25, v132
	v_fmac_f32_e32 v179, s25, v133
	v_fmac_f32_e32 v180, s25, v134
	v_fmac_f32_e32 v181, s25, v135
	v_fmac_f32_e32 v182, s25, v136
	v_fmac_f32_e32 v183, s25, v137
	v_fmac_f32_e32 v184, s25, v138
	v_fmac_f32_e32 v185, s25, v139
	s_waitcnt vmcnt(32)
	v_readlane_b32 s25, v247, 8
	v_and_b32_e32 v124, s6, v40
	v_and_b32_e32 v125, s7, v40
	v_and_b32_e32 v126, s8, v40
	v_lshrrev_b32_e32 v127, 24, v40
	v_and_b32_e32 v128, s6, v41
	v_and_b32_e32 v129, s7, v41
	v_and_b32_e32 v130, s8, v41
	v_lshrrev_b32_e32 v131, 24, v41
	s_lshl_b32 s30, s76, 12
	s_add_u32 s28, s26, s30
	s_addc_u32 s29, s27, 0
	global_load_dwordx2 v[40:41], v162, s[28:29]
	v_fmac_f32_e32 v178, s25, v124
	v_fmac_f32_e32 v179, s25, v125
	v_fmac_f32_e32 v180, s25, v126
	v_fmac_f32_e32 v181, s25, v127
	v_fmac_f32_e32 v182, s25, v128
	v_fmac_f32_e32 v183, s25, v129
	v_fmac_f32_e32 v184, s25, v130
	v_fmac_f32_e32 v185, s25, v131
	v_readlane_b32 s25, v247, 9
	v_and_b32_e32 v132, s6, v42
	v_and_b32_e32 v133, s7, v42
	v_and_b32_e32 v134, s8, v42
	v_lshrrev_b32_e32 v135, 24, v42
	v_and_b32_e32 v136, s6, v43
	v_and_b32_e32 v137, s7, v43
	v_and_b32_e32 v138, s8, v43
	v_lshrrev_b32_e32 v139, 24, v43
	s_lshl_b32 s30, s77, 12
	s_add_u32 s28, s26, s30
	s_addc_u32 s29, s27, 0
	global_load_dwordx2 v[42:43], v162, s[28:29]
	v_fmac_f32_e32 v178, s25, v132
	v_fmac_f32_e32 v179, s25, v133
	v_fmac_f32_e32 v180, s25, v134
	v_fmac_f32_e32 v181, s25, v135
	v_fmac_f32_e32 v182, s25, v136
	v_fmac_f32_e32 v183, s25, v137
	v_fmac_f32_e32 v184, s25, v138
	v_fmac_f32_e32 v185, s25, v139
	v_readlane_b32 s25, v247, 10
	v_and_b32_e32 v124, s6, v44
	v_and_b32_e32 v125, s7, v44
	v_and_b32_e32 v126, s8, v44
	v_lshrrev_b32_e32 v127, 24, v44
	v_and_b32_e32 v128, s6, v45
	v_and_b32_e32 v129, s7, v45
	v_and_b32_e32 v130, s8, v45
	v_lshrrev_b32_e32 v131, 24, v45
	s_lshl_b32 s30, s78, 12
	s_add_u32 s28, s26, s30
	s_addc_u32 s29, s27, 0
	global_load_dwordx2 v[44:45], v162, s[28:29]
	v_fmac_f32_e32 v178, s25, v124
	v_fmac_f32_e32 v179, s25, v125
	v_fmac_f32_e32 v180, s25, v126
	v_fmac_f32_e32 v181, s25, v127
	v_fmac_f32_e32 v182, s25, v128
	v_fmac_f32_e32 v183, s25, v129
	v_fmac_f32_e32 v184, s25, v130
	v_fmac_f32_e32 v185, s25, v131
	v_readlane_b32 s25, v247, 11
	v_and_b32_e32 v132, s6, v46
	v_and_b32_e32 v133, s7, v46
	v_and_b32_e32 v134, s8, v46
	v_lshrrev_b32_e32 v135, 24, v46
	v_and_b32_e32 v136, s6, v47
	v_and_b32_e32 v137, s7, v47
	v_and_b32_e32 v138, s8, v47
	v_lshrrev_b32_e32 v139, 24, v47
	s_lshl_b32 s30, s79, 12
	s_add_u32 s28, s26, s30
	s_addc_u32 s29, s27, 0
	global_load_dwordx2 v[46:47], v162, s[28:29]
	v_fmac_f32_e32 v178, s25, v132
	v_fmac_f32_e32 v179, s25, v133
	v_fmac_f32_e32 v180, s25, v134
	v_fmac_f32_e32 v181, s25, v135
	v_fmac_f32_e32 v182, s25, v136
	v_fmac_f32_e32 v183, s25, v137
	v_fmac_f32_e32 v184, s25, v138
	v_fmac_f32_e32 v185, s25, v139
	s_waitcnt vmcnt(32)
	v_readlane_b32 s25, v247, 12
	v_and_b32_e32 v124, s6, v48
	v_and_b32_e32 v125, s7, v48
	v_and_b32_e32 v126, s8, v48
	v_lshrrev_b32_e32 v127, 24, v48
	v_and_b32_e32 v128, s6, v49
	v_and_b32_e32 v129, s7, v49
	v_and_b32_e32 v130, s8, v49
	v_lshrrev_b32_e32 v131, 24, v49
	s_lshl_b32 s30, s80, 12
	s_add_u32 s28, s26, s30
	s_addc_u32 s29, s27, 0
	global_load_dwordx2 v[48:49], v162, s[28:29]
	v_fmac_f32_e32 v178, s25, v124
	v_fmac_f32_e32 v179, s25, v125
	v_fmac_f32_e32 v180, s25, v126
	v_fmac_f32_e32 v181, s25, v127
	v_fmac_f32_e32 v182, s25, v128
	v_fmac_f32_e32 v183, s25, v129
	v_fmac_f32_e32 v184, s25, v130
	v_fmac_f32_e32 v185, s25, v131
	v_readlane_b32 s25, v247, 13
	v_and_b32_e32 v132, s6, v50
	v_and_b32_e32 v133, s7, v50
	v_and_b32_e32 v134, s8, v50
	v_lshrrev_b32_e32 v135, 24, v50
	v_and_b32_e32 v136, s6, v51
	v_and_b32_e32 v137, s7, v51
	v_and_b32_e32 v138, s8, v51
	v_lshrrev_b32_e32 v139, 24, v51
	s_lshl_b32 s30, s81, 12
	s_add_u32 s28, s26, s30
	s_addc_u32 s29, s27, 0
	global_load_dwordx2 v[50:51], v162, s[28:29]
	v_fmac_f32_e32 v178, s25, v132
	v_fmac_f32_e32 v179, s25, v133
	v_fmac_f32_e32 v180, s25, v134
	v_fmac_f32_e32 v181, s25, v135
	v_fmac_f32_e32 v182, s25, v136
	v_fmac_f32_e32 v183, s25, v137
	v_fmac_f32_e32 v184, s25, v138
	v_fmac_f32_e32 v185, s25, v139
	v_readlane_b32 s25, v247, 14
	v_and_b32_e32 v124, s6, v52
	v_and_b32_e32 v125, s7, v52
	v_and_b32_e32 v126, s8, v52
	v_lshrrev_b32_e32 v127, 24, v52
	v_and_b32_e32 v128, s6, v53
	v_and_b32_e32 v129, s7, v53
	v_and_b32_e32 v130, s8, v53
	v_lshrrev_b32_e32 v131, 24, v53
	s_lshl_b32 s30, s82, 12
	s_add_u32 s28, s26, s30
	s_addc_u32 s29, s27, 0
	global_load_dwordx2 v[52:53], v162, s[28:29]
	v_fmac_f32_e32 v178, s25, v124
	v_fmac_f32_e32 v179, s25, v125
	v_fmac_f32_e32 v180, s25, v126
	v_fmac_f32_e32 v181, s25, v127
	v_fmac_f32_e32 v182, s25, v128
	v_fmac_f32_e32 v183, s25, v129
	v_fmac_f32_e32 v184, s25, v130
	v_fmac_f32_e32 v185, s25, v131
	v_readlane_b32 s25, v247, 15
	v_and_b32_e32 v132, s6, v54
	v_and_b32_e32 v133, s7, v54
	v_and_b32_e32 v134, s8, v54
	v_lshrrev_b32_e32 v135, 24, v54
	v_and_b32_e32 v136, s6, v55
	v_and_b32_e32 v137, s7, v55
	v_and_b32_e32 v138, s8, v55
	v_lshrrev_b32_e32 v139, 24, v55
	s_lshl_b32 s30, s83, 12
	s_add_u32 s28, s26, s30
	s_addc_u32 s29, s27, 0
	global_load_dwordx2 v[54:55], v162, s[28:29]
	v_fmac_f32_e32 v178, s25, v132
	v_fmac_f32_e32 v179, s25, v133
	v_fmac_f32_e32 v180, s25, v134
	v_fmac_f32_e32 v181, s25, v135
	v_fmac_f32_e32 v182, s25, v136
	v_fmac_f32_e32 v183, s25, v137
	v_fmac_f32_e32 v184, s25, v138
	v_fmac_f32_e32 v185, s25, v139
	s_waitcnt vmcnt(32)
	v_readlane_b32 s25, v247, 16
	v_and_b32_e32 v124, s6, v56
	v_and_b32_e32 v125, s7, v56
	v_and_b32_e32 v126, s8, v56
	v_lshrrev_b32_e32 v127, 24, v56
	v_and_b32_e32 v128, s6, v57
	v_and_b32_e32 v129, s7, v57
	v_and_b32_e32 v130, s8, v57
	v_lshrrev_b32_e32 v131, 24, v57
	s_waitcnt lgkmcnt(0)
	s_load_dwordx16 s[68:83], s[38:39], 0x0 glc
	s_lshl_b32 s30, s84, 12
	s_add_u32 s28, s26, s30
	s_addc_u32 s29, s27, 0
	global_load_dwordx2 v[56:57], v162, s[28:29]
	v_fmac_f32_e32 v178, s25, v124
	v_fmac_f32_e32 v179, s25, v125
	v_fmac_f32_e32 v180, s25, v126
	v_fmac_f32_e32 v181, s25, v127
	v_fmac_f32_e32 v182, s25, v128
	v_fmac_f32_e32 v183, s25, v129
	v_fmac_f32_e32 v184, s25, v130
	v_fmac_f32_e32 v185, s25, v131
	v_readlane_b32 s25, v247, 17
	v_and_b32_e32 v132, s6, v58
	v_and_b32_e32 v133, s7, v58
	v_and_b32_e32 v134, s8, v58
	v_lshrrev_b32_e32 v135, 24, v58
	v_and_b32_e32 v136, s6, v59
	v_and_b32_e32 v137, s7, v59
	v_and_b32_e32 v138, s8, v59
	v_lshrrev_b32_e32 v139, 24, v59
	s_lshl_b32 s30, s85, 12
	s_add_u32 s28, s26, s30
	s_addc_u32 s29, s27, 0
	global_load_dwordx2 v[58:59], v162, s[28:29]
	v_fmac_f32_e32 v178, s25, v132
	v_fmac_f32_e32 v179, s25, v133
	v_fmac_f32_e32 v180, s25, v134
	v_fmac_f32_e32 v181, s25, v135
	v_fmac_f32_e32 v182, s25, v136
	v_fmac_f32_e32 v183, s25, v137
	v_fmac_f32_e32 v184, s25, v138
	v_fmac_f32_e32 v185, s25, v139
	v_readlane_b32 s25, v247, 18
	v_and_b32_e32 v124, s6, v60
	v_and_b32_e32 v125, s7, v60
	v_and_b32_e32 v126, s8, v60
	v_lshrrev_b32_e32 v127, 24, v60
	v_and_b32_e32 v128, s6, v61
	v_and_b32_e32 v129, s7, v61
	v_and_b32_e32 v130, s8, v61
	v_lshrrev_b32_e32 v131, 24, v61
	s_lshl_b32 s30, s86, 12
	s_add_u32 s28, s26, s30
	s_addc_u32 s29, s27, 0
	global_load_dwordx2 v[60:61], v162, s[28:29]
	v_fmac_f32_e32 v178, s25, v124
	v_fmac_f32_e32 v179, s25, v125
	v_fmac_f32_e32 v180, s25, v126
	v_fmac_f32_e32 v181, s25, v127
	v_fmac_f32_e32 v182, s25, v128
	v_fmac_f32_e32 v183, s25, v129
	v_fmac_f32_e32 v184, s25, v130
	v_fmac_f32_e32 v185, s25, v131
	v_readlane_b32 s25, v247, 19
	v_and_b32_e32 v132, s6, v62
	v_and_b32_e32 v133, s7, v62
	v_and_b32_e32 v134, s8, v62
	v_lshrrev_b32_e32 v135, 24, v62
	v_and_b32_e32 v136, s6, v63
	v_and_b32_e32 v137, s7, v63
	v_and_b32_e32 v138, s8, v63
	v_lshrrev_b32_e32 v139, 24, v63
	s_lshl_b32 s30, s87, 12
	s_add_u32 s28, s26, s30
	s_addc_u32 s29, s27, 0
	global_load_dwordx2 v[62:63], v162, s[28:29]
	v_fmac_f32_e32 v178, s25, v132
	v_fmac_f32_e32 v179, s25, v133
	v_fmac_f32_e32 v180, s25, v134
	v_fmac_f32_e32 v181, s25, v135
	v_fmac_f32_e32 v182, s25, v136
	v_fmac_f32_e32 v183, s25, v137
	v_fmac_f32_e32 v184, s25, v138
	v_fmac_f32_e32 v185, s25, v139
	s_waitcnt vmcnt(32)
	v_readlane_b32 s25, v247, 20
	v_and_b32_e32 v124, s6, v64
	v_and_b32_e32 v125, s7, v64
	v_and_b32_e32 v126, s8, v64
	v_lshrrev_b32_e32 v127, 24, v64
	v_and_b32_e32 v128, s6, v65
	v_and_b32_e32 v129, s7, v65
	v_and_b32_e32 v130, s8, v65
	v_lshrrev_b32_e32 v131, 24, v65
	s_lshl_b32 s30, s88, 12
	s_add_u32 s28, s26, s30
	s_addc_u32 s29, s27, 0
	global_load_dwordx2 v[64:65], v162, s[28:29]
	v_fmac_f32_e32 v178, s25, v124
	v_fmac_f32_e32 v179, s25, v125
	v_fmac_f32_e32 v180, s25, v126
	v_fmac_f32_e32 v181, s25, v127
	v_fmac_f32_e32 v182, s25, v128
	v_fmac_f32_e32 v183, s25, v129
	v_fmac_f32_e32 v184, s25, v130
	v_fmac_f32_e32 v185, s25, v131
	v_readlane_b32 s25, v247, 21
	v_and_b32_e32 v132, s6, v66
	v_and_b32_e32 v133, s7, v66
	v_and_b32_e32 v134, s8, v66
	v_lshrrev_b32_e32 v135, 24, v66
	v_and_b32_e32 v136, s6, v67
	v_and_b32_e32 v137, s7, v67
	v_and_b32_e32 v138, s8, v67
	v_lshrrev_b32_e32 v139, 24, v67
	s_lshl_b32 s30, s89, 12
	s_add_u32 s28, s26, s30
	s_addc_u32 s29, s27, 0
	global_load_dwordx2 v[66:67], v162, s[28:29]
	v_fmac_f32_e32 v178, s25, v132
	v_fmac_f32_e32 v179, s25, v133
	v_fmac_f32_e32 v180, s25, v134
	v_fmac_f32_e32 v181, s25, v135
	v_fmac_f32_e32 v182, s25, v136
	v_fmac_f32_e32 v183, s25, v137
	v_fmac_f32_e32 v184, s25, v138
	v_fmac_f32_e32 v185, s25, v139
	v_readlane_b32 s25, v247, 22
	v_and_b32_e32 v124, s6, v68
	v_and_b32_e32 v125, s7, v68
	v_and_b32_e32 v126, s8, v68
	v_lshrrev_b32_e32 v127, 24, v68
	v_and_b32_e32 v128, s6, v69
	v_and_b32_e32 v129, s7, v69
	v_and_b32_e32 v130, s8, v69
	v_lshrrev_b32_e32 v131, 24, v69
	s_lshl_b32 s30, s90, 12
	s_add_u32 s28, s26, s30
	s_addc_u32 s29, s27, 0
	global_load_dwordx2 v[68:69], v162, s[28:29]
	v_fmac_f32_e32 v178, s25, v124
	v_fmac_f32_e32 v179, s25, v125
	v_fmac_f32_e32 v180, s25, v126
	v_fmac_f32_e32 v181, s25, v127
	v_fmac_f32_e32 v182, s25, v128
	v_fmac_f32_e32 v183, s25, v129
	v_fmac_f32_e32 v184, s25, v130
	v_fmac_f32_e32 v185, s25, v131
	v_readlane_b32 s25, v247, 23
	v_and_b32_e32 v132, s6, v70
	v_and_b32_e32 v133, s7, v70
	v_and_b32_e32 v134, s8, v70
	v_lshrrev_b32_e32 v135, 24, v70
	v_and_b32_e32 v136, s6, v71
	v_and_b32_e32 v137, s7, v71
	v_and_b32_e32 v138, s8, v71
	v_lshrrev_b32_e32 v139, 24, v71
	s_lshl_b32 s30, s91, 12
	s_add_u32 s28, s26, s30
	s_addc_u32 s29, s27, 0
	global_load_dwordx2 v[70:71], v162, s[28:29]
	v_fmac_f32_e32 v178, s25, v132
	v_fmac_f32_e32 v179, s25, v133
	v_fmac_f32_e32 v180, s25, v134
	v_fmac_f32_e32 v181, s25, v135
	v_fmac_f32_e32 v182, s25, v136
	v_fmac_f32_e32 v183, s25, v137
	v_fmac_f32_e32 v184, s25, v138
	v_fmac_f32_e32 v185, s25, v139
	s_waitcnt vmcnt(32)
	v_readlane_b32 s25, v247, 24
	v_and_b32_e32 v124, s6, v72
	v_and_b32_e32 v125, s7, v72
	v_and_b32_e32 v126, s8, v72
	v_lshrrev_b32_e32 v127, 24, v72
	v_and_b32_e32 v128, s6, v73
	v_and_b32_e32 v129, s7, v73
	v_and_b32_e32 v130, s8, v73
	v_lshrrev_b32_e32 v131, 24, v73
	s_lshl_b32 s30, s92, 12
	s_add_u32 s28, s26, s30
	s_addc_u32 s29, s27, 0
	global_load_dwordx2 v[72:73], v162, s[28:29]
	v_fmac_f32_e32 v178, s25, v124
	v_fmac_f32_e32 v179, s25, v125
	v_fmac_f32_e32 v180, s25, v126
	v_fmac_f32_e32 v181, s25, v127
	v_fmac_f32_e32 v182, s25, v128
	v_fmac_f32_e32 v183, s25, v129
	v_fmac_f32_e32 v184, s25, v130
	v_fmac_f32_e32 v185, s25, v131
	v_readlane_b32 s25, v247, 25
	v_and_b32_e32 v132, s6, v74
	v_and_b32_e32 v133, s7, v74
	v_and_b32_e32 v134, s8, v74
	v_lshrrev_b32_e32 v135, 24, v74
	v_and_b32_e32 v136, s6, v75
	v_and_b32_e32 v137, s7, v75
	v_and_b32_e32 v138, s8, v75
	v_lshrrev_b32_e32 v139, 24, v75
	s_lshl_b32 s30, s93, 12
	s_add_u32 s28, s26, s30
	s_addc_u32 s29, s27, 0
	global_load_dwordx2 v[74:75], v162, s[28:29]
	v_fmac_f32_e32 v178, s25, v132
	v_fmac_f32_e32 v179, s25, v133
	v_fmac_f32_e32 v180, s25, v134
	v_fmac_f32_e32 v181, s25, v135
	v_fmac_f32_e32 v182, s25, v136
	v_fmac_f32_e32 v183, s25, v137
	v_fmac_f32_e32 v184, s25, v138
	v_fmac_f32_e32 v185, s25, v139
	v_readlane_b32 s25, v247, 26
	v_and_b32_e32 v124, s6, v76
	v_and_b32_e32 v125, s7, v76
	v_and_b32_e32 v126, s8, v76
	v_lshrrev_b32_e32 v127, 24, v76
	v_and_b32_e32 v128, s6, v77
	v_and_b32_e32 v129, s7, v77
	v_and_b32_e32 v130, s8, v77
	v_lshrrev_b32_e32 v131, 24, v77
	s_lshl_b32 s30, s94, 12
	s_add_u32 s28, s26, s30
	s_addc_u32 s29, s27, 0
	global_load_dwordx2 v[76:77], v162, s[28:29]
	v_fmac_f32_e32 v178, s25, v124
	v_fmac_f32_e32 v179, s25, v125
	v_fmac_f32_e32 v180, s25, v126
	v_fmac_f32_e32 v181, s25, v127
	v_fmac_f32_e32 v182, s25, v128
	v_fmac_f32_e32 v183, s25, v129
	v_fmac_f32_e32 v184, s25, v130
	v_fmac_f32_e32 v185, s25, v131
	v_readlane_b32 s25, v247, 27
	v_and_b32_e32 v132, s6, v78
	v_and_b32_e32 v133, s7, v78
	v_and_b32_e32 v134, s8, v78
	v_lshrrev_b32_e32 v135, 24, v78
	v_and_b32_e32 v136, s6, v79
	v_and_b32_e32 v137, s7, v79
	v_and_b32_e32 v138, s8, v79
	v_lshrrev_b32_e32 v139, 24, v79
	s_lshl_b32 s30, s95, 12
	s_add_u32 s28, s26, s30
	s_addc_u32 s29, s27, 0
	global_load_dwordx2 v[78:79], v162, s[28:29]
	v_fmac_f32_e32 v178, s25, v132
	v_fmac_f32_e32 v179, s25, v133
	v_fmac_f32_e32 v180, s25, v134
	v_fmac_f32_e32 v181, s25, v135
	v_fmac_f32_e32 v182, s25, v136
	v_fmac_f32_e32 v183, s25, v137
	v_fmac_f32_e32 v184, s25, v138
	v_fmac_f32_e32 v185, s25, v139
	s_waitcnt vmcnt(32)
	v_readlane_b32 s25, v247, 28
	v_and_b32_e32 v124, s6, v80
	v_and_b32_e32 v125, s7, v80
	v_and_b32_e32 v126, s8, v80
	v_lshrrev_b32_e32 v127, 24, v80
	v_and_b32_e32 v128, s6, v81
	v_and_b32_e32 v129, s7, v81
	v_and_b32_e32 v130, s8, v81
	v_lshrrev_b32_e32 v131, 24, v81
	s_lshl_b32 s30, s96, 12
	s_add_u32 s28, s26, s30
	s_addc_u32 s29, s27, 0
	global_load_dwordx2 v[80:81], v162, s[28:29]
	v_fmac_f32_e32 v178, s25, v124
	v_fmac_f32_e32 v179, s25, v125
	v_fmac_f32_e32 v180, s25, v126
	v_fmac_f32_e32 v181, s25, v127
	v_fmac_f32_e32 v182, s25, v128
	v_fmac_f32_e32 v183, s25, v129
	v_fmac_f32_e32 v184, s25, v130
	v_fmac_f32_e32 v185, s25, v131
	v_readlane_b32 s25, v247, 29
	v_and_b32_e32 v132, s6, v82
	v_and_b32_e32 v133, s7, v82
	v_and_b32_e32 v134, s8, v82
	v_lshrrev_b32_e32 v135, 24, v82
	v_and_b32_e32 v136, s6, v83
	v_and_b32_e32 v137, s7, v83
	v_and_b32_e32 v138, s8, v83
	v_lshrrev_b32_e32 v139, 24, v83
	s_lshl_b32 s30, s97, 12
	s_add_u32 s28, s26, s30
	s_addc_u32 s29, s27, 0
	global_load_dwordx2 v[82:83], v162, s[28:29]
	v_fmac_f32_e32 v178, s25, v132
	v_fmac_f32_e32 v179, s25, v133
	v_fmac_f32_e32 v180, s25, v134
	v_fmac_f32_e32 v181, s25, v135
	v_fmac_f32_e32 v182, s25, v136
	v_fmac_f32_e32 v183, s25, v137
	v_fmac_f32_e32 v184, s25, v138
	v_fmac_f32_e32 v185, s25, v139
	v_readlane_b32 s25, v247, 30
	v_and_b32_e32 v124, s6, v84
	v_and_b32_e32 v125, s7, v84
	v_and_b32_e32 v126, s8, v84
	v_lshrrev_b32_e32 v127, 24, v84
	v_and_b32_e32 v128, s6, v85
	v_and_b32_e32 v129, s7, v85
	v_and_b32_e32 v130, s8, v85
	v_lshrrev_b32_e32 v131, 24, v85
	s_lshl_b32 s30, s98, 12
	s_add_u32 s28, s26, s30
	s_addc_u32 s29, s27, 0
	global_load_dwordx2 v[84:85], v162, s[28:29]
	v_fmac_f32_e32 v178, s25, v124
	v_fmac_f32_e32 v179, s25, v125
	v_fmac_f32_e32 v180, s25, v126
	v_fmac_f32_e32 v181, s25, v127
	v_fmac_f32_e32 v182, s25, v128
	v_fmac_f32_e32 v183, s25, v129
	v_fmac_f32_e32 v184, s25, v130
	v_fmac_f32_e32 v185, s25, v131
	v_readlane_b32 s25, v247, 31
	v_and_b32_e32 v132, s6, v86
	v_and_b32_e32 v133, s7, v86
	v_and_b32_e32 v134, s8, v86
	v_lshrrev_b32_e32 v135, 24, v86
	v_and_b32_e32 v136, s6, v87
	v_and_b32_e32 v137, s7, v87
	v_and_b32_e32 v138, s8, v87
	v_lshrrev_b32_e32 v139, 24, v87
	s_lshl_b32 s30, s99, 12
	s_add_u32 s28, s26, s30
	s_addc_u32 s29, s27, 0
	global_load_dwordx2 v[86:87], v162, s[28:29]
	v_fmac_f32_e32 v178, s25, v132
	v_fmac_f32_e32 v179, s25, v133
	v_fmac_f32_e32 v180, s25, v134
	v_fmac_f32_e32 v181, s25, v135
	v_fmac_f32_e32 v182, s25, v136
	v_fmac_f32_e32 v183, s25, v137
	v_fmac_f32_e32 v184, s25, v138
	v_fmac_f32_e32 v185, s25, v139
	s_waitcnt vmcnt(28)
	v_readlane_b32 s25, v247, 32
	v_and_b32_e32 v124, s6, v24
	v_and_b32_e32 v125, s7, v24
	v_and_b32_e32 v126, s8, v24
	v_lshrrev_b32_e32 v127, 24, v24
	v_and_b32_e32 v128, s6, v25
	v_and_b32_e32 v129, s7, v25
	v_and_b32_e32 v130, s8, v25
	v_lshrrev_b32_e32 v131, 24, v25
	v_fmac_f32_e32 v178, s25, v124
	v_fmac_f32_e32 v179, s25, v125
	v_fmac_f32_e32 v180, s25, v126
	v_fmac_f32_e32 v181, s25, v127
	v_fmac_f32_e32 v182, s25, v128
	v_fmac_f32_e32 v183, s25, v129
	v_fmac_f32_e32 v184, s25, v130
	v_fmac_f32_e32 v185, s25, v131
	v_readlane_b32 s25, v247, 33
	v_and_b32_e32 v132, s6, v26
	v_and_b32_e32 v133, s7, v26
	v_and_b32_e32 v134, s8, v26
	v_lshrrev_b32_e32 v135, 24, v26
	v_and_b32_e32 v136, s6, v27
	v_and_b32_e32 v137, s7, v27
	v_and_b32_e32 v138, s8, v27
	v_lshrrev_b32_e32 v139, 24, v27
	v_fmac_f32_e32 v178, s25, v132
	v_fmac_f32_e32 v179, s25, v133
	v_fmac_f32_e32 v180, s25, v134
	v_fmac_f32_e32 v181, s25, v135
	v_fmac_f32_e32 v182, s25, v136
	v_fmac_f32_e32 v183, s25, v137
	v_fmac_f32_e32 v184, s25, v138
	v_fmac_f32_e32 v185, s25, v139
	v_readlane_b32 s25, v247, 34
	v_and_b32_e32 v124, s6, v28
	v_and_b32_e32 v125, s7, v28
	v_and_b32_e32 v126, s8, v28
	v_lshrrev_b32_e32 v127, 24, v28
	v_and_b32_e32 v128, s6, v29
	v_and_b32_e32 v129, s7, v29
	v_and_b32_e32 v130, s8, v29
	v_lshrrev_b32_e32 v131, 24, v29
	v_fmac_f32_e32 v178, s25, v124
	v_fmac_f32_e32 v179, s25, v125
	v_fmac_f32_e32 v180, s25, v126
	v_fmac_f32_e32 v181, s25, v127
	v_fmac_f32_e32 v182, s25, v128
	v_fmac_f32_e32 v183, s25, v129
	v_fmac_f32_e32 v184, s25, v130
	v_fmac_f32_e32 v185, s25, v131
	v_readlane_b32 s25, v247, 35
	v_and_b32_e32 v132, s6, v30
	v_and_b32_e32 v133, s7, v30
	v_and_b32_e32 v134, s8, v30
	v_lshrrev_b32_e32 v135, 24, v30
	v_and_b32_e32 v136, s6, v31
	v_and_b32_e32 v137, s7, v31
	v_and_b32_e32 v138, s8, v31
	v_lshrrev_b32_e32 v139, 24, v31
	v_fmac_f32_e32 v178, s25, v132
	v_fmac_f32_e32 v179, s25, v133
	v_fmac_f32_e32 v180, s25, v134
	v_fmac_f32_e32 v181, s25, v135
	v_fmac_f32_e32 v182, s25, v136
	v_fmac_f32_e32 v183, s25, v137
	v_fmac_f32_e32 v184, s25, v138
	v_fmac_f32_e32 v185, s25, v139
	s_waitcnt vmcnt(24)
	v_readlane_b32 s25, v247, 36
	v_and_b32_e32 v124, s6, v32
	v_and_b32_e32 v125, s7, v32
	v_and_b32_e32 v126, s8, v32
	v_lshrrev_b32_e32 v127, 24, v32
	v_and_b32_e32 v128, s6, v33
	v_and_b32_e32 v129, s7, v33
	v_and_b32_e32 v130, s8, v33
	v_lshrrev_b32_e32 v131, 24, v33
	v_fmac_f32_e32 v178, s25, v124
	v_fmac_f32_e32 v179, s25, v125
	v_fmac_f32_e32 v180, s25, v126
	v_fmac_f32_e32 v181, s25, v127
	v_fmac_f32_e32 v182, s25, v128
	v_fmac_f32_e32 v183, s25, v129
	v_fmac_f32_e32 v184, s25, v130
	v_fmac_f32_e32 v185, s25, v131
	v_readlane_b32 s25, v247, 37
	v_and_b32_e32 v132, s6, v34
	v_and_b32_e32 v133, s7, v34
	v_and_b32_e32 v134, s8, v34
	v_lshrrev_b32_e32 v135, 24, v34
	v_and_b32_e32 v136, s6, v35
	v_and_b32_e32 v137, s7, v35
	v_and_b32_e32 v138, s8, v35
	v_lshrrev_b32_e32 v139, 24, v35
	v_fmac_f32_e32 v178, s25, v132
	v_fmac_f32_e32 v179, s25, v133
	v_fmac_f32_e32 v180, s25, v134
	v_fmac_f32_e32 v181, s25, v135
	v_fmac_f32_e32 v182, s25, v136
	v_fmac_f32_e32 v183, s25, v137
	v_fmac_f32_e32 v184, s25, v138
	v_fmac_f32_e32 v185, s25, v139
	v_readlane_b32 s25, v247, 38
	v_and_b32_e32 v124, s6, v36
	v_and_b32_e32 v125, s7, v36
	v_and_b32_e32 v126, s8, v36
	v_lshrrev_b32_e32 v127, 24, v36
	v_and_b32_e32 v128, s6, v37
	v_and_b32_e32 v129, s7, v37
	v_and_b32_e32 v130, s8, v37
	v_lshrrev_b32_e32 v131, 24, v37
	v_fmac_f32_e32 v178, s25, v124
	v_fmac_f32_e32 v179, s25, v125
	v_fmac_f32_e32 v180, s25, v126
	v_fmac_f32_e32 v181, s25, v127
	v_fmac_f32_e32 v182, s25, v128
	v_fmac_f32_e32 v183, s25, v129
	v_fmac_f32_e32 v184, s25, v130
	v_fmac_f32_e32 v185, s25, v131
	v_readlane_b32 s25, v247, 39
	v_and_b32_e32 v132, s6, v38
	v_and_b32_e32 v133, s7, v38
	v_and_b32_e32 v134, s8, v38
	v_lshrrev_b32_e32 v135, 24, v38
	v_and_b32_e32 v136, s6, v39
	v_and_b32_e32 v137, s7, v39
	v_and_b32_e32 v138, s8, v39
	v_lshrrev_b32_e32 v139, 24, v39
	v_fmac_f32_e32 v178, s25, v132
	v_fmac_f32_e32 v179, s25, v133
	v_fmac_f32_e32 v180, s25, v134
	v_fmac_f32_e32 v181, s25, v135
	v_fmac_f32_e32 v182, s25, v136
	v_fmac_f32_e32 v183, s25, v137
	v_fmac_f32_e32 v184, s25, v138
	v_fmac_f32_e32 v185, s25, v139
	s_waitcnt vmcnt(20)
	v_readlane_b32 s25, v247, 40
	v_and_b32_e32 v124, s6, v40
	v_and_b32_e32 v125, s7, v40
	v_and_b32_e32 v126, s8, v40
	v_lshrrev_b32_e32 v127, 24, v40
	v_and_b32_e32 v128, s6, v41
	v_and_b32_e32 v129, s7, v41
	v_and_b32_e32 v130, s8, v41
	v_lshrrev_b32_e32 v131, 24, v41
	v_fmac_f32_e32 v178, s25, v124
	v_fmac_f32_e32 v179, s25, v125
	v_fmac_f32_e32 v180, s25, v126
	v_fmac_f32_e32 v181, s25, v127
	v_fmac_f32_e32 v182, s25, v128
	v_fmac_f32_e32 v183, s25, v129
	v_fmac_f32_e32 v184, s25, v130
	v_fmac_f32_e32 v185, s25, v131
	v_readlane_b32 s25, v247, 41
	v_and_b32_e32 v132, s6, v42
	v_and_b32_e32 v133, s7, v42
	v_and_b32_e32 v134, s8, v42
	v_lshrrev_b32_e32 v135, 24, v42
	v_and_b32_e32 v136, s6, v43
	v_and_b32_e32 v137, s7, v43
	v_and_b32_e32 v138, s8, v43
	v_lshrrev_b32_e32 v139, 24, v43
	v_fmac_f32_e32 v178, s25, v132
	v_fmac_f32_e32 v179, s25, v133
	v_fmac_f32_e32 v180, s25, v134
	v_fmac_f32_e32 v181, s25, v135
	v_fmac_f32_e32 v182, s25, v136
	v_fmac_f32_e32 v183, s25, v137
	v_fmac_f32_e32 v184, s25, v138
	v_fmac_f32_e32 v185, s25, v139
	v_readlane_b32 s25, v247, 42
	v_and_b32_e32 v124, s6, v44
	v_and_b32_e32 v125, s7, v44
	v_and_b32_e32 v126, s8, v44
	v_lshrrev_b32_e32 v127, 24, v44
	v_and_b32_e32 v128, s6, v45
	v_and_b32_e32 v129, s7, v45
	v_and_b32_e32 v130, s8, v45
	v_lshrrev_b32_e32 v131, 24, v45
	v_fmac_f32_e32 v178, s25, v124
	v_fmac_f32_e32 v179, s25, v125
	v_fmac_f32_e32 v180, s25, v126
	v_fmac_f32_e32 v181, s25, v127
	v_fmac_f32_e32 v182, s25, v128
	v_fmac_f32_e32 v183, s25, v129
	v_fmac_f32_e32 v184, s25, v130
	v_fmac_f32_e32 v185, s25, v131
	v_readlane_b32 s25, v247, 43
	v_and_b32_e32 v132, s6, v46
	v_and_b32_e32 v133, s7, v46
	v_and_b32_e32 v134, s8, v46
	v_lshrrev_b32_e32 v135, 24, v46
	v_and_b32_e32 v136, s6, v47
	v_and_b32_e32 v137, s7, v47
	v_and_b32_e32 v138, s8, v47
	v_lshrrev_b32_e32 v139, 24, v47
	v_fmac_f32_e32 v178, s25, v132
	v_fmac_f32_e32 v179, s25, v133
	v_fmac_f32_e32 v180, s25, v134
	v_fmac_f32_e32 v181, s25, v135
	v_fmac_f32_e32 v182, s25, v136
	v_fmac_f32_e32 v183, s25, v137
	v_fmac_f32_e32 v184, s25, v138
	v_fmac_f32_e32 v185, s25, v139
	s_waitcnt vmcnt(16)
	v_readlane_b32 s25, v247, 44
	v_and_b32_e32 v124, s6, v48
	v_and_b32_e32 v125, s7, v48
	v_and_b32_e32 v126, s8, v48
	v_lshrrev_b32_e32 v127, 24, v48
	v_and_b32_e32 v128, s6, v49
	v_and_b32_e32 v129, s7, v49
	v_and_b32_e32 v130, s8, v49
	v_lshrrev_b32_e32 v131, 24, v49
	v_fmac_f32_e32 v178, s25, v124
	v_fmac_f32_e32 v179, s25, v125
	v_fmac_f32_e32 v180, s25, v126
	v_fmac_f32_e32 v181, s25, v127
	v_fmac_f32_e32 v182, s25, v128
	v_fmac_f32_e32 v183, s25, v129
	v_fmac_f32_e32 v184, s25, v130
	v_fmac_f32_e32 v185, s25, v131
	v_readlane_b32 s25, v247, 45
	v_and_b32_e32 v132, s6, v50
	v_and_b32_e32 v133, s7, v50
	v_and_b32_e32 v134, s8, v50
	v_lshrrev_b32_e32 v135, 24, v50
	v_and_b32_e32 v136, s6, v51
	v_and_b32_e32 v137, s7, v51
	v_and_b32_e32 v138, s8, v51
	v_lshrrev_b32_e32 v139, 24, v51
	v_fmac_f32_e32 v178, s25, v132
	v_fmac_f32_e32 v179, s25, v133
	v_fmac_f32_e32 v180, s25, v134
	v_fmac_f32_e32 v181, s25, v135
	v_fmac_f32_e32 v182, s25, v136
	v_fmac_f32_e32 v183, s25, v137
	v_fmac_f32_e32 v184, s25, v138
	v_fmac_f32_e32 v185, s25, v139
	v_readlane_b32 s25, v247, 46
	v_and_b32_e32 v124, s6, v52
	v_and_b32_e32 v125, s7, v52
	v_and_b32_e32 v126, s8, v52
	v_lshrrev_b32_e32 v127, 24, v52
	v_and_b32_e32 v128, s6, v53
	v_and_b32_e32 v129, s7, v53
	v_and_b32_e32 v130, s8, v53
	v_lshrrev_b32_e32 v131, 24, v53
	v_fmac_f32_e32 v178, s25, v124
	v_fmac_f32_e32 v179, s25, v125
	v_fmac_f32_e32 v180, s25, v126
	v_fmac_f32_e32 v181, s25, v127
	v_fmac_f32_e32 v182, s25, v128
	v_fmac_f32_e32 v183, s25, v129
	v_fmac_f32_e32 v184, s25, v130
	v_fmac_f32_e32 v185, s25, v131
	v_readlane_b32 s25, v247, 47
	v_and_b32_e32 v132, s6, v54
	v_and_b32_e32 v133, s7, v54
	v_and_b32_e32 v134, s8, v54
	v_lshrrev_b32_e32 v135, 24, v54
	v_and_b32_e32 v136, s6, v55
	v_and_b32_e32 v137, s7, v55
	v_and_b32_e32 v138, s8, v55
	v_lshrrev_b32_e32 v139, 24, v55
	v_fmac_f32_e32 v178, s25, v132
	v_fmac_f32_e32 v179, s25, v133
	v_fmac_f32_e32 v180, s25, v134
	v_fmac_f32_e32 v181, s25, v135
	v_fmac_f32_e32 v182, s25, v136
	v_fmac_f32_e32 v183, s25, v137
	v_fmac_f32_e32 v184, s25, v138
	v_fmac_f32_e32 v185, s25, v139
	s_waitcnt vmcnt(12)
	v_readlane_b32 s25, v247, 48
	v_and_b32_e32 v124, s6, v56
	v_and_b32_e32 v125, s7, v56
	v_and_b32_e32 v126, s8, v56
	v_lshrrev_b32_e32 v127, 24, v56
	v_and_b32_e32 v128, s6, v57
	v_and_b32_e32 v129, s7, v57
	v_and_b32_e32 v130, s8, v57
	v_lshrrev_b32_e32 v131, 24, v57
	v_fmac_f32_e32 v178, s25, v124
	v_fmac_f32_e32 v179, s25, v125
	v_fmac_f32_e32 v180, s25, v126
	v_fmac_f32_e32 v181, s25, v127
	v_fmac_f32_e32 v182, s25, v128
	v_fmac_f32_e32 v183, s25, v129
	v_fmac_f32_e32 v184, s25, v130
	v_fmac_f32_e32 v185, s25, v131
	v_readlane_b32 s25, v247, 49
	v_and_b32_e32 v132, s6, v58
	v_and_b32_e32 v133, s7, v58
	v_and_b32_e32 v134, s8, v58
	v_lshrrev_b32_e32 v135, 24, v58
	v_and_b32_e32 v136, s6, v59
	v_and_b32_e32 v137, s7, v59
	v_and_b32_e32 v138, s8, v59
	v_lshrrev_b32_e32 v139, 24, v59
	v_fmac_f32_e32 v178, s25, v132
	v_fmac_f32_e32 v179, s25, v133
	v_fmac_f32_e32 v180, s25, v134
	v_fmac_f32_e32 v181, s25, v135
	v_fmac_f32_e32 v182, s25, v136
	v_fmac_f32_e32 v183, s25, v137
	v_fmac_f32_e32 v184, s25, v138
	v_fmac_f32_e32 v185, s25, v139
	v_readlane_b32 s25, v247, 50
	v_and_b32_e32 v124, s6, v60
	v_and_b32_e32 v125, s7, v60
	v_and_b32_e32 v126, s8, v60
	v_lshrrev_b32_e32 v127, 24, v60
	v_and_b32_e32 v128, s6, v61
	v_and_b32_e32 v129, s7, v61
	v_and_b32_e32 v130, s8, v61
	v_lshrrev_b32_e32 v131, 24, v61
	v_fmac_f32_e32 v178, s25, v124
	v_fmac_f32_e32 v179, s25, v125
	v_fmac_f32_e32 v180, s25, v126
	v_fmac_f32_e32 v181, s25, v127
	v_fmac_f32_e32 v182, s25, v128
	v_fmac_f32_e32 v183, s25, v129
	v_fmac_f32_e32 v184, s25, v130
	v_fmac_f32_e32 v185, s25, v131
	v_readlane_b32 s25, v247, 51
	v_and_b32_e32 v132, s6, v62
	v_and_b32_e32 v133, s7, v62
	v_and_b32_e32 v134, s8, v62
	v_lshrrev_b32_e32 v135, 24, v62
	v_and_b32_e32 v136, s6, v63
	v_and_b32_e32 v137, s7, v63
	v_and_b32_e32 v138, s8, v63
	v_lshrrev_b32_e32 v139, 24, v63
	v_fmac_f32_e32 v178, s25, v132
	v_fmac_f32_e32 v179, s25, v133
	v_fmac_f32_e32 v180, s25, v134
	v_fmac_f32_e32 v181, s25, v135
	v_fmac_f32_e32 v182, s25, v136
	v_fmac_f32_e32 v183, s25, v137
	v_fmac_f32_e32 v184, s25, v138
	v_fmac_f32_e32 v185, s25, v139
	s_waitcnt vmcnt(8)
	v_readlane_b32 s25, v247, 52
	v_and_b32_e32 v124, s6, v64
	v_and_b32_e32 v125, s7, v64
	v_and_b32_e32 v126, s8, v64
	v_lshrrev_b32_e32 v127, 24, v64
	v_and_b32_e32 v128, s6, v65
	v_and_b32_e32 v129, s7, v65
	v_and_b32_e32 v130, s8, v65
	v_lshrrev_b32_e32 v131, 24, v65
	v_fmac_f32_e32 v178, s25, v124
	v_fmac_f32_e32 v179, s25, v125
	v_fmac_f32_e32 v180, s25, v126
	v_fmac_f32_e32 v181, s25, v127
	v_fmac_f32_e32 v182, s25, v128
	v_fmac_f32_e32 v183, s25, v129
	v_fmac_f32_e32 v184, s25, v130
	v_fmac_f32_e32 v185, s25, v131
	v_readlane_b32 s25, v247, 53
	v_and_b32_e32 v132, s6, v66
	v_and_b32_e32 v133, s7, v66
	v_and_b32_e32 v134, s8, v66
	v_lshrrev_b32_e32 v135, 24, v66
	v_and_b32_e32 v136, s6, v67
	v_and_b32_e32 v137, s7, v67
	v_and_b32_e32 v138, s8, v67
	v_lshrrev_b32_e32 v139, 24, v67
	v_fmac_f32_e32 v178, s25, v132
	v_fmac_f32_e32 v179, s25, v133
	v_fmac_f32_e32 v180, s25, v134
	v_fmac_f32_e32 v181, s25, v135
	v_fmac_f32_e32 v182, s25, v136
	v_fmac_f32_e32 v183, s25, v137
	v_fmac_f32_e32 v184, s25, v138
	v_fmac_f32_e32 v185, s25, v139
	v_readlane_b32 s25, v247, 54
	v_and_b32_e32 v124, s6, v68
	v_and_b32_e32 v125, s7, v68
	v_and_b32_e32 v126, s8, v68
	v_lshrrev_b32_e32 v127, 24, v68
	v_and_b32_e32 v128, s6, v69
	v_and_b32_e32 v129, s7, v69
	v_and_b32_e32 v130, s8, v69
	v_lshrrev_b32_e32 v131, 24, v69
	v_fmac_f32_e32 v178, s25, v124
	v_fmac_f32_e32 v179, s25, v125
	v_fmac_f32_e32 v180, s25, v126
	v_fmac_f32_e32 v181, s25, v127
	v_fmac_f32_e32 v182, s25, v128
	v_fmac_f32_e32 v183, s25, v129
	v_fmac_f32_e32 v184, s25, v130
	v_fmac_f32_e32 v185, s25, v131
	v_readlane_b32 s25, v247, 55
	v_and_b32_e32 v132, s6, v70
	v_and_b32_e32 v133, s7, v70
	v_and_b32_e32 v134, s8, v70
	v_lshrrev_b32_e32 v135, 24, v70
	v_and_b32_e32 v136, s6, v71
	v_and_b32_e32 v137, s7, v71
	v_and_b32_e32 v138, s8, v71
	v_lshrrev_b32_e32 v139, 24, v71
	v_fmac_f32_e32 v178, s25, v132
	v_fmac_f32_e32 v179, s25, v133
	v_fmac_f32_e32 v180, s25, v134
	v_fmac_f32_e32 v181, s25, v135
	v_fmac_f32_e32 v182, s25, v136
	v_fmac_f32_e32 v183, s25, v137
	v_fmac_f32_e32 v184, s25, v138
	v_fmac_f32_e32 v185, s25, v139
	s_waitcnt vmcnt(4)
	v_readlane_b32 s25, v247, 56
	v_and_b32_e32 v124, s6, v72
	v_and_b32_e32 v125, s7, v72
	v_and_b32_e32 v126, s8, v72
	v_lshrrev_b32_e32 v127, 24, v72
	v_and_b32_e32 v128, s6, v73
	v_and_b32_e32 v129, s7, v73
	v_and_b32_e32 v130, s8, v73
	v_lshrrev_b32_e32 v131, 24, v73
	v_fmac_f32_e32 v178, s25, v124
	v_fmac_f32_e32 v179, s25, v125
	v_fmac_f32_e32 v180, s25, v126
	v_fmac_f32_e32 v181, s25, v127
	v_fmac_f32_e32 v182, s25, v128
	v_fmac_f32_e32 v183, s25, v129
	v_fmac_f32_e32 v184, s25, v130
	v_fmac_f32_e32 v185, s25, v131
	v_readlane_b32 s25, v247, 57
	v_and_b32_e32 v132, s6, v74
	v_and_b32_e32 v133, s7, v74
	v_and_b32_e32 v134, s8, v74
	v_lshrrev_b32_e32 v135, 24, v74
	v_and_b32_e32 v136, s6, v75
	v_and_b32_e32 v137, s7, v75
	v_and_b32_e32 v138, s8, v75
	v_lshrrev_b32_e32 v139, 24, v75
	v_fmac_f32_e32 v178, s25, v132
	v_fmac_f32_e32 v179, s25, v133
	v_fmac_f32_e32 v180, s25, v134
	v_fmac_f32_e32 v181, s25, v135
	v_fmac_f32_e32 v182, s25, v136
	v_fmac_f32_e32 v183, s25, v137
	v_fmac_f32_e32 v184, s25, v138
	v_fmac_f32_e32 v185, s25, v139
	v_readlane_b32 s25, v247, 58
	v_and_b32_e32 v124, s6, v76
	v_and_b32_e32 v125, s7, v76
	v_and_b32_e32 v126, s8, v76
	v_lshrrev_b32_e32 v127, 24, v76
	v_and_b32_e32 v128, s6, v77
	v_and_b32_e32 v129, s7, v77
	v_and_b32_e32 v130, s8, v77
	v_lshrrev_b32_e32 v131, 24, v77
	v_fmac_f32_e32 v178, s25, v124
	v_fmac_f32_e32 v179, s25, v125
	v_fmac_f32_e32 v180, s25, v126
	v_fmac_f32_e32 v181, s25, v127
	v_fmac_f32_e32 v182, s25, v128
	v_fmac_f32_e32 v183, s25, v129
	v_fmac_f32_e32 v184, s25, v130
	v_fmac_f32_e32 v185, s25, v131
	v_readlane_b32 s25, v247, 59
	v_and_b32_e32 v132, s6, v78
	v_and_b32_e32 v133, s7, v78
	v_and_b32_e32 v134, s8, v78
	v_lshrrev_b32_e32 v135, 24, v78
	v_and_b32_e32 v136, s6, v79
	v_and_b32_e32 v137, s7, v79
	v_and_b32_e32 v138, s8, v79
	v_lshrrev_b32_e32 v139, 24, v79
	v_fmac_f32_e32 v178, s25, v132
	v_fmac_f32_e32 v179, s25, v133
	v_fmac_f32_e32 v180, s25, v134
	v_fmac_f32_e32 v181, s25, v135
	v_fmac_f32_e32 v182, s25, v136
	v_fmac_f32_e32 v183, s25, v137
	v_fmac_f32_e32 v184, s25, v138
	v_fmac_f32_e32 v185, s25, v139
	s_waitcnt vmcnt(0)
	v_readlane_b32 s25, v247, 60
	v_and_b32_e32 v124, s6, v80
	v_and_b32_e32 v125, s7, v80
	v_and_b32_e32 v126, s8, v80
	v_lshrrev_b32_e32 v127, 24, v80
	v_and_b32_e32 v128, s6, v81
	v_and_b32_e32 v129, s7, v81
	v_and_b32_e32 v130, s8, v81
	v_lshrrev_b32_e32 v131, 24, v81
	v_fmac_f32_e32 v178, s25, v124
	v_fmac_f32_e32 v179, s25, v125
	v_fmac_f32_e32 v180, s25, v126
	v_fmac_f32_e32 v181, s25, v127
	v_fmac_f32_e32 v182, s25, v128
	v_fmac_f32_e32 v183, s25, v129
	v_fmac_f32_e32 v184, s25, v130
	v_fmac_f32_e32 v185, s25, v131
	v_readlane_b32 s25, v247, 61
	v_and_b32_e32 v132, s6, v82
	v_and_b32_e32 v133, s7, v82
	v_and_b32_e32 v134, s8, v82
	v_lshrrev_b32_e32 v135, 24, v82
	v_and_b32_e32 v136, s6, v83
	v_and_b32_e32 v137, s7, v83
	v_and_b32_e32 v138, s8, v83
	v_lshrrev_b32_e32 v139, 24, v83
	v_fmac_f32_e32 v178, s25, v132
	v_fmac_f32_e32 v179, s25, v133
	v_fmac_f32_e32 v180, s25, v134
	v_fmac_f32_e32 v181, s25, v135
	v_fmac_f32_e32 v182, s25, v136
	v_fmac_f32_e32 v183, s25, v137
	v_fmac_f32_e32 v184, s25, v138
	v_fmac_f32_e32 v185, s25, v139
	v_readlane_b32 s25, v247, 62
	v_and_b32_e32 v124, s6, v84
	v_and_b32_e32 v125, s7, v84
	v_and_b32_e32 v126, s8, v84
	v_lshrrev_b32_e32 v127, 24, v84
	v_and_b32_e32 v128, s6, v85
	v_and_b32_e32 v129, s7, v85
	v_and_b32_e32 v130, s8, v85
	v_lshrrev_b32_e32 v131, 24, v85
	v_fmac_f32_e32 v178, s25, v124
	v_fmac_f32_e32 v179, s25, v125
	v_fmac_f32_e32 v180, s25, v126
	v_fmac_f32_e32 v181, s25, v127
	v_fmac_f32_e32 v182, s25, v128
	v_fmac_f32_e32 v183, s25, v129
	v_fmac_f32_e32 v184, s25, v130
	v_fmac_f32_e32 v185, s25, v131
	v_readlane_b32 s25, v247, 63
	v_and_b32_e32 v132, s6, v86
	v_and_b32_e32 v133, s7, v86
	v_and_b32_e32 v134, s8, v86
	v_lshrrev_b32_e32 v135, 24, v86
	v_and_b32_e32 v136, s6, v87
	v_and_b32_e32 v137, s7, v87
	v_and_b32_e32 v138, s8, v87
	v_lshrrev_b32_e32 v139, 24, v87
	v_fmac_f32_e32 v178, s25, v132
	v_fmac_f32_e32 v179, s25, v133
	v_fmac_f32_e32 v180, s25, v134
	v_fmac_f32_e32 v181, s25, v135
	v_fmac_f32_e32 v182, s25, v136
	v_fmac_f32_e32 v183, s25, v137
	v_fmac_f32_e32 v184, s25, v138
	v_fmac_f32_e32 v185, s25, v139
	v_lshlrev_b32_e32 v132, 16, v242
	v_and_b32_e32 v133, 0xffff0000, v242
	v_lshlrev_b32_e32 v134, 16, v243
	v_and_b32_e32 v135, 0xffff0000, v243
	v_lshlrev_b32_e32 v136, 16, v244
	v_and_b32_e32 v137, 0xffff0000, v244
	v_lshlrev_b32_e32 v138, 16, v245
	v_and_b32_e32 v139, 0xffff0000, v245
	v_mul_f32_e32 v178, 0x58000000, v178
	v_mul_f32_e32 v179, 0x54000000, v179
	v_mul_f32_e32 v180, 0x50000000, v180
	v_mul_f32_e32 v181, 0x58000000, v181
	v_mul_f32_e32 v182, 0x58000000, v182
	v_mul_f32_e32 v183, 0x54000000, v183
	v_mul_f32_e32 v184, 0x50000000, v184
	v_mul_f32_e32 v185, 0x58000000, v185
	v_add_f32_e32 v178, v178, v248
	v_add_f32_e32 v179, v179, v248
	v_add_f32_e32 v180, v180, v248
	v_add_f32_e32 v181, v181, v248
	v_add_f32_e32 v182, v182, v248
	v_add_f32_e32 v183, v183, v248
	v_add_f32_e32 v184, v184, v248
	v_add_f32_e32 v185, v185, v248
	v_add_f32_e32 v124, v132, v178
	v_add_f32_e32 v125, v133, v179
	v_add_f32_e32 v126, v134, v180
	v_add_f32_e32 v127, v135, v181
	v_add_f32_e32 v128, v136, v182
	v_add_f32_e32 v129, v137, v183
	v_add_f32_e32 v130, v138, v184
	v_add_f32_e32 v131, v139, v185
	v_mul_f32_e32 v16, v124, v124
	v_fmac_f32_e32 v16, v125, v125
	v_fmac_f32_e32 v16, v126, v126
	v_fmac_f32_e32 v16, v127, v127
	v_fmac_f32_e32 v16, v128, v128
	v_fmac_f32_e32 v16, v129, v129
	v_fmac_f32_e32 v16, v130, v130
	v_fmac_f32_e32 v16, v131, v131
	s_nop 1
	v_add_f32_dpp v17, v16, v16 quad_perm:[1,0,3,2] row_mask:0xf bank_mask:0xf
	s_nop 1
	v_add_f32_dpp v16, v17, v17 quad_perm:[2,3,0,1] row_mask:0xf bank_mask:0xf
	s_nop 1
	v_add_f32_dpp v17, v16, v16 row_half_mirror row_mask:0xf bank_mask:0xf
	s_nop 1
	v_add_f32_dpp v16, v17, v17 row_ror:8 row_mask:0xf bank_mask:0xf
	v_mov_b32_e32 v17, v16
	s_nop 1
	v_permlane16_swap_b32_e32 v16, v17
	v_add_f32_e32 v16, v16, v17
	v_mov_b32_e32 v17, v16
	s_nop 1
	v_permlane32_swap_b32_e32 v16, v17
	v_add_f32_e32 v16, v16, v17
	global_store_dwordx4 v[20:21], v[124:127], off
	global_store_dwordx4 v[20:21], v[128:131], off offset:16
	s_lshl_b32 s30, s16, 7
	s_add_u32 s28, s62, s30
	s_addc_u32 s29, s63, 0
	v_lshlrev_b32_e32 v18, 1, v1
	s_mov_b64 exec, s[2:3]
	global_store_dword v18, v16, s[28:29]
	s_mov_b64 exec, -1
	s_waitcnt lgkmcnt(0)
	s_load_dwordx16 s[84:99], s[38:39], 0x40 glc
	s_lshl_b32 s30, s68, 12
	s_add_u32 s28, s26, s30
	s_addc_u32 s29, s27, 0
	global_load_dwordx2 v[24:25], v162, s[28:29]
	s_lshl_b32 s30, s69, 12
	s_add_u32 s28, s26, s30
	s_addc_u32 s29, s27, 0
	global_load_dwordx2 v[26:27], v162, s[28:29]
	s_lshl_b32 s30, s70, 12
	s_add_u32 s28, s26, s30
	s_addc_u32 s29, s27, 0
	global_load_dwordx2 v[28:29], v162, s[28:29]
	s_lshl_b32 s30, s71, 12
	s_add_u32 s28, s26, s30
	s_addc_u32 s29, s27, 0
	global_load_dwordx2 v[30:31], v162, s[28:29]
	s_lshl_b32 s30, s72, 12
	s_add_u32 s28, s26, s30
	s_addc_u32 s29, s27, 0
	global_load_dwordx2 v[32:33], v162, s[28:29]
	s_lshl_b32 s30, s73, 12
	s_add_u32 s28, s26, s30
	s_addc_u32 s29, s27, 0
	global_load_dwordx2 v[34:35], v162, s[28:29]
	s_lshl_b32 s30, s74, 12
	s_add_u32 s28, s26, s30
	s_addc_u32 s29, s27, 0
	global_load_dwordx2 v[36:37], v162, s[28:29]
	s_lshl_b32 s30, s75, 12
	s_add_u32 s28, s26, s30
	s_addc_u32 s29, s27, 0
	global_load_dwordx2 v[38:39], v162, s[28:29]
	s_lshl_b32 s30, s76, 12
	s_add_u32 s28, s26, s30
	s_addc_u32 s29, s27, 0
	global_load_dwordx2 v[40:41], v162, s[28:29]
	s_lshl_b32 s30, s77, 12
	s_add_u32 s28, s26, s30
	s_addc_u32 s29, s27, 0
	global_load_dwordx2 v[42:43], v162, s[28:29]
	s_lshl_b32 s30, s78, 12
	s_add_u32 s28, s26, s30
	s_addc_u32 s29, s27, 0
	global_load_dwordx2 v[44:45], v162, s[28:29]
	s_lshl_b32 s30, s79, 12
	s_add_u32 s28, s26, s30
	s_addc_u32 s29, s27, 0
	global_load_dwordx2 v[46:47], v162, s[28:29]
	s_lshl_b32 s30, s80, 12
	s_add_u32 s28, s26, s30
	s_addc_u32 s29, s27, 0
	global_load_dwordx2 v[48:49], v162, s[28:29]
	s_lshl_b32 s30, s81, 12
	s_add_u32 s28, s26, s30
	s_addc_u32 s29, s27, 0
	global_load_dwordx2 v[50:51], v162, s[28:29]
	s_lshl_b32 s30, s82, 12
	s_add_u32 s28, s26, s30
	s_addc_u32 s29, s27, 0
	global_load_dwordx2 v[52:53], v162, s[28:29]
	s_lshl_b32 s30, s83, 12
	s_add_u32 s28, s26, s30
	s_addc_u32 s29, s27, 0
	global_load_dwordx2 v[54:55], v162, s[28:29]
	s_waitcnt lgkmcnt(0)
	s_load_dwordx16 s[68:83], s[38:39], 0x80 glc
	s_lshl_b32 s30, s84, 12
	s_add_u32 s28, s26, s30
	s_addc_u32 s29, s27, 0
	global_load_dwordx2 v[56:57], v162, s[28:29]
	s_lshl_b32 s30, s85, 12
	s_add_u32 s28, s26, s30
	s_addc_u32 s29, s27, 0
	global_load_dwordx2 v[58:59], v162, s[28:29]
	s_lshl_b32 s30, s86, 12
	s_add_u32 s28, s26, s30
	s_addc_u32 s29, s27, 0
	global_load_dwordx2 v[60:61], v162, s[28:29]
	s_lshl_b32 s30, s87, 12
	s_add_u32 s28, s26, s30
	s_addc_u32 s29, s27, 0
	global_load_dwordx2 v[62:63], v162, s[28:29]
	s_lshl_b32 s30, s88, 12
	s_add_u32 s28, s26, s30
	s_addc_u32 s29, s27, 0
	global_load_dwordx2 v[64:65], v162, s[28:29]
	s_lshl_b32 s30, s89, 12
	s_add_u32 s28, s26, s30
	s_addc_u32 s29, s27, 0
	global_load_dwordx2 v[66:67], v162, s[28:29]
	s_lshl_b32 s30, s90, 12
	s_add_u32 s28, s26, s30
	s_addc_u32 s29, s27, 0
	global_load_dwordx2 v[68:69], v162, s[28:29]
	s_lshl_b32 s30, s91, 12
	s_add_u32 s28, s26, s30
	s_addc_u32 s29, s27, 0
	global_load_dwordx2 v[70:71], v162, s[28:29]
	s_lshl_b32 s30, s92, 12
	s_add_u32 s28, s26, s30
	s_addc_u32 s29, s27, 0
	global_load_dwordx2 v[72:73], v162, s[28:29]
	s_lshl_b32 s30, s93, 12
	s_add_u32 s28, s26, s30
	s_addc_u32 s29, s27, 0
	global_load_dwordx2 v[74:75], v162, s[28:29]
	s_lshl_b32 s30, s94, 12
	s_add_u32 s28, s26, s30
	s_addc_u32 s29, s27, 0
	global_load_dwordx2 v[76:77], v162, s[28:29]
	s_lshl_b32 s30, s95, 12
	s_add_u32 s28, s26, s30
	s_addc_u32 s29, s27, 0
	global_load_dwordx2 v[78:79], v162, s[28:29]
	s_lshl_b32 s30, s96, 12
	s_add_u32 s28, s26, s30
	s_addc_u32 s29, s27, 0
	global_load_dwordx2 v[80:81], v162, s[28:29]
	s_lshl_b32 s30, s97, 12
	s_add_u32 s28, s26, s30
	s_addc_u32 s29, s27, 0
	global_load_dwordx2 v[82:83], v162, s[28:29]
	s_lshl_b32 s30, s98, 12
	s_add_u32 s28, s26, s30
	s_addc_u32 s29, s27, 0
	global_load_dwordx2 v[84:85], v162, s[28:29]
	s_lshl_b32 s30, s99, 12
	s_add_u32 s28, s26, s30
	s_addc_u32 s29, s27, 0
	global_load_dwordx2 v[86:87], v162, s[28:29]
	s_add_i32 s16, s16, 1
	s_cmp_lt_i32 s16, s17
	s_cbranch_scc1 .Lpb_tok
	s_waitcnt vmcnt(0)
	s_waitcnt vmcnt(0)
	v_cmp_eq_u32_e32 vcc, 0, v0
	s_waitcnt vmcnt(0) lgkmcnt(0)
	s_barrier
	s_and_saveexec_b64 s[2:3], vcc
	s_cbranch_execz .Lgbc_1444
	v_readlane_b32 s4, v237, 5
	s_waitcnt vmcnt(0) expcnt(0) lgkmcnt(0)
	s_nop 0
	v_mov_b32_e32 v1, s4
	ds_read_b32 v3, v1
	ds_read_b32 v1, v1 offset:4
	s_waitcnt lgkmcnt(1)
	v_cmp_ne_u32_e32 vcc, 0, v3
	s_branch .Lgbc_1412
	v_readlane_b32 s4, v237, 2
	v_readlane_b32 s5, v237, 3
	s_load_dwordx2 s[8:9], s[6:7], 0x4
	s_lshl_b64 s[4:5], s[4:5], 2
	v_readlane_b32 s6, v237, 0
	s_add_u32 s4, s6, s4
	v_readlane_b32 s6, v237, 1
	s_addc_u32 s5, s6, s5
	s_add_u32 s6, s4, 0x1000
	s_addc_u32 s7, s5, 0
	s_waitcnt lgkmcnt(0)
	s_mul_i32 s20, s8, s38
	s_add_u32 s8, s4, 0x1100
	s_mul_i32 s20, s20, s9
	s_addc_u32 s9, s5, 0
	s_add_u32 s10, s4, 0x1200
	s_addc_u32 s11, s5, 0
	s_add_u32 s12, s4, 0x1300
	s_addc_u32 s13, s5, 0
	s_mov_b32 s21, 1
	v_mov_b32_e32 v17, 0
	s_branch .Lgbc_1400
